# phase F layer 0: 8 row loads issued together + latent rows use ds_read_b128 instead of flat loads (per-step vmcnt(0) gone)
# baseline (speedup 1.0000x reference)
.LBB0_1365:
	s_cmpk_lt_i32 s0, 0x4000
	s_cbranch_scc1 .Lf_lat_L0
	s_cmp_lg_u32 s1, -1
	s_cselect_b32 s52, s1, 0
	s_cselect_b32 s53, s43, 0
	s_cmp_lg_u32 s45, -1
	s_cselect_b32 s61, s45, 0
	s_cselect_b32 s62, s43, 0
	s_cmpk_lt_i32 s0, 0x4000
	s_cselect_b32 s53, s53, s42
	s_cselect_b32 s52, s52, s33
	s_waitcnt vmcnt(7) lgkmcnt(7)
	v_lshl_add_u64 v[18:19], s[40:41], 0, v[110:111]
	v_lshl_add_u64 v[118:119], s[52:53], 0, v[112:113]
	s_mov_b32 s52, 0x1b41000
	v_add_co_u32_e32 v14, vcc, s52, v18
	ds_read_b128 v[86:89], v134
	ds_read_b128 v[82:85], v134 offset:8192
	ds_read_b128 v[78:81], v134 offset:16384
	ds_read_b128 v[74:77], v134 offset:24576
	ds_read_b128 v[70:73], v134 offset:32768
	ds_read_b128 v[66:69], v134 offset:40960
	ds_read_b128 v[62:65], v134 offset:49152
	ds_read_b128 v[58:61], v134 offset:57344
	ds_read_b128 v[54:57], v135
	ds_read_b128 v[50:53], v136
	ds_read_b128 v[46:49], v137
	ds_read_b128 v[42:45], v138
	ds_read_b128 v[38:41], v139
	ds_read_b128 v[34:37], v140
	s_waitcnt vmcnt(4) lgkmcnt(14)
	ds_read_b128 v[30:33], v141
	ds_read_b128 v[26:29], v142
	v_addc_co_u32_e32 v15, vcc, 0, v19, vcc
	global_load_dwordx4 v[2:5], v[14:15], off offset:3072
	global_load_dwordx4 v[6:9], v[14:15], off offset:2048
	s_mov_b32 s52, 0x1b40000
	v_add_co_u32_e32 v94, vcc, s52, v18
	s_cselect_b32 s63, s62, s55
	s_nop 0
	v_addc_co_u32_e32 v95, vcc, 0, v19, vcc
	global_load_dwordx4 v[10:13], v[14:15], off offset:1024
	s_nop 0
	global_load_dwordx4 v[14:17], v[14:15], off
	global_load_dwordx4 v[90:93], v[94:95], off offset:1024
	global_load_dwordx4 v[102:105], v[94:95], off
	global_load_dwordx4 v[18:21], v[94:95], off offset:3072
	global_load_dwordx4 v[22:25], v[94:95], off offset:2048
	s_cselect_b32 s62, s61, s54
	v_lshl_add_u64 v[116:117], s[62:63], 0, v[112:113]
	s_mov_b32 s52, 0x800000
	v_lshl_add_u64 v[120:121], s[40:41], 0, v[108:109]
	s_waitcnt vmcnt(7)
	v_mov_b32_e32 v221, v3
	s_waitcnt vmcnt(6)
	v_mov_b32_e32 v220, v7
	v_mov_b32_e32 v218, v6
	v_mov_b32_e32 v219, v2
	v_pk_mul_f32 v[220:221], v[220:221], v[220:221]
	s_nop 0
	v_pk_fma_f32 v[218:219], v[218:219], v[218:219], v[220:221]
	v_mov_b32_e32 v220, v8
	v_mov_b32_e32 v221, v4
	v_pk_fma_f32 v[218:219], v[220:221], v[220:221], v[218:219]
	v_mov_b32_e32 v220, v9
	v_mov_b32_e32 v221, v5
	v_pk_fma_f32 v[114:115], v[220:221], v[220:221], v[218:219]
	ds_read_b128 v[98:101], v133
	s_waitcnt vmcnt(5)
	v_mov_b32_e32 v225, v11
	s_waitcnt vmcnt(4)
	v_mov_b32_e32 v224, v15
	v_mov_b32_e32 v222, v14
	v_mov_b32_e32 v223, v10
	v_pk_mul_f32 v[224:225], v[224:225], v[224:225]
	s_waitcnt vmcnt(3)
	v_mul_f32_e32 v215, v91, v91
	v_pk_fma_f32 v[222:223], v[222:223], v[222:223], v[224:225]
	v_mov_b32_e32 v224, v16
	v_mov_b32_e32 v225, v12
	v_pk_fma_f32 v[222:223], v[224:225], v[224:225], v[222:223]
	v_mov_b32_e32 v224, v17
	v_mov_b32_e32 v225, v13
	v_pk_fma_f32 v[124:125], v[224:225], v[224:225], v[222:223]
	s_nop 0
	flat_load_dwordx4 v[94:97], v[118:119]
	flat_load_dwordx4 v[210:213], v[116:117]
	s_waitcnt vmcnt(0)
	v_mul_f32_e32 v216, v103, v103
	v_fmac_f32_e32 v215, v90, v90
	v_fmac_f32_e32 v216, v102, v102
	v_fmac_f32_e32 v215, v92, v92
	v_fmac_f32_e32 v216, v104, v104
	v_fmac_f32_e32 v215, v93, v93
	v_fmac_f32_e32 v216, v105, v105
	v_mul_f32_e32 v190, v19, v19
	v_mul_f32_e32 v214, v23, v23
	v_fmac_f32_e32 v214, v22, v22
	v_fmac_f32_e32 v190, v18, v18
	v_fmac_f32_e32 v214, v24, v24
	v_fmac_f32_e32 v190, v20, v20
	v_fmac_f32_e32 v214, v25, v25
	s_waitcnt lgkmcnt(0)
	v_mov_b32_e32 v122, v210
	v_add_f32_e32 v210, v216, v215
	v_fmac_f32_e32 v190, v21, v21
	v_add_f32_e32 v210, v210, v214
	v_add_f32_e32 v190, v210, v190
	v_add_f32_e32 v124, v190, v124
	v_add_f32_e32 v124, v124, v125
	v_add_f32_e32 v114, v124, v114
	v_add_f32_e32 v114, v114, v115
	ds_bpermute_b32 v115, v1, v114
	v_mov_b32_e32 v124, v102
	v_mov_b32_e32 v125, v104
	v_mov_b32_e32 v104, v103
	v_mov_b32_e32 v123, v212
	s_waitcnt lgkmcnt(0)
	v_add_f32_e32 v114, v114, v115
	ds_bpermute_b32 v115, v128, v114
	v_mov_b32_e32 v212, v211
	v_mov_b32_e32 v210, v98
	v_mov_b32_e32 v211, v100
	v_mov_b32_e32 v100, v99
	s_waitcnt lgkmcnt(0)
	v_add_f32_e32 v114, v114, v115
	ds_bpermute_b32 v115, v129, v114
	v_pk_add_f32 v[126:127], v[122:123], 1.0 op_sel_hi:[1,0]
	v_pk_add_f32 v[122:123], v[212:213], 1.0 op_sel_hi:[1,0]
	s_waitcnt lgkmcnt(0)
	v_add_f32_e32 v114, v114, v115
	ds_bpermute_b32 v115, v130, v114
	s_waitcnt lgkmcnt(0)
	v_add_f32_e32 v114, v114, v115
	ds_bpermute_b32 v115, v131, v114
	s_waitcnt lgkmcnt(0)
	v_add_f32_e32 v114, v114, v115
	ds_bpermute_b32 v115, v132, v114
	s_waitcnt lgkmcnt(0)
	v_add_f32_e32 v114, v114, v115
	v_fmamk_f32 v114, v114, 0x3a000000, v207
	v_cmp_gt_f32_e32 vcc, s52, v114
	v_mul_f32_e32 v115, 0x4b800000, v114
	s_mov_b32 s52, 0x2ec40000
	v_cndmask_b32_e32 v114, v114, v115, vcc
	v_rsq_f32_e32 v114, v114
	s_nop 0
	v_mul_f32_e32 v115, 0x45800000, v114
	v_cndmask_b32_e32 v114, v114, v115, vcc
	v_pk_mul_f32 v[124:125], v[124:125], v[114:115] op_sel_hi:[1,0]
	v_pk_mul_f32 v[102:103], v[104:105], v[114:115] op_sel_hi:[1,0]
	v_pk_mul_f32 v[124:125], v[210:211], v[124:125]
	v_mov_b32_e32 v211, v96
	v_pk_mul_f32 v[98:99], v[100:101], v[102:103]
	v_mov_b32_e32 v96, v95
	v_mov_b32_e32 v210, v94
	v_pk_fma_f32 v[96:97], v[122:123], v[98:99], v[96:97]
	v_pk_fma_f32 v[124:125], v[126:127], v[124:125], v[210:211]
	v_fma_f32 v33, v97, v33, 0
	v_fmac_f32_e32 v33, v125, v32
	v_and_b32_sdwa v98, v97, v208 dst_sel:DWORD dst_unused:UNUSED_PAD src0_sel:WORD_1 src1_sel:DWORD
	v_fmac_f32_e32 v33, v96, v31
	v_and_b32_sdwa v94, v125, v208 dst_sel:DWORD dst_unused:UNUSED_PAD src0_sel:WORD_1 src1_sel:DWORD
	v_and_b32_sdwa v99, v96, v208 dst_sel:DWORD dst_unused:UNUSED_PAD src0_sel:WORD_1 src1_sel:DWORD
	v_add3_u32 v98, v97, v98, s57
	v_fmac_f32_e32 v33, v124, v30
	v_fma_f32 v30, v97, v29, 0
	v_and_b32_sdwa v95, v124, v208 dst_sel:DWORD dst_unused:UNUSED_PAD src0_sel:WORD_1 src1_sel:DWORD
	v_add3_u32 v94, v125, v94, s57
	v_add3_u32 v99, v96, v99, s57
	v_and_b32_e32 v98, 0xffff0000, v98
	v_fma_f32 v89, v97, v89, 0
	v_fma_f32 v85, v97, v85, 0
	v_fma_f32 v81, v97, v81, 0
	v_fma_f32 v77, v97, v77, 0
	v_fma_f32 v73, v97, v73, 0
	v_fma_f32 v69, v97, v69, 0
	v_fma_f32 v65, v97, v65, 0
	v_fma_f32 v61, v97, v61, 0
	v_fma_f32 v57, v97, v57, 0
	v_fma_f32 v53, v97, v53, 0
	v_fma_f32 v49, v97, v49, 0
	v_fma_f32 v45, v97, v45, 0
	v_fma_f32 v41, v97, v41, 0
	v_fma_f32 v37, v97, v37, 0
	v_fmac_f32_e32 v30, v125, v28
	v_add3_u32 v95, v124, v95, s57
	v_and_b32_e32 v100, 0xffff0000, v99
	v_or_b32_sdwa v99, v98, v94 dst_sel:DWORD dst_unused:UNUSED_PAD src0_sel:DWORD src1_sel:WORD_1
	v_add_co_u32_e32 v94, vcc, s52, v120
	v_fmac_f32_e32 v89, v125, v88
	v_fmac_f32_e32 v85, v125, v84
	v_fmac_f32_e32 v81, v125, v80
	v_fmac_f32_e32 v77, v125, v76
	v_fmac_f32_e32 v73, v125, v72
	v_fmac_f32_e32 v69, v125, v68
	v_fmac_f32_e32 v65, v125, v64
	v_fmac_f32_e32 v61, v125, v60
	v_fmac_f32_e32 v57, v125, v56
	v_fmac_f32_e32 v53, v125, v52
	v_fmac_f32_e32 v49, v125, v48
	v_fmac_f32_e32 v45, v125, v44
	v_fmac_f32_e32 v41, v125, v40
	v_fmac_f32_e32 v37, v125, v36
	v_fmac_f32_e32 v30, v96, v27
	v_or_b32_sdwa v98, v100, v95 dst_sel:DWORD dst_unused:UNUSED_PAD src0_sel:DWORD src1_sel:WORD_1
	v_addc_co_u32_e32 v95, vcc, 0, v121, vcc
	v_fmac_f32_e32 v89, v96, v87
	v_fmac_f32_e32 v85, v96, v83
	v_fmac_f32_e32 v81, v96, v79
	v_fmac_f32_e32 v77, v96, v75
	v_fmac_f32_e32 v73, v96, v71
	v_fmac_f32_e32 v69, v96, v67
	v_fmac_f32_e32 v65, v96, v63
	v_fmac_f32_e32 v61, v96, v59
	v_fmac_f32_e32 v57, v96, v55
	v_fmac_f32_e32 v53, v96, v51
	v_fmac_f32_e32 v49, v96, v47
	v_fmac_f32_e32 v45, v96, v43
	v_fmac_f32_e32 v41, v96, v39
	v_fmac_f32_e32 v37, v96, v35
	v_fmac_f32_e32 v30, v124, v26
	global_store_dwordx2 v[94:95], v[98:99], off
	v_fmac_f32_e32 v89, v124, v86
	v_fmac_f32_e32 v85, v124, v82
	v_fmac_f32_e32 v81, v124, v78
	v_fmac_f32_e32 v77, v124, v74
	v_fmac_f32_e32 v73, v124, v70
	v_fmac_f32_e32 v69, v124, v66
	v_fmac_f32_e32 v65, v124, v62
	v_fmac_f32_e32 v61, v124, v58
	v_fmac_f32_e32 v57, v124, v54
	v_fmac_f32_e32 v53, v124, v50
	v_fmac_f32_e32 v49, v124, v46
	v_fmac_f32_e32 v45, v124, v42
	v_fmac_f32_e32 v41, v124, v38
	v_fmac_f32_e32 v37, v124, v34
	ds_read_b128 v[96:99], v143
	flat_load_dwordx4 v[100:103], v[118:119] offset:1024
	flat_load_dwordx4 v[120:123], v[116:117] offset:1024
	v_mov_b32_e32 v26, v90
	v_mov_b32_e32 v27, v92
	v_pk_mul_f32 v[26:27], v[26:27], v[114:115] op_sel_hi:[1,0]
	s_waitcnt lgkmcnt(0)
	v_mov_b32_e32 v28, v96
	v_mov_b32_e32 v29, v98
	v_pk_mul_f32 v[26:27], v[26:27], v[28:29]
	v_mov_b32_e32 v92, v91
	v_mov_b32_e32 v98, v97
	s_waitcnt vmcnt(0)
	v_mov_b32_e32 v34, v100
	v_mov_b32_e32 v28, v120
	v_mov_b32_e32 v29, v122
	v_pk_add_f32 v[28:29], v[28:29], 1.0 op_sel_hi:[1,0]
	v_mov_b32_e32 v35, v102
	v_pk_fma_f32 v[26:27], v[26:27], v[28:29], v[34:35]
	v_pk_mul_f32 v[28:29], v[92:93], v[114:115] op_sel_hi:[1,0]
	ds_read_b128 v[90:93], v134 offset:1024
	v_mov_b32_e32 v122, v121
	v_pk_mul_f32 v[28:29], v[28:29], v[98:99]
	v_pk_add_f32 v[34:35], v[122:123], 1.0 op_sel_hi:[1,0]
	v_mov_b32_e32 v102, v101
	v_pk_fma_f32 v[28:29], v[28:29], v[34:35], v[102:103]
	v_and_b32_sdwa v31, v27, v208 dst_sel:DWORD dst_unused:UNUSED_PAD src0_sel:WORD_1 src1_sel:DWORD
	s_waitcnt lgkmcnt(0)
	v_fmac_f32_e32 v89, v29, v93
	v_fmac_f32_e32 v89, v27, v92
	v_fmac_f32_e32 v89, v28, v91
	v_fmac_f32_e32 v89, v26, v90
	ds_read_b128 v[90:93], v134 offset:9216
	v_and_b32_sdwa v34, v29, v208 dst_sel:DWORD dst_unused:UNUSED_PAD src0_sel:WORD_1 src1_sel:DWORD
	v_and_b32_sdwa v35, v28, v208 dst_sel:DWORD dst_unused:UNUSED_PAD src0_sel:WORD_1 src1_sel:DWORD
	v_and_b32_sdwa v32, v26, v208 dst_sel:DWORD dst_unused:UNUSED_PAD src0_sel:WORD_1 src1_sel:DWORD
	v_add3_u32 v34, v29, v34, s57
	s_waitcnt lgkmcnt(0)
	v_fmac_f32_e32 v85, v29, v93
	v_fmac_f32_e32 v85, v27, v92
	v_fmac_f32_e32 v85, v28, v91
	v_fmac_f32_e32 v85, v26, v90
	ds_read_b128 v[90:93], v134 offset:17408
	v_add3_u32 v35, v28, v35, s57
	v_add3_u32 v32, v26, v32, s57
	v_add3_u32 v31, v27, v31, s57
	v_and_b32_e32 v34, 0xffff0000, v34
	s_waitcnt lgkmcnt(0)
	v_fmac_f32_e32 v81, v29, v93
	v_fmac_f32_e32 v81, v27, v92
	v_fmac_f32_e32 v81, v28, v91
	v_fmac_f32_e32 v81, v26, v90
	ds_read_b128 v[90:93], v134 offset:25600
	v_and_b32_e32 v36, 0xffff0000, v35
	v_or_b32_sdwa v35, v34, v31 dst_sel:DWORD dst_unused:UNUSED_PAD src0_sel:DWORD src1_sel:WORD_1
	v_or_b32_sdwa v34, v36, v32 dst_sel:DWORD dst_unused:UNUSED_PAD src0_sel:DWORD src1_sel:WORD_1
	global_store_dwordx2 v[94:95], v[34:35], off offset:512
	s_waitcnt lgkmcnt(0)
	v_fmac_f32_e32 v77, v29, v93
	v_fmac_f32_e32 v77, v27, v92
	v_fmac_f32_e32 v77, v28, v91
	v_fmac_f32_e32 v77, v26, v90
	ds_read_b128 v[90:93], v134 offset:33792
	s_waitcnt lgkmcnt(0)
	v_fmac_f32_e32 v73, v29, v93
	v_fmac_f32_e32 v73, v27, v92
	v_fmac_f32_e32 v73, v28, v91
	v_fmac_f32_e32 v73, v26, v90
	ds_read_b128 v[90:93], v134 offset:41984
	s_waitcnt lgkmcnt(0)
	v_fmac_f32_e32 v69, v29, v93
	v_fmac_f32_e32 v69, v27, v92
	v_fmac_f32_e32 v69, v28, v91
	v_fmac_f32_e32 v69, v26, v90
	ds_read_b128 v[90:93], v134 offset:50176
	s_waitcnt lgkmcnt(0)
	v_fmac_f32_e32 v65, v29, v93
	v_fmac_f32_e32 v65, v27, v92
	v_fmac_f32_e32 v65, v28, v91
	v_fmac_f32_e32 v65, v26, v90
	ds_read_b128 v[90:93], v134 offset:58368
	s_waitcnt lgkmcnt(0)
	v_fmac_f32_e32 v61, v29, v93
	v_fmac_f32_e32 v61, v27, v92
	v_fmac_f32_e32 v61, v28, v91
	v_fmac_f32_e32 v61, v26, v90
	ds_read_b128 v[90:93], v144
	s_waitcnt lgkmcnt(0)
	v_fmac_f32_e32 v57, v29, v93
	v_fmac_f32_e32 v57, v27, v92
	v_fmac_f32_e32 v57, v28, v91
	v_fmac_f32_e32 v57, v26, v90
	ds_read_b128 v[90:93], v145
	s_waitcnt lgkmcnt(0)
	v_fmac_f32_e32 v53, v29, v93
	v_fmac_f32_e32 v53, v27, v92
	v_fmac_f32_e32 v53, v28, v91
	v_fmac_f32_e32 v53, v26, v90
	ds_read_b128 v[90:93], v146
	s_waitcnt lgkmcnt(0)
	v_fmac_f32_e32 v49, v29, v93
	v_fmac_f32_e32 v49, v27, v92
	v_fmac_f32_e32 v49, v28, v91
	v_fmac_f32_e32 v49, v26, v90
	ds_read_b128 v[90:93], v147
	s_waitcnt lgkmcnt(0)
	v_fmac_f32_e32 v45, v29, v93
	v_fmac_f32_e32 v45, v27, v92
	v_fmac_f32_e32 v45, v28, v91
	v_fmac_f32_e32 v45, v26, v90
	ds_read_b128 v[90:93], v148
	s_waitcnt lgkmcnt(0)
	v_fmac_f32_e32 v41, v29, v93
	v_fmac_f32_e32 v41, v27, v92
	v_fmac_f32_e32 v41, v28, v91
	v_fmac_f32_e32 v41, v26, v90
	ds_read_b128 v[90:93], v149
	s_waitcnt lgkmcnt(0)
	v_fmac_f32_e32 v37, v29, v93
	v_fmac_f32_e32 v37, v27, v92
	v_fmac_f32_e32 v37, v28, v91
	v_fmac_f32_e32 v37, v26, v90
	ds_read_b128 v[90:93], v150
	s_waitcnt lgkmcnt(0)
	v_fmac_f32_e32 v33, v29, v93
	v_fmac_f32_e32 v33, v27, v92
	v_fmac_f32_e32 v33, v28, v91
	v_fmac_f32_e32 v33, v26, v90
	ds_read_b128 v[90:93], v151
	s_waitcnt lgkmcnt(0)
	v_fmac_f32_e32 v30, v29, v93
	v_fmac_f32_e32 v30, v27, v92
	v_fmac_f32_e32 v30, v28, v91
	v_fmac_f32_e32 v30, v26, v90
	ds_read_b128 v[90:93], v152
	flat_load_dwordx4 v[96:99], v[118:119] offset:2048
	flat_load_dwordx4 v[100:103], v[116:117] offset:2048
	v_mov_b32_e32 v27, v24
	v_mov_b32_e32 v24, v23
	v_mov_b32_e32 v26, v22
	s_waitcnt lgkmcnt(0)
	v_mov_b32_e32 v29, v92
	v_pk_mul_f32 v[22:23], v[24:25], v[114:115] op_sel_hi:[1,0]
	v_mov_b32_e32 v92, v91
	v_mov_b32_e32 v28, v90
	v_pk_mul_f32 v[22:23], v[22:23], v[92:93]
	ds_read_b128 v[90:93], v134 offset:2048
	v_pk_mul_f32 v[26:27], v[26:27], v[114:115] op_sel_hi:[1,0]
	s_waitcnt vmcnt(0)
	v_mov_b32_e32 v35, v98
	v_pk_mul_f32 v[26:27], v[26:27], v[28:29]
	v_mov_b32_e32 v29, v102
	v_mov_b32_e32 v102, v101
	v_mov_b32_e32 v28, v100
	v_pk_add_f32 v[24:25], v[102:103], 1.0 op_sel_hi:[1,0]
	v_mov_b32_e32 v98, v97
	v_pk_add_f32 v[28:29], v[28:29], 1.0 op_sel_hi:[1,0]
	v_mov_b32_e32 v34, v96
	v_pk_fma_f32 v[22:23], v[22:23], v[24:25], v[98:99]
	v_pk_fma_f32 v[26:27], v[26:27], v[28:29], v[34:35]
	s_waitcnt lgkmcnt(0)
	v_fmac_f32_e32 v89, v23, v93
	v_fmac_f32_e32 v89, v27, v92
	v_fmac_f32_e32 v89, v22, v91
	v_fmac_f32_e32 v89, v26, v90
	ds_read_b128 v[90:93], v134 offset:10240
	v_and_b32_sdwa v25, v26, v208 dst_sel:DWORD dst_unused:UNUSED_PAD src0_sel:WORD_1 src1_sel:DWORD
	v_add3_u32 v28, v26, v25, s57
	v_and_b32_sdwa v25, v23, v208 dst_sel:DWORD dst_unused:UNUSED_PAD src0_sel:WORD_1 src1_sel:DWORD
	v_and_b32_sdwa v29, v22, v208 dst_sel:DWORD dst_unused:UNUSED_PAD src0_sel:WORD_1 src1_sel:DWORD
	s_waitcnt lgkmcnt(0)
	v_fmac_f32_e32 v85, v23, v93
	v_fmac_f32_e32 v85, v27, v92
	v_fmac_f32_e32 v85, v22, v91
	v_fmac_f32_e32 v85, v26, v90
	ds_read_b128 v[90:93], v134 offset:18432
	v_and_b32_sdwa v24, v27, v208 dst_sel:DWORD dst_unused:UNUSED_PAD src0_sel:WORD_1 src1_sel:DWORD
	v_add3_u32 v25, v23, v25, s57
	v_add3_u32 v29, v22, v29, s57
	v_add3_u32 v24, v27, v24, s57
	s_waitcnt lgkmcnt(0)
	v_fmac_f32_e32 v81, v23, v93
	v_fmac_f32_e32 v81, v27, v92
	v_fmac_f32_e32 v81, v22, v91
	v_fmac_f32_e32 v81, v26, v90
	ds_read_b128 v[90:93], v134 offset:26624
	v_and_b32_e32 v25, 0xffff0000, v25
	v_and_b32_e32 v29, 0xffff0000, v29
	v_or_b32_sdwa v25, v25, v24 dst_sel:DWORD dst_unused:UNUSED_PAD src0_sel:DWORD src1_sel:WORD_1
	v_or_b32_sdwa v24, v29, v28 dst_sel:DWORD dst_unused:UNUSED_PAD src0_sel:DWORD src1_sel:WORD_1
	s_waitcnt lgkmcnt(0)
	v_fmac_f32_e32 v77, v23, v93
	v_fmac_f32_e32 v77, v27, v92
	v_fmac_f32_e32 v77, v22, v91
	v_fmac_f32_e32 v77, v26, v90
	ds_read_b128 v[90:93], v134 offset:34816
	global_store_dwordx2 v[94:95], v[24:25], off offset:1024
	s_waitcnt lgkmcnt(0)
	v_fmac_f32_e32 v73, v23, v93
	v_fmac_f32_e32 v73, v27, v92
	v_fmac_f32_e32 v73, v22, v91
	v_fmac_f32_e32 v73, v26, v90
	ds_read_b128 v[90:93], v134 offset:43008
	s_waitcnt lgkmcnt(0)
	v_fmac_f32_e32 v69, v23, v93
	v_fmac_f32_e32 v69, v27, v92
	v_fmac_f32_e32 v69, v22, v91
	v_fmac_f32_e32 v69, v26, v90
	ds_read_b128 v[90:93], v134 offset:51200
	s_waitcnt lgkmcnt(0)
	v_fmac_f32_e32 v65, v23, v93
	v_fmac_f32_e32 v65, v27, v92
	v_fmac_f32_e32 v65, v22, v91
	v_fmac_f32_e32 v65, v26, v90
	ds_read_b128 v[90:93], v134 offset:59392
	s_waitcnt lgkmcnt(0)
	v_fmac_f32_e32 v61, v23, v93
	v_fmac_f32_e32 v61, v27, v92
	v_fmac_f32_e32 v61, v22, v91
	v_fmac_f32_e32 v61, v26, v90
	ds_read_b128 v[90:93], v153
	s_waitcnt lgkmcnt(0)
	v_fmac_f32_e32 v57, v23, v93
	v_fmac_f32_e32 v57, v27, v92
	v_fmac_f32_e32 v57, v22, v91
	v_fmac_f32_e32 v57, v26, v90
	ds_read_b128 v[90:93], v154
	s_waitcnt lgkmcnt(0)
	v_fmac_f32_e32 v53, v23, v93
	v_fmac_f32_e32 v53, v27, v92
	v_fmac_f32_e32 v53, v22, v91
	v_fmac_f32_e32 v53, v26, v90
	ds_read_b128 v[90:93], v155
	s_waitcnt lgkmcnt(0)
	v_fmac_f32_e32 v49, v23, v93
	v_fmac_f32_e32 v49, v27, v92
	v_fmac_f32_e32 v49, v22, v91
	v_fmac_f32_e32 v49, v26, v90
	ds_read_b128 v[90:93], v156
	s_waitcnt lgkmcnt(0)
	v_fmac_f32_e32 v45, v23, v93
	v_fmac_f32_e32 v45, v27, v92
	v_fmac_f32_e32 v45, v22, v91
	v_fmac_f32_e32 v45, v26, v90
	ds_read_b128 v[90:93], v157
	s_waitcnt lgkmcnt(0)
	v_fmac_f32_e32 v41, v23, v93
	v_fmac_f32_e32 v41, v27, v92
	v_fmac_f32_e32 v41, v22, v91
	v_fmac_f32_e32 v41, v26, v90
	ds_read_b128 v[90:93], v158
	s_waitcnt lgkmcnt(0)
	v_fmac_f32_e32 v37, v23, v93
	v_fmac_f32_e32 v37, v27, v92
	v_fmac_f32_e32 v37, v22, v91
	v_fmac_f32_e32 v37, v26, v90
	ds_read_b128 v[90:93], v159
	s_waitcnt lgkmcnt(0)
	v_fmac_f32_e32 v33, v23, v93
	v_fmac_f32_e32 v33, v27, v92
	v_fmac_f32_e32 v33, v22, v91
	v_fmac_f32_e32 v33, v26, v90
	ds_read_b128 v[90:93], v160
	s_waitcnt lgkmcnt(0)
	v_fmac_f32_e32 v30, v23, v93
	v_fmac_f32_e32 v30, v27, v92
	v_fmac_f32_e32 v30, v22, v91
	v_fmac_f32_e32 v30, v26, v90
	ds_read_b128 v[24:27], v161
	flat_load_dwordx4 v[90:93], v[118:119] offset:3072
	flat_load_dwordx4 v[96:99], v[116:117] offset:3072
	v_mov_b32_e32 v22, v18
	v_mov_b32_e32 v23, v20
	v_pk_mul_f32 v[22:23], v[22:23], v[114:115] op_sel_hi:[1,0]
	s_waitcnt lgkmcnt(0)
	v_mov_b32_e32 v28, v24
	v_mov_b32_e32 v29, v26
	v_pk_mul_f32 v[22:23], v[22:23], v[28:29]
	v_mov_b32_e32 v20, v19
	v_pk_mul_f32 v[18:19], v[20:21], v[114:115] op_sel_hi:[1,0]
	v_mov_b32_e32 v26, v25
	v_pk_mul_f32 v[18:19], v[18:19], v[26:27]
	s_waitcnt vmcnt(0)
	v_mov_b32_e32 v34, v90
	v_mov_b32_e32 v28, v96
	v_mov_b32_e32 v29, v98
	v_pk_add_f32 v[28:29], v[28:29], 1.0 op_sel_hi:[1,0]
	v_mov_b32_e32 v35, v92
	v_mov_b32_e32 v98, v97
	v_pk_fma_f32 v[22:23], v[22:23], v[28:29], v[34:35]
	v_pk_add_f32 v[20:21], v[98:99], 1.0 op_sel_hi:[1,0]
	v_mov_b32_e32 v92, v91
	v_pk_fma_f32 v[18:19], v[18:19], v[20:21], v[92:93]
	v_and_b32_sdwa v21, v22, v208 dst_sel:DWORD dst_unused:UNUSED_PAD src0_sel:WORD_1 src1_sel:DWORD
	v_add3_u32 v24, v22, v21, s57
	v_and_b32_sdwa v21, v19, v208 dst_sel:DWORD dst_unused:UNUSED_PAD src0_sel:WORD_1 src1_sel:DWORD
	v_and_b32_sdwa v25, v18, v208 dst_sel:DWORD dst_unused:UNUSED_PAD src0_sel:WORD_1 src1_sel:DWORD
	v_and_b32_sdwa v20, v23, v208 dst_sel:DWORD dst_unused:UNUSED_PAD src0_sel:WORD_1 src1_sel:DWORD
	v_add3_u32 v21, v19, v21, s57
	v_add3_u32 v25, v18, v25, s57
	v_add3_u32 v20, v23, v20, s57
	v_and_b32_e32 v21, 0xffff0000, v21
	v_and_b32_e32 v25, 0xffff0000, v25
	v_or_b32_sdwa v21, v21, v20 dst_sel:DWORD dst_unused:UNUSED_PAD src0_sel:DWORD src1_sel:WORD_1
	v_or_b32_sdwa v20, v25, v24 dst_sel:DWORD dst_unused:UNUSED_PAD src0_sel:DWORD src1_sel:WORD_1
	ds_read_b128 v[24:27], v134 offset:3072
	global_store_dwordx2 v[94:95], v[20:21], off offset:1536
	s_waitcnt lgkmcnt(0)
	v_fmac_f32_e32 v89, v19, v27
	v_fmac_f32_e32 v89, v23, v26
	v_fmac_f32_e32 v89, v18, v25
	v_fmac_f32_e32 v89, v22, v24
	ds_read_b128 v[24:27], v134 offset:11264
	s_waitcnt lgkmcnt(0)
	v_fmac_f32_e32 v85, v19, v27
	v_fmac_f32_e32 v85, v23, v26
	v_fmac_f32_e32 v85, v18, v25
	v_fmac_f32_e32 v85, v22, v24
	ds_read_b128 v[24:27], v134 offset:19456
	s_waitcnt lgkmcnt(0)
	v_fmac_f32_e32 v81, v19, v27
	v_fmac_f32_e32 v81, v23, v26
	v_fmac_f32_e32 v81, v18, v25
	v_fmac_f32_e32 v81, v22, v24
	ds_read_b128 v[24:27], v134 offset:27648
	s_waitcnt lgkmcnt(0)
	v_fmac_f32_e32 v77, v19, v27
	v_fmac_f32_e32 v77, v23, v26
	v_fmac_f32_e32 v77, v18, v25
	v_fmac_f32_e32 v77, v22, v24
	ds_read_b128 v[24:27], v134 offset:35840
	s_waitcnt lgkmcnt(0)
	v_fmac_f32_e32 v73, v19, v27
	v_fmac_f32_e32 v73, v23, v26
	v_fmac_f32_e32 v73, v18, v25
	v_fmac_f32_e32 v73, v22, v24
	ds_read_b128 v[24:27], v134 offset:44032
	s_waitcnt lgkmcnt(0)
	v_fmac_f32_e32 v69, v19, v27
	v_fmac_f32_e32 v69, v23, v26
	v_fmac_f32_e32 v69, v18, v25
	v_fmac_f32_e32 v69, v22, v24
	ds_read_b128 v[24:27], v134 offset:52224
	s_waitcnt lgkmcnt(0)
	v_fmac_f32_e32 v65, v19, v27
	v_fmac_f32_e32 v65, v23, v26
	v_fmac_f32_e32 v65, v18, v25
	v_fmac_f32_e32 v65, v22, v24
	ds_read_b128 v[24:27], v134 offset:60416
	s_waitcnt lgkmcnt(0)
	v_fmac_f32_e32 v61, v19, v27
	v_fmac_f32_e32 v61, v23, v26
	v_fmac_f32_e32 v61, v18, v25
	v_fmac_f32_e32 v61, v22, v24
	ds_read_b128 v[24:27], v162
	s_waitcnt lgkmcnt(0)
	v_fmac_f32_e32 v57, v19, v27
	v_fmac_f32_e32 v57, v23, v26
	v_fmac_f32_e32 v57, v18, v25
	v_fmac_f32_e32 v57, v22, v24
	ds_read_b128 v[24:27], v163
	s_waitcnt lgkmcnt(0)
	v_fmac_f32_e32 v53, v19, v27
	v_fmac_f32_e32 v53, v23, v26
	v_fmac_f32_e32 v53, v18, v25
	v_fmac_f32_e32 v53, v22, v24
	ds_read_b128 v[24:27], v164
	s_waitcnt lgkmcnt(0)
	v_fmac_f32_e32 v49, v19, v27
	v_fmac_f32_e32 v49, v23, v26
	v_fmac_f32_e32 v49, v18, v25
	v_fmac_f32_e32 v49, v22, v24
	ds_read_b128 v[24:27], v165
	s_waitcnt lgkmcnt(0)
	v_fmac_f32_e32 v45, v19, v27
	v_fmac_f32_e32 v45, v23, v26
	v_fmac_f32_e32 v45, v18, v25
	v_fmac_f32_e32 v45, v22, v24
	ds_read_b128 v[24:27], v166
	s_waitcnt lgkmcnt(0)
	v_fmac_f32_e32 v41, v19, v27
	v_fmac_f32_e32 v41, v23, v26
	v_fmac_f32_e32 v41, v18, v25
	v_fmac_f32_e32 v41, v22, v24
	ds_read_b128 v[24:27], v167
	s_waitcnt lgkmcnt(0)
	v_fmac_f32_e32 v37, v19, v27
	v_fmac_f32_e32 v37, v23, v26
	v_fmac_f32_e32 v37, v18, v25
	v_fmac_f32_e32 v37, v22, v24
	ds_read_b128 v[24:27], v168
	s_waitcnt lgkmcnt(0)
	v_fmac_f32_e32 v33, v19, v27
	v_fmac_f32_e32 v33, v23, v26
	v_fmac_f32_e32 v33, v18, v25
	v_fmac_f32_e32 v33, v22, v24
	ds_read_b128 v[24:27], v169
	s_waitcnt lgkmcnt(0)
	v_fmac_f32_e32 v30, v19, v27
	v_fmac_f32_e32 v30, v23, v26
	v_fmac_f32_e32 v30, v18, v25
	v_fmac_f32_e32 v30, v22, v24
	v_add_co_u32_e32 v18, vcc, s56, v118
	ds_read_b128 v[24:27], v170
	s_nop 0
	v_addc_co_u32_e32 v19, vcc, 0, v119, vcc
	v_add_co_u32_e32 v20, vcc, s56, v116
	flat_load_dwordx4 v[90:93], v[18:19]
	s_nop 0
	v_addc_co_u32_e32 v21, vcc, 0, v117, vcc
	flat_load_dwordx4 v[96:99], v[20:21]
	v_mov_b32_e32 v22, v14
	v_mov_b32_e32 v23, v16
	v_pk_mul_f32 v[22:23], v[22:23], v[114:115] op_sel_hi:[1,0]
	s_waitcnt lgkmcnt(0)
	v_mov_b32_e32 v28, v24
	v_mov_b32_e32 v29, v26
	v_pk_mul_f32 v[22:23], v[22:23], v[28:29]
	v_mov_b32_e32 v16, v15
	v_pk_mul_f32 v[14:15], v[16:17], v[114:115] op_sel_hi:[1,0]
	v_mov_b32_e32 v26, v25
	v_pk_mul_f32 v[14:15], v[14:15], v[26:27]
	s_waitcnt vmcnt(0)
	v_mov_b32_e32 v34, v90
	v_mov_b32_e32 v35, v92
	v_mov_b32_e32 v92, v91
	v_mov_b32_e32 v28, v96
	v_mov_b32_e32 v29, v98
	v_pk_add_f32 v[28:29], v[28:29], 1.0 op_sel_hi:[1,0]
	v_mov_b32_e32 v98, v97
	v_pk_fma_f32 v[22:23], v[22:23], v[28:29], v[34:35]
	v_pk_add_f32 v[16:17], v[98:99], 1.0 op_sel_hi:[1,0]
	s_nop 0
	v_pk_fma_f32 v[14:15], v[14:15], v[16:17], v[92:93]
	v_and_b32_sdwa v17, v22, v208 dst_sel:DWORD dst_unused:UNUSED_PAD src0_sel:WORD_1 src1_sel:DWORD
	v_add3_u32 v24, v22, v17, s57
	v_and_b32_sdwa v17, v15, v208 dst_sel:DWORD dst_unused:UNUSED_PAD src0_sel:WORD_1 src1_sel:DWORD
	v_and_b32_sdwa v25, v14, v208 dst_sel:DWORD dst_unused:UNUSED_PAD src0_sel:WORD_1 src1_sel:DWORD
	v_and_b32_sdwa v16, v23, v208 dst_sel:DWORD dst_unused:UNUSED_PAD src0_sel:WORD_1 src1_sel:DWORD
	v_add3_u32 v17, v15, v17, s57
	v_add3_u32 v25, v14, v25, s57
	v_add3_u32 v16, v23, v16, s57
	v_and_b32_e32 v17, 0xffff0000, v17
	v_and_b32_e32 v25, 0xffff0000, v25
	v_or_b32_sdwa v17, v17, v16 dst_sel:DWORD dst_unused:UNUSED_PAD src0_sel:DWORD src1_sel:WORD_1
	v_or_b32_sdwa v16, v25, v24 dst_sel:DWORD dst_unused:UNUSED_PAD src0_sel:DWORD src1_sel:WORD_1
	ds_read_b128 v[24:27], v134 offset:4096
	global_store_dwordx2 v[94:95], v[16:17], off offset:2048
	s_waitcnt lgkmcnt(0)
	v_fmac_f32_e32 v89, v15, v27
	v_fmac_f32_e32 v89, v23, v26
	v_fmac_f32_e32 v89, v14, v25
	v_fmac_f32_e32 v89, v22, v24
	ds_read_b128 v[24:27], v134 offset:12288
	s_waitcnt lgkmcnt(0)
	v_fmac_f32_e32 v85, v15, v27
	v_fmac_f32_e32 v85, v23, v26
	v_fmac_f32_e32 v85, v14, v25
	v_fmac_f32_e32 v85, v22, v24
	ds_read_b128 v[24:27], v134 offset:20480
	s_waitcnt lgkmcnt(0)
	v_fmac_f32_e32 v81, v15, v27
	v_fmac_f32_e32 v81, v23, v26
	v_fmac_f32_e32 v81, v14, v25
	v_fmac_f32_e32 v81, v22, v24
	ds_read_b128 v[24:27], v134 offset:28672
	s_waitcnt lgkmcnt(0)
	v_fmac_f32_e32 v77, v15, v27
	v_fmac_f32_e32 v77, v23, v26
	v_fmac_f32_e32 v77, v14, v25
	v_fmac_f32_e32 v77, v22, v24
	ds_read_b128 v[24:27], v134 offset:36864
	s_waitcnt lgkmcnt(0)
	v_fmac_f32_e32 v73, v15, v27
	v_fmac_f32_e32 v73, v23, v26
	v_fmac_f32_e32 v73, v14, v25
	v_fmac_f32_e32 v73, v22, v24
	ds_read_b128 v[24:27], v134 offset:45056
	s_waitcnt lgkmcnt(0)
	v_fmac_f32_e32 v69, v15, v27
	v_fmac_f32_e32 v69, v23, v26
	v_fmac_f32_e32 v69, v14, v25
	v_fmac_f32_e32 v69, v22, v24
	ds_read_b128 v[24:27], v134 offset:53248
	s_waitcnt lgkmcnt(0)
	v_fmac_f32_e32 v65, v15, v27
	v_fmac_f32_e32 v65, v23, v26
	v_fmac_f32_e32 v65, v14, v25
	v_fmac_f32_e32 v65, v22, v24
	ds_read_b128 v[24:27], v134 offset:61440
	s_waitcnt lgkmcnt(0)
	v_fmac_f32_e32 v61, v15, v27
	v_fmac_f32_e32 v61, v23, v26
	v_fmac_f32_e32 v61, v14, v25
	v_fmac_f32_e32 v61, v22, v24
	ds_read_b128 v[24:27], v171
	s_waitcnt lgkmcnt(0)
	v_fmac_f32_e32 v57, v15, v27
	v_fmac_f32_e32 v57, v23, v26
	v_fmac_f32_e32 v57, v14, v25
	v_fmac_f32_e32 v57, v22, v24
	ds_read_b128 v[24:27], v172
	s_waitcnt lgkmcnt(0)
	v_fmac_f32_e32 v53, v15, v27
	v_fmac_f32_e32 v53, v23, v26
	v_fmac_f32_e32 v53, v14, v25
	v_fmac_f32_e32 v53, v22, v24
	ds_read_b128 v[24:27], v173
	s_waitcnt lgkmcnt(0)
	v_fmac_f32_e32 v49, v15, v27
	v_fmac_f32_e32 v49, v23, v26
	v_fmac_f32_e32 v49, v14, v25
	v_fmac_f32_e32 v49, v22, v24
	ds_read_b128 v[24:27], v174
	s_waitcnt lgkmcnt(0)
	v_fmac_f32_e32 v45, v15, v27
	v_fmac_f32_e32 v45, v23, v26
	v_fmac_f32_e32 v45, v14, v25
	v_fmac_f32_e32 v45, v22, v24
	ds_read_b128 v[24:27], v175
	s_waitcnt lgkmcnt(0)
	v_fmac_f32_e32 v41, v15, v27
	v_fmac_f32_e32 v41, v23, v26
	v_fmac_f32_e32 v41, v14, v25
	v_fmac_f32_e32 v41, v22, v24
	ds_read_b128 v[24:27], v176
	s_waitcnt lgkmcnt(0)
	v_fmac_f32_e32 v37, v15, v27
	v_fmac_f32_e32 v37, v23, v26
	v_fmac_f32_e32 v37, v14, v25
	v_fmac_f32_e32 v37, v22, v24
	ds_read_b128 v[24:27], v177
	s_waitcnt lgkmcnt(0)
	v_fmac_f32_e32 v33, v15, v27
	v_fmac_f32_e32 v33, v23, v26
	v_fmac_f32_e32 v33, v14, v25
	v_fmac_f32_e32 v33, v22, v24
	ds_read_b128 v[24:27], v178
	s_waitcnt lgkmcnt(0)
	v_fmac_f32_e32 v30, v15, v27
	v_fmac_f32_e32 v30, v23, v26
	v_fmac_f32_e32 v30, v14, v25
	v_fmac_f32_e32 v30, v22, v24
	ds_read_b128 v[22:25], v179
	flat_load_dwordx4 v[26:29], v[18:19] offset:1024
	flat_load_dwordx4 v[90:93], v[20:21] offset:1024
	v_mov_b32_e32 v15, v12
	v_mov_b32_e32 v12, v11
	v_mov_b32_e32 v14, v10
	s_waitcnt lgkmcnt(0)
	v_mov_b32_e32 v17, v24
	v_pk_mul_f32 v[10:11], v[12:13], v[114:115] op_sel_hi:[1,0]
	v_mov_b32_e32 v24, v23
	v_mov_b32_e32 v16, v22
	v_pk_mul_f32 v[10:11], v[10:11], v[24:25]
	ds_read_b128 v[22:25], v134 offset:5120
	v_pk_mul_f32 v[14:15], v[14:15], v[114:115] op_sel_hi:[1,0]
	s_waitcnt vmcnt(0)
	v_mov_b32_e32 v35, v28
	v_pk_mul_f32 v[14:15], v[14:15], v[16:17]
	v_mov_b32_e32 v17, v92
	v_mov_b32_e32 v92, v91
	v_mov_b32_e32 v16, v90
	v_pk_add_f32 v[12:13], v[92:93], 1.0 op_sel_hi:[1,0]
	v_mov_b32_e32 v28, v27
	v_pk_add_f32 v[16:17], v[16:17], 1.0 op_sel_hi:[1,0]
	v_mov_b32_e32 v34, v26
	v_pk_fma_f32 v[10:11], v[10:11], v[12:13], v[28:29]
	v_pk_fma_f32 v[14:15], v[14:15], v[16:17], v[34:35]
	s_waitcnt lgkmcnt(0)
	v_fmac_f32_e32 v89, v11, v25
	v_fmac_f32_e32 v89, v15, v24
	v_fmac_f32_e32 v89, v10, v23
	v_fmac_f32_e32 v89, v14, v22
	ds_read_b128 v[22:25], v134 offset:13312
	v_and_b32_sdwa v13, v14, v208 dst_sel:DWORD dst_unused:UNUSED_PAD src0_sel:WORD_1 src1_sel:DWORD
	v_add3_u32 v16, v14, v13, s57
	v_and_b32_sdwa v13, v11, v208 dst_sel:DWORD dst_unused:UNUSED_PAD src0_sel:WORD_1 src1_sel:DWORD
	v_and_b32_sdwa v17, v10, v208 dst_sel:DWORD dst_unused:UNUSED_PAD src0_sel:WORD_1 src1_sel:DWORD
	s_waitcnt lgkmcnt(0)
	v_fmac_f32_e32 v85, v11, v25
	v_fmac_f32_e32 v85, v15, v24
	v_fmac_f32_e32 v85, v10, v23
	v_fmac_f32_e32 v85, v14, v22
	ds_read_b128 v[22:25], v134 offset:21504
	v_and_b32_sdwa v12, v15, v208 dst_sel:DWORD dst_unused:UNUSED_PAD src0_sel:WORD_1 src1_sel:DWORD
	v_add3_u32 v13, v11, v13, s57
	v_add3_u32 v17, v10, v17, s57
	v_add3_u32 v12, v15, v12, s57
	s_waitcnt lgkmcnt(0)
	v_fmac_f32_e32 v81, v11, v25
	v_fmac_f32_e32 v81, v15, v24
	v_fmac_f32_e32 v81, v10, v23
	v_fmac_f32_e32 v81, v14, v22
	ds_read_b128 v[22:25], v134 offset:29696
	v_and_b32_e32 v13, 0xffff0000, v13
	v_and_b32_e32 v17, 0xffff0000, v17
	v_or_b32_sdwa v13, v13, v12 dst_sel:DWORD dst_unused:UNUSED_PAD src0_sel:DWORD src1_sel:WORD_1
	v_or_b32_sdwa v12, v17, v16 dst_sel:DWORD dst_unused:UNUSED_PAD src0_sel:DWORD src1_sel:WORD_1
	s_waitcnt lgkmcnt(0)
	v_fmac_f32_e32 v77, v11, v25
	v_fmac_f32_e32 v77, v15, v24
	v_fmac_f32_e32 v77, v10, v23
	v_fmac_f32_e32 v77, v14, v22
	ds_read_b128 v[22:25], v134 offset:37888
	global_store_dwordx2 v[94:95], v[12:13], off offset:2560
	s_waitcnt lgkmcnt(0)
	v_fmac_f32_e32 v73, v11, v25
	v_fmac_f32_e32 v73, v15, v24
	v_fmac_f32_e32 v73, v10, v23
	v_fmac_f32_e32 v73, v14, v22
	ds_read_b128 v[22:25], v134 offset:46080
	s_waitcnt lgkmcnt(0)
	v_fmac_f32_e32 v69, v11, v25
	v_fmac_f32_e32 v69, v15, v24
	v_fmac_f32_e32 v69, v10, v23
	v_fmac_f32_e32 v69, v14, v22
	ds_read_b128 v[22:25], v134 offset:54272
	s_waitcnt lgkmcnt(0)
	v_fmac_f32_e32 v65, v11, v25
	v_fmac_f32_e32 v65, v15, v24
	v_fmac_f32_e32 v65, v10, v23
	v_fmac_f32_e32 v65, v14, v22
	ds_read_b128 v[22:25], v134 offset:62464
	s_waitcnt lgkmcnt(0)
	v_fmac_f32_e32 v61, v11, v25
	v_fmac_f32_e32 v61, v15, v24
	v_fmac_f32_e32 v61, v10, v23
	v_fmac_f32_e32 v61, v14, v22
	ds_read_b128 v[22:25], v180
	s_waitcnt lgkmcnt(0)
	v_fmac_f32_e32 v57, v11, v25
	v_fmac_f32_e32 v57, v15, v24
	v_fmac_f32_e32 v57, v10, v23
	v_fmac_f32_e32 v57, v14, v22
	ds_read_b128 v[22:25], v181
	s_waitcnt lgkmcnt(0)
	v_fmac_f32_e32 v53, v11, v25
	v_fmac_f32_e32 v53, v15, v24
	v_fmac_f32_e32 v53, v10, v23
	v_fmac_f32_e32 v53, v14, v22
	ds_read_b128 v[22:25], v182
	s_waitcnt lgkmcnt(0)
	v_fmac_f32_e32 v49, v11, v25
	v_fmac_f32_e32 v49, v15, v24
	v_fmac_f32_e32 v49, v10, v23
	v_fmac_f32_e32 v49, v14, v22
	ds_read_b128 v[22:25], v183
	s_waitcnt lgkmcnt(0)
	v_fmac_f32_e32 v45, v11, v25
	v_fmac_f32_e32 v45, v15, v24
	v_fmac_f32_e32 v45, v10, v23
	v_fmac_f32_e32 v45, v14, v22
	ds_read_b128 v[22:25], v184
	s_waitcnt lgkmcnt(0)
	v_fmac_f32_e32 v41, v11, v25
	v_fmac_f32_e32 v41, v15, v24
	v_fmac_f32_e32 v41, v10, v23
	v_fmac_f32_e32 v41, v14, v22
	ds_read_b128 v[22:25], v185
	s_waitcnt lgkmcnt(0)
	v_fmac_f32_e32 v37, v11, v25
	v_fmac_f32_e32 v37, v15, v24
	v_fmac_f32_e32 v37, v10, v23
	v_fmac_f32_e32 v37, v14, v22
	ds_read_b128 v[22:25], v186
	s_waitcnt lgkmcnt(0)
	v_fmac_f32_e32 v33, v11, v25
	v_fmac_f32_e32 v33, v15, v24
	v_fmac_f32_e32 v33, v10, v23
	v_fmac_f32_e32 v33, v14, v22
	ds_read_b128 v[22:25], v187
	s_waitcnt lgkmcnt(0)
	v_fmac_f32_e32 v30, v11, v25
	v_fmac_f32_e32 v30, v15, v24
	v_fmac_f32_e32 v30, v10, v23
	v_fmac_f32_e32 v30, v14, v22
	ds_read_b128 v[12:15], v188
	flat_load_dwordx4 v[22:25], v[18:19] offset:2048
	flat_load_dwordx4 v[26:29], v[20:21] offset:2048
	v_mov_b32_e32 v10, v6
	v_mov_b32_e32 v11, v8
	v_pk_mul_f32 v[10:11], v[10:11], v[114:115] op_sel_hi:[1,0]
	s_waitcnt lgkmcnt(0)
	v_mov_b32_e32 v16, v12
	v_mov_b32_e32 v17, v14
	v_pk_mul_f32 v[10:11], v[10:11], v[16:17]
	v_mov_b32_e32 v8, v7
	v_pk_mul_f32 v[6:7], v[8:9], v[114:115] op_sel_hi:[1,0]
	v_mov_b32_e32 v14, v13
	v_pk_mul_f32 v[6:7], v[6:7], v[14:15]
	s_waitcnt vmcnt(0)
	v_mov_b32_e32 v34, v22
	v_mov_b32_e32 v16, v26
	v_mov_b32_e32 v17, v28
	v_pk_add_f32 v[16:17], v[16:17], 1.0 op_sel_hi:[1,0]
	v_mov_b32_e32 v35, v24
	v_mov_b32_e32 v28, v27
	v_pk_fma_f32 v[10:11], v[10:11], v[16:17], v[34:35]
	v_pk_add_f32 v[8:9], v[28:29], 1.0 op_sel_hi:[1,0]
	v_mov_b32_e32 v24, v23
	v_pk_fma_f32 v[6:7], v[6:7], v[8:9], v[24:25]
	v_and_b32_sdwa v9, v10, v208 dst_sel:DWORD dst_unused:UNUSED_PAD src0_sel:WORD_1 src1_sel:DWORD
	v_add3_u32 v12, v10, v9, s57
	v_and_b32_sdwa v9, v7, v208 dst_sel:DWORD dst_unused:UNUSED_PAD src0_sel:WORD_1 src1_sel:DWORD
	v_and_b32_sdwa v13, v6, v208 dst_sel:DWORD dst_unused:UNUSED_PAD src0_sel:WORD_1 src1_sel:DWORD
	v_and_b32_sdwa v8, v11, v208 dst_sel:DWORD dst_unused:UNUSED_PAD src0_sel:WORD_1 src1_sel:DWORD
	v_add3_u32 v9, v7, v9, s57
	v_add3_u32 v13, v6, v13, s57
	v_add3_u32 v8, v11, v8, s57
	v_and_b32_e32 v9, 0xffff0000, v9
	v_and_b32_e32 v13, 0xffff0000, v13
	v_or_b32_sdwa v9, v9, v8 dst_sel:DWORD dst_unused:UNUSED_PAD src0_sel:DWORD src1_sel:WORD_1
	v_or_b32_sdwa v8, v13, v12 dst_sel:DWORD dst_unused:UNUSED_PAD src0_sel:DWORD src1_sel:WORD_1
	ds_read_b128 v[12:15], v134 offset:6144
	global_store_dwordx2 v[94:95], v[8:9], off offset:3072
	s_waitcnt lgkmcnt(0)
	v_fmac_f32_e32 v89, v7, v15
	v_fmac_f32_e32 v89, v11, v14
	v_fmac_f32_e32 v89, v6, v13
	v_fmac_f32_e32 v89, v10, v12
	ds_read_b128 v[12:15], v134 offset:14336
	s_waitcnt lgkmcnt(0)
	v_fmac_f32_e32 v85, v7, v15
	v_fmac_f32_e32 v85, v11, v14
	v_fmac_f32_e32 v85, v6, v13
	v_fmac_f32_e32 v85, v10, v12
	ds_read_b128 v[12:15], v134 offset:22528
	s_waitcnt lgkmcnt(0)
	v_fmac_f32_e32 v81, v7, v15
	v_fmac_f32_e32 v81, v11, v14
	v_fmac_f32_e32 v81, v6, v13
	v_fmac_f32_e32 v81, v10, v12
	ds_read_b128 v[12:15], v134 offset:30720
	s_waitcnt lgkmcnt(0)
	v_fmac_f32_e32 v77, v7, v15
	v_fmac_f32_e32 v77, v11, v14
	v_fmac_f32_e32 v77, v6, v13
	v_fmac_f32_e32 v77, v10, v12
	ds_read_b128 v[12:15], v134 offset:38912
	s_waitcnt lgkmcnt(0)
	v_fmac_f32_e32 v73, v7, v15
	v_fmac_f32_e32 v73, v11, v14
	v_fmac_f32_e32 v73, v6, v13
	v_fmac_f32_e32 v73, v10, v12
	ds_read_b128 v[12:15], v134 offset:47104
	s_waitcnt lgkmcnt(0)
	v_fmac_f32_e32 v69, v7, v15
	v_fmac_f32_e32 v69, v11, v14
	v_fmac_f32_e32 v69, v6, v13
	v_fmac_f32_e32 v69, v10, v12
	ds_read_b128 v[12:15], v134 offset:55296
	s_waitcnt lgkmcnt(0)
	v_fmac_f32_e32 v65, v7, v15
	v_fmac_f32_e32 v65, v11, v14
	v_fmac_f32_e32 v65, v6, v13
	v_fmac_f32_e32 v65, v10, v12
	ds_read_b128 v[12:15], v134 offset:63488
	s_waitcnt lgkmcnt(0)
	v_fmac_f32_e32 v61, v7, v15
	v_fmac_f32_e32 v61, v11, v14
	v_fmac_f32_e32 v61, v6, v13
	v_fmac_f32_e32 v61, v10, v12
	ds_read_b128 v[12:15], v189
	s_waitcnt lgkmcnt(0)
	v_fmac_f32_e32 v57, v7, v15
	v_fmac_f32_e32 v57, v11, v14
	v_fmac_f32_e32 v57, v6, v13
	v_fmac_f32_e32 v57, v10, v12
	ds_read_b128 v[12:15], v191
	s_waitcnt lgkmcnt(0)
	v_fmac_f32_e32 v53, v7, v15
	v_fmac_f32_e32 v53, v11, v14
	v_fmac_f32_e32 v53, v6, v13
	v_fmac_f32_e32 v53, v10, v12
	ds_read_b128 v[12:15], v192
	s_waitcnt lgkmcnt(0)
	v_fmac_f32_e32 v49, v7, v15
	v_fmac_f32_e32 v49, v11, v14
	v_fmac_f32_e32 v49, v6, v13
	v_fmac_f32_e32 v49, v10, v12
	ds_read_b128 v[12:15], v193
	s_waitcnt lgkmcnt(0)
	v_fmac_f32_e32 v45, v7, v15
	v_fmac_f32_e32 v45, v11, v14
	v_fmac_f32_e32 v45, v6, v13
	v_fmac_f32_e32 v45, v10, v12
	ds_read_b128 v[12:15], v194
	s_waitcnt lgkmcnt(0)
	v_fmac_f32_e32 v41, v7, v15
	v_fmac_f32_e32 v41, v11, v14
	v_fmac_f32_e32 v41, v6, v13
	v_fmac_f32_e32 v41, v10, v12
	ds_read_b128 v[12:15], v195
	s_waitcnt lgkmcnt(0)
	v_fmac_f32_e32 v37, v7, v15
	v_fmac_f32_e32 v37, v11, v14
	v_fmac_f32_e32 v37, v6, v13
	v_fmac_f32_e32 v37, v10, v12
	ds_read_b128 v[12:15], v196
	s_waitcnt lgkmcnt(0)
	v_fmac_f32_e32 v33, v7, v15
	v_fmac_f32_e32 v33, v11, v14
	v_fmac_f32_e32 v33, v6, v13
	v_fmac_f32_e32 v33, v10, v12
	ds_read_b128 v[12:15], v197
	s_waitcnt lgkmcnt(0)
	v_fmac_f32_e32 v30, v7, v15
	v_fmac_f32_e32 v30, v11, v14
	v_fmac_f32_e32 v30, v6, v13
	v_fmac_f32_e32 v30, v10, v12
	ds_read_b128 v[8:11], v198
	flat_load_dwordx4 v[12:15], v[18:19] offset:3072
	s_nop 0
	flat_load_dwordx4 v[16:19], v[20:21] offset:3072
	v_mov_b32_e32 v6, v2
	v_mov_b32_e32 v7, v4
	v_pk_mul_f32 v[6:7], v[6:7], v[114:115] op_sel_hi:[1,0]
	s_waitcnt lgkmcnt(0)
	v_mov_b32_e32 v20, v8
	v_mov_b32_e32 v21, v10
	v_pk_mul_f32 v[6:7], v[6:7], v[20:21]
	v_mov_b32_e32 v4, v3
	v_pk_mul_f32 v[2:3], v[4:5], v[114:115] op_sel_hi:[1,0]
	v_mov_b32_e32 v10, v9
	v_pk_mul_f32 v[2:3], v[2:3], v[10:11]
	s_waitcnt vmcnt(0)
	v_mov_b32_e32 v22, v12
	v_mov_b32_e32 v20, v16
	v_mov_b32_e32 v21, v18
	v_pk_add_f32 v[20:21], v[20:21], 1.0 op_sel_hi:[1,0]
	v_mov_b32_e32 v23, v14
	v_mov_b32_e32 v18, v17
	v_pk_fma_f32 v[6:7], v[6:7], v[20:21], v[22:23]
	v_pk_add_f32 v[4:5], v[18:19], 1.0 op_sel_hi:[1,0]
	v_mov_b32_e32 v14, v13
	v_pk_fma_f32 v[2:3], v[2:3], v[4:5], v[14:15]
	v_and_b32_sdwa v5, v6, v208 dst_sel:DWORD dst_unused:UNUSED_PAD src0_sel:WORD_1 src1_sel:DWORD
	v_add3_u32 v8, v6, v5, s57
	v_and_b32_sdwa v5, v3, v208 dst_sel:DWORD dst_unused:UNUSED_PAD src0_sel:WORD_1 src1_sel:DWORD
	v_and_b32_sdwa v9, v2, v208 dst_sel:DWORD dst_unused:UNUSED_PAD src0_sel:WORD_1 src1_sel:DWORD
	v_and_b32_sdwa v4, v7, v208 dst_sel:DWORD dst_unused:UNUSED_PAD src0_sel:WORD_1 src1_sel:DWORD
	v_add3_u32 v5, v3, v5, s57
	v_add3_u32 v9, v2, v9, s57
	v_add3_u32 v4, v7, v4, s57
	v_and_b32_e32 v5, 0xffff0000, v5
	v_and_b32_e32 v9, 0xffff0000, v9
	v_or_b32_sdwa v5, v5, v4 dst_sel:DWORD dst_unused:UNUSED_PAD src0_sel:DWORD src1_sel:WORD_1
	v_or_b32_sdwa v4, v9, v8 dst_sel:DWORD dst_unused:UNUSED_PAD src0_sel:DWORD src1_sel:WORD_1
	ds_read_b128 v[8:11], v134 offset:7168
	global_store_dwordx2 v[94:95], v[4:5], off offset:3584
	s_waitcnt lgkmcnt(0)
	v_fmac_f32_e32 v89, v3, v11
	v_fmac_f32_e32 v89, v7, v10
	v_fmac_f32_e32 v89, v2, v9
	v_fmac_f32_e32 v89, v6, v8
	ds_read_b128 v[8:11], v134 offset:15360
	s_waitcnt lgkmcnt(0)
	v_fmac_f32_e32 v85, v3, v11
	v_fmac_f32_e32 v85, v7, v10
	v_fmac_f32_e32 v85, v2, v9
	v_fmac_f32_e32 v85, v6, v8
	ds_read_b128 v[8:11], v134 offset:23552
	s_waitcnt lgkmcnt(0)
	v_fmac_f32_e32 v81, v3, v11
	v_fmac_f32_e32 v81, v7, v10
	v_fmac_f32_e32 v81, v2, v9
	v_fmac_f32_e32 v81, v6, v8
	ds_read_b128 v[8:11], v134 offset:31744
	s_waitcnt lgkmcnt(0)
	v_fmac_f32_e32 v77, v3, v11
	v_fmac_f32_e32 v77, v7, v10
	v_fmac_f32_e32 v77, v2, v9
	v_fmac_f32_e32 v77, v6, v8
	ds_read_b128 v[8:11], v134 offset:39936
	s_waitcnt lgkmcnt(0)
	v_fmac_f32_e32 v73, v3, v11
	v_fmac_f32_e32 v73, v7, v10
	v_fmac_f32_e32 v73, v2, v9
	v_fmac_f32_e32 v73, v6, v8
	ds_read_b128 v[8:11], v134 offset:48128
	s_waitcnt lgkmcnt(0)
	v_fmac_f32_e32 v69, v3, v11
	v_fmac_f32_e32 v69, v7, v10
	v_fmac_f32_e32 v69, v2, v9
	v_fmac_f32_e32 v69, v6, v8
	ds_read_b128 v[8:11], v134 offset:56320
	s_waitcnt lgkmcnt(0)
	v_fmac_f32_e32 v65, v3, v11
	v_fmac_f32_e32 v65, v7, v10
	v_fmac_f32_e32 v65, v2, v9
	v_fmac_f32_e32 v65, v6, v8
	ds_read_b128 v[8:11], v134 offset:64512
	s_waitcnt lgkmcnt(0)
	v_fmac_f32_e32 v61, v3, v11
	v_fmac_f32_e32 v61, v7, v10
	v_fmac_f32_e32 v61, v2, v9
	v_fmac_f32_e32 v61, v6, v8
	ds_read_b128 v[8:11], v199
	s_waitcnt lgkmcnt(0)
	v_fmac_f32_e32 v57, v3, v11
	v_fmac_f32_e32 v57, v7, v10
	v_fmac_f32_e32 v57, v2, v9
	v_fmac_f32_e32 v57, v6, v8
	ds_read_b128 v[8:11], v200
	s_waitcnt lgkmcnt(0)
	v_fmac_f32_e32 v53, v3, v11
	v_fmac_f32_e32 v53, v7, v10
	v_fmac_f32_e32 v53, v2, v9
	v_fmac_f32_e32 v53, v6, v8
	ds_read_b128 v[8:11], v201
	s_waitcnt lgkmcnt(0)
	v_fmac_f32_e32 v49, v3, v11
	v_fmac_f32_e32 v49, v7, v10
	v_fmac_f32_e32 v49, v2, v9
	v_fmac_f32_e32 v49, v6, v8
	ds_read_b128 v[8:11], v202
	s_waitcnt lgkmcnt(0)
	v_fmac_f32_e32 v45, v3, v11
	v_fmac_f32_e32 v45, v7, v10
	v_fmac_f32_e32 v45, v2, v9
	v_fmac_f32_e32 v45, v6, v8
	ds_read_b128 v[8:11], v203
	s_waitcnt lgkmcnt(0)
	v_fmac_f32_e32 v41, v3, v11
	v_fmac_f32_e32 v41, v7, v10
	v_fmac_f32_e32 v41, v2, v9
	v_fmac_f32_e32 v41, v6, v8
	ds_read_b128 v[8:11], v204
	s_waitcnt lgkmcnt(0)
	v_fmac_f32_e32 v37, v3, v11
	v_fmac_f32_e32 v37, v7, v10
	v_fmac_f32_e32 v37, v2, v9
	v_fmac_f32_e32 v37, v6, v8
	ds_read_b128 v[8:11], v205
	s_waitcnt lgkmcnt(0)
	v_fmac_f32_e32 v33, v3, v11
	v_fmac_f32_e32 v33, v7, v10
	v_fmac_f32_e32 v33, v2, v9
	v_fmac_f32_e32 v33, v6, v8
	ds_read_b128 v[8:11], v206
	s_waitcnt lgkmcnt(0)
	v_fmac_f32_e32 v30, v3, v11
	v_fmac_f32_e32 v30, v7, v10
	v_fmac_f32_e32 v30, v2, v9
	v_fmac_f32_e32 v30, v6, v8
	ds_bpermute_b32 v6, v1, v81
	ds_bpermute_b32 v7, v1, v77
	ds_bpermute_b32 v22, v1, v49
	ds_bpermute_b32 v10, v1, v73
	ds_bpermute_b32 v24, v1, v41
	s_waitcnt lgkmcnt(4)
	v_add_f32_e32 v6, v81, v6
	ds_bpermute_b32 v8, v128, v6
	s_waitcnt lgkmcnt(4)
	v_add_f32_e32 v7, v77, v7
	ds_bpermute_b32 v9, v128, v7
	s_waitcnt lgkmcnt(4)
	v_add_f32_e32 v22, v49, v22
	ds_bpermute_b32 v23, v128, v22
	s_waitcnt lgkmcnt(2)
	v_add_f32_e32 v6, v6, v8
	ds_bpermute_b32 v8, v129, v6
	s_waitcnt lgkmcnt(2)
	v_add_f32_e32 v7, v7, v9
	ds_bpermute_b32 v9, v129, v7
	s_waitcnt lgkmcnt(2)
	v_add_f32_e32 v22, v22, v23
	ds_bpermute_b32 v23, v129, v22
	s_waitcnt lgkmcnt(2)
	v_add_f32_e32 v6, v6, v8
	ds_bpermute_b32 v8, v130, v6
	s_waitcnt lgkmcnt(2)
	v_add_f32_e32 v7, v7, v9
	ds_bpermute_b32 v9, v130, v7
	v_add_f32_e32 v10, v73, v10
	s_waitcnt lgkmcnt(2)
	v_add_f32_e32 v22, v22, v23
	s_waitcnt lgkmcnt(1)
	v_add_f32_e32 v6, v6, v8
	ds_bpermute_b32 v8, v131, v6
	s_waitcnt lgkmcnt(1)
	v_add_f32_e32 v9, v7, v9
	ds_bpermute_b32 v12, v131, v9
	v_add_f32_e32 v23, v41, v24
	ds_bpermute_b32 v11, v128, v10
	s_waitcnt lgkmcnt(2)
	v_add_f32_e32 v6, v6, v8
	ds_bpermute_b32 v8, v1, v69
	ds_bpermute_b32 v24, v128, v23
	ds_bpermute_b32 v27, v130, v22
	s_waitcnt lgkmcnt(3)
	v_add_f32_e32 v10, v10, v11
	ds_bpermute_b32 v11, v129, v10
	s_waitcnt lgkmcnt(3)
	v_add_f32_e32 v13, v69, v8
	ds_bpermute_b32 v14, v128, v13
	v_add_f32_e32 v8, v9, v12
	s_waitcnt lgkmcnt(3)
	v_add_f32_e32 v23, v23, v24
	ds_bpermute_b32 v24, v129, v23
	s_waitcnt lgkmcnt(2)
	v_add_f32_e32 v10, v10, v11
	s_waitcnt lgkmcnt(1)
	v_add_f32_e32 v12, v13, v14
	ds_bpermute_b32 v14, v1, v65
	v_add_f32_e32 v22, v22, v27
	s_waitcnt lgkmcnt(1)
	v_add_f32_e32 v23, v23, v24
	ds_bpermute_b32 v11, v130, v10
	ds_bpermute_b32 v27, v131, v22
	s_waitcnt lgkmcnt(2)
	v_add_f32_e32 v14, v65, v14
	ds_bpermute_b32 v15, v128, v14
	ds_bpermute_b32 v24, v130, v23
	s_waitcnt lgkmcnt(3)
	v_add_f32_e32 v10, v10, v11
	s_waitcnt lgkmcnt(2)
	v_add_f32_e32 v22, v22, v27
	ds_bpermute_b32 v11, v131, v10
	s_waitcnt lgkmcnt(2)
	v_add_f32_e32 v14, v14, v15
	ds_bpermute_b32 v15, v129, v14
	s_waitcnt lgkmcnt(2)
	v_add_f32_e32 v27, v23, v24
	ds_bpermute_b32 v28, v131, v27
	ds_bpermute_b32 v2, v1, v89
	ds_bpermute_b32 v3, v1, v85
	s_waitcnt lgkmcnt(3)
	v_add_f32_e32 v14, v14, v15
	ds_bpermute_b32 v15, v130, v14
	v_add_f32_e32 v10, v10, v11
	ds_bpermute_b32 v11, v1, v61
	ds_bpermute_b32 v18, v1, v57
	ds_bpermute_b32 v29, v1, v37
	s_waitcnt lgkmcnt(3)
	v_add_f32_e32 v14, v14, v15
	ds_bpermute_b32 v15, v131, v14
	ds_bpermute_b32 v31, v1, v30
	v_add_f32_e32 v2, v89, v2
	v_add_f32_e32 v3, v85, v3
	s_waitcnt lgkmcnt(4)
	v_add_f32_e32 v16, v61, v11
	s_waitcnt lgkmcnt(1)
	v_add_f32_e32 v14, v14, v15
	ds_bpermute_b32 v15, v1, v53
	v_add_f32_e32 v18, v57, v18
	v_add_f32_e32 v29, v37, v29
	s_waitcnt lgkmcnt(1)
	v_add_f32_e32 v30, v30, v31
	ds_bpermute_b32 v4, v128, v2
	s_waitcnt lgkmcnt(1)
	v_add_f32_e32 v20, v53, v15
	ds_bpermute_b32 v21, v128, v20
	ds_bpermute_b32 v5, v128, v3
	ds_bpermute_b32 v17, v128, v16
	ds_bpermute_b32 v19, v128, v18
	ds_bpermute_b32 v32, v128, v29
	s_waitcnt lgkmcnt(4)
	v_add_f32_e32 v20, v20, v21
	ds_bpermute_b32 v21, v129, v20
	ds_bpermute_b32 v31, v128, v30
	v_add_f32_e32 v2, v2, v4
	s_waitcnt lgkmcnt(5)
	v_add_f32_e32 v3, v3, v5
	s_waitcnt lgkmcnt(4)
	v_add_f32_e32 v16, v16, v17
	s_waitcnt lgkmcnt(1)
	v_add_f32_e32 v20, v20, v21
	ds_bpermute_b32 v21, v130, v20
	v_add_f32_e32 v18, v18, v19
	v_add_f32_e32 v29, v29, v32
	s_waitcnt lgkmcnt(1)
	v_add_f32_e32 v30, v30, v31
	ds_bpermute_b32 v4, v129, v2
	s_waitcnt lgkmcnt(1)
	v_add_f32_e32 v20, v20, v21
	ds_bpermute_b32 v21, v1, v45
	ds_bpermute_b32 v25, v131, v20
	ds_bpermute_b32 v5, v129, v3
	ds_bpermute_b32 v13, v129, v12
	ds_bpermute_b32 v17, v129, v16
	s_waitcnt lgkmcnt(4)
	v_add_f32_e32 v21, v45, v21
	ds_bpermute_b32 v26, v128, v21
	s_waitcnt lgkmcnt(4)
	v_add_f32_e32 v20, v20, v25
	ds_bpermute_b32 v19, v129, v18
	ds_bpermute_b32 v32, v129, v29
	ds_bpermute_b32 v31, v129, v30
	s_waitcnt lgkmcnt(3)
	v_add_f32_e32 v21, v21, v26
	ds_bpermute_b32 v26, v129, v21
	v_add_f32_e32 v2, v2, v4
	v_add_f32_e32 v3, v3, v5
	v_add_f32_e32 v12, v12, v13
	v_add_f32_e32 v16, v16, v17
	s_waitcnt lgkmcnt(0)
	v_add_f32_e32 v25, v21, v26
	ds_bpermute_b32 v26, v130, v25
	v_add_f32_e32 v18, v18, v19
	v_add_f32_e32 v29, v29, v32
	v_add_f32_e32 v30, v30, v31
	ds_bpermute_b32 v4, v130, v2
	s_waitcnt lgkmcnt(1)
	v_add_f32_e32 v25, v25, v26
	ds_bpermute_b32 v26, v131, v25
	ds_bpermute_b32 v5, v130, v3
	ds_bpermute_b32 v13, v130, v12
	ds_bpermute_b32 v17, v130, v16
	ds_bpermute_b32 v19, v130, v18
	s_waitcnt lgkmcnt(4)
	v_add_f32_e32 v24, v25, v26
	v_add_f32_e32 v26, v27, v28
	ds_bpermute_b32 v28, v1, v33
	ds_bpermute_b32 v32, v130, v29
	ds_bpermute_b32 v31, v130, v30
	v_add_f32_e32 v2, v2, v4
	s_waitcnt lgkmcnt(6)
	v_add_f32_e32 v3, v3, v5
	s_waitcnt lgkmcnt(2)
	v_add_f32_e32 v28, v33, v28
	ds_bpermute_b32 v33, v128, v28
	v_add_f32_e32 v12, v12, v13
	v_add_f32_e32 v16, v16, v17
	v_add_f32_e32 v18, v18, v19
	s_waitcnt lgkmcnt(2)
	v_add_f32_e32 v29, v29, v32
	s_waitcnt lgkmcnt(0)
	v_add_f32_e32 v28, v28, v33
	ds_bpermute_b32 v33, v129, v28
	v_add_f32_e32 v35, v30, v31
	ds_bpermute_b32 v4, v131, v2
	ds_bpermute_b32 v5, v131, v3
	ds_bpermute_b32 v13, v131, v12
	s_waitcnt lgkmcnt(3)
	v_add_f32_e32 v28, v28, v33
	ds_bpermute_b32 v33, v130, v28
	ds_bpermute_b32 v17, v131, v16
	ds_bpermute_b32 v19, v131, v18
	ds_bpermute_b32 v32, v131, v29
	ds_bpermute_b32 v36, v131, v35
	s_waitcnt lgkmcnt(4)
	v_add_f32_e32 v33, v28, v33
	ds_bpermute_b32 v34, v131, v33
	v_add_f32_e32 v2, v2, v4
	v_add_f32_e32 v3, v3, v5
	v_add_f32_e32 v12, v12, v13
	s_waitcnt lgkmcnt(4)
	v_add_f32_e32 v16, v16, v17
	s_waitcnt lgkmcnt(3)
	v_add_f32_e32 v18, v18, v19
	s_waitcnt lgkmcnt(2)
	v_add_f32_e32 v28, v29, v32
	s_waitcnt lgkmcnt(0)
	v_add_f32_e32 v29, v33, v34
	v_add_f32_e32 v32, v35, v36
	ds_bpermute_b32 v4, v132, v2
	ds_bpermute_b32 v5, v132, v3
	ds_bpermute_b32 v7, v132, v6
	ds_bpermute_b32 v9, v132, v8
	ds_bpermute_b32 v11, v132, v10
	ds_bpermute_b32 v13, v132, v12
	ds_bpermute_b32 v15, v132, v14
	ds_bpermute_b32 v17, v132, v16
	ds_bpermute_b32 v19, v132, v18
	ds_bpermute_b32 v21, v132, v20
	ds_bpermute_b32 v23, v132, v22
	ds_bpermute_b32 v25, v132, v24
	ds_bpermute_b32 v27, v132, v26
	ds_bpermute_b32 v30, v132, v28
	ds_bpermute_b32 v31, v132, v29
	ds_bpermute_b32 v33, v132, v32
	s_and_saveexec_b64 s[52:53], s[2:3]
	s_cbranch_execz .LBB0_1364
	s_waitcnt lgkmcnt(14)
	v_add_f32_e32 v2, v2, v4
	v_add_f32_e32 v3, v3, v5
	s_mov_b32 s61, 0xff61b1e6
	v_max3_f32 v4, v2, s61, v3
	s_waitcnt lgkmcnt(13)
	v_add_f32_e32 v5, v6, v7
	s_waitcnt lgkmcnt(12)
	v_add_f32_e32 v6, v8, v9
	v_max3_f32 v4, v4, v5, v6
	s_waitcnt lgkmcnt(11)
	v_add_f32_e32 v7, v10, v11
	s_waitcnt lgkmcnt(10)
	v_add_f32_e32 v8, v12, v13
	v_max3_f32 v4, v4, v7, v8
	s_waitcnt lgkmcnt(9)
	v_add_f32_e32 v11, v14, v15
	s_waitcnt lgkmcnt(8)
	v_add_f32_e32 v15, v16, v17
	v_max3_f32 v4, v4, v11, v15
	s_waitcnt lgkmcnt(7)
	v_add_f32_e32 v16, v18, v19
	s_waitcnt lgkmcnt(6)
	v_add_f32_e32 v17, v20, v21
	v_max3_f32 v4, v4, v16, v17
	s_waitcnt lgkmcnt(5)
	v_add_f32_e32 v18, v22, v23
	s_waitcnt lgkmcnt(4)
	v_add_f32_e32 v19, v24, v25
	v_max3_f32 v4, v4, v18, v19
	s_waitcnt lgkmcnt(3)
	v_add_f32_e32 v14, v26, v27
	s_waitcnt lgkmcnt(2)
	v_add_f32_e32 v13, v28, v30
	s_waitcnt lgkmcnt(0)
	v_add_f32_e32 v32, v32, v33
	v_max3_f32 v4, v4, v14, v13
	v_add_f32_e32 v10, v29, v31
	v_max3_f32 v12, v4, v10, v32
	v_sub_f32_e32 v4, v32, v12
	v_mul_f32_e32 v9, 0x3fb8aa3b, v4
	v_fma_f32 v20, v4, s58, -v9
	v_rndne_f32_e32 v21, v9
	v_fmac_f32_e32 v20, 0x32a5705f, v4
	v_sub_f32_e32 v9, v9, v21
	v_add_f32_e32 v9, v9, v20
	v_exp_f32_e32 v9, v9
	v_cvt_i32_f32_e32 v20, v21
	v_cmp_ngt_f32_e32 vcc, s59, v4
	v_sub_f32_e32 v2, v2, v12
	v_sub_f32_e32 v3, v3, v12
	v_ldexp_f32 v9, v9, v20
	v_cndmask_b32_e32 v9, 0, v9, vcc
	v_cmp_nlt_f32_e32 vcc, s60, v4
	v_mul_f32_e32 v4, 0x3fb8aa3b, v2
	v_fma_f32 v20, v2, s58, -v4
	v_rndne_f32_e32 v21, v4
	v_fmac_f32_e32 v20, 0x32a5705f, v2
	v_sub_f32_e32 v4, v4, v21
	v_add_f32_e32 v4, v4, v20
	v_exp_f32_e32 v4, v4
	v_cvt_i32_f32_e32 v20, v21
	v_cndmask_b32_e32 v9, v209, v9, vcc
	v_cmp_ngt_f32_e32 vcc, s59, v2
	v_sub_f32_e32 v17, v17, v12
	v_ldexp_f32 v4, v4, v20
	v_cndmask_b32_e32 v4, 0, v4, vcc
	v_cmp_nlt_f32_e32 vcc, s60, v2
	v_sub_f32_e32 v18, v18, v12
	v_sub_f32_e32 v19, v19, v12
	v_cndmask_b32_e32 v2, v209, v4, vcc
	v_mul_f32_e32 v4, 0x3fb8aa3b, v3
	v_fma_f32 v20, v3, s58, -v4
	v_rndne_f32_e32 v21, v4
	v_fmac_f32_e32 v20, 0x32a5705f, v3
	v_sub_f32_e32 v4, v4, v21
	v_add_f32_e32 v4, v4, v20
	v_exp_f32_e32 v4, v4
	v_cvt_i32_f32_e32 v20, v21
	v_cmp_ngt_f32_e32 vcc, s59, v3
	v_sub_f32_e32 v14, v14, v12
	v_sub_f32_e32 v13, v13, v12
	v_ldexp_f32 v4, v4, v20
	v_cndmask_b32_e32 v4, 0, v4, vcc
	v_cmp_nlt_f32_e32 vcc, s60, v3
	v_sub_f32_e32 v10, v10, v12
	s_nop 0
	v_cndmask_b32_e32 v3, v209, v4, vcc
	v_sub_f32_e32 v4, v5, v12
	v_mul_f32_e32 v5, 0x3fb8aa3b, v4
	v_fma_f32 v21, v4, s58, -v5
	v_rndne_f32_e32 v22, v5
	v_fmac_f32_e32 v21, 0x32a5705f, v4
	v_sub_f32_e32 v5, v5, v22
	v_add_f32_e32 v5, v5, v21
	v_exp_f32_e32 v5, v5
	v_cvt_i32_f32_e32 v21, v22
	v_cmp_ngt_f32_e32 vcc, s59, v4
	v_add_f32_e32 v20, v2, v3
	v_ldexp_f32 v5, v5, v21
	v_cndmask_b32_e32 v5, 0, v5, vcc
	v_cmp_nlt_f32_e32 vcc, s60, v4
	s_nop 1
	v_cndmask_b32_e32 v4, v209, v5, vcc
	v_sub_f32_e32 v5, v6, v12
	v_mul_f32_e32 v6, 0x3fb8aa3b, v5
	v_fma_f32 v21, v5, s58, -v6
	v_rndne_f32_e32 v22, v6
	v_fmac_f32_e32 v21, 0x32a5705f, v5
	v_sub_f32_e32 v6, v6, v22
	v_add_f32_e32 v6, v6, v21
	v_exp_f32_e32 v6, v6
	v_cvt_i32_f32_e32 v21, v22
	v_cmp_ngt_f32_e32 vcc, s59, v5
	v_add_f32_e32 v20, v4, v20
	v_ldexp_f32 v6, v6, v21
	v_cndmask_b32_e32 v6, 0, v6, vcc
	v_cmp_nlt_f32_e32 vcc, s60, v5
	s_nop 1
	v_cndmask_b32_e32 v5, v209, v6, vcc
	v_sub_f32_e32 v6, v7, v12
	v_mul_f32_e32 v7, 0x3fb8aa3b, v6
	v_fma_f32 v21, v6, s58, -v7
	v_rndne_f32_e32 v22, v7
	v_fmac_f32_e32 v21, 0x32a5705f, v6
	v_sub_f32_e32 v7, v7, v22
	v_add_f32_e32 v7, v7, v21
	v_exp_f32_e32 v7, v7
	v_cvt_i32_f32_e32 v21, v22
	v_cmp_ngt_f32_e32 vcc, s59, v6
	v_add_f32_e32 v20, v5, v20
	v_ldexp_f32 v7, v7, v21
	v_cndmask_b32_e32 v7, 0, v7, vcc
	v_cmp_nlt_f32_e32 vcc, s60, v6
	s_nop 1
	v_cndmask_b32_e32 v6, v209, v7, vcc
	v_sub_f32_e32 v7, v8, v12
	v_mul_f32_e32 v8, 0x3fb8aa3b, v7
	v_fma_f32 v21, v7, s58, -v8
	v_rndne_f32_e32 v22, v8
	v_fmac_f32_e32 v21, 0x32a5705f, v7
	v_sub_f32_e32 v8, v8, v22
	v_add_f32_e32 v8, v8, v21
	v_exp_f32_e32 v8, v8
	v_cvt_i32_f32_e32 v21, v22
	v_cmp_ngt_f32_e32 vcc, s59, v7
	v_add_f32_e32 v20, v6, v20
	v_ldexp_f32 v8, v8, v21
	v_cndmask_b32_e32 v8, 0, v8, vcc
	v_cmp_nlt_f32_e32 vcc, s60, v7
	s_nop 1
	v_cndmask_b32_e32 v7, v209, v8, vcc
	v_sub_f32_e32 v8, v11, v12
	v_mul_f32_e32 v11, 0x3fb8aa3b, v8
	v_fma_f32 v21, v8, s58, -v11
	v_rndne_f32_e32 v22, v11
	v_fmac_f32_e32 v21, 0x32a5705f, v8
	v_sub_f32_e32 v11, v11, v22
	v_add_f32_e32 v11, v11, v21
	v_exp_f32_e32 v11, v11
	v_cvt_i32_f32_e32 v21, v22
	v_cmp_ngt_f32_e32 vcc, s59, v8
	v_add_f32_e32 v20, v7, v20
	v_ldexp_f32 v11, v11, v21
	v_cndmask_b32_e32 v11, 0, v11, vcc
	v_cmp_nlt_f32_e32 vcc, s60, v8
	s_nop 1
	v_cndmask_b32_e32 v8, v209, v11, vcc
	v_sub_f32_e32 v11, v15, v12
	v_mul_f32_e32 v15, 0x3fb8aa3b, v11
	v_fma_f32 v21, v11, s58, -v15
	v_rndne_f32_e32 v22, v15
	v_fmac_f32_e32 v21, 0x32a5705f, v11
	v_sub_f32_e32 v15, v15, v22
	v_add_f32_e32 v15, v15, v21
	v_exp_f32_e32 v15, v15
	v_cvt_i32_f32_e32 v21, v22
	v_cmp_ngt_f32_e32 vcc, s59, v11
	v_add_f32_e32 v20, v8, v20
	v_ldexp_f32 v15, v15, v21
	v_cndmask_b32_e32 v15, 0, v15, vcc
	v_cmp_nlt_f32_e32 vcc, s60, v11
	s_nop 1
	v_cndmask_b32_e32 v11, v209, v15, vcc
	v_sub_f32_e32 v15, v16, v12
	v_mul_f32_e32 v16, 0x3fb8aa3b, v15
	v_fma_f32 v21, v15, s58, -v16
	v_rndne_f32_e32 v22, v16
	v_fmac_f32_e32 v21, 0x32a5705f, v15
	v_sub_f32_e32 v16, v16, v22
	v_add_f32_e32 v16, v16, v21
	v_exp_f32_e32 v16, v16
	v_cvt_i32_f32_e32 v21, v22
	v_cmp_ngt_f32_e32 vcc, s59, v15
	v_add_f32_e32 v20, v11, v20
	v_mul_f32_e32 v12, 0x3fb8aa3b, v10
	v_ldexp_f32 v16, v16, v21
	v_cndmask_b32_e32 v16, 0, v16, vcc
	v_cmp_nlt_f32_e32 vcc, s60, v15
	s_nop 1
	v_cndmask_b32_e32 v15, v209, v16, vcc
	v_add_f32_e32 v16, v15, v20
	v_mul_f32_e32 v20, 0x3fb8aa3b, v17
	v_fma_f32 v21, v17, s58, -v20
	v_rndne_f32_e32 v22, v20
	v_fmac_f32_e32 v21, 0x32a5705f, v17
	v_sub_f32_e32 v20, v20, v22
	v_add_f32_e32 v20, v20, v21
	v_exp_f32_e32 v20, v20
	v_cvt_i32_f32_e32 v21, v22
	v_cmp_ngt_f32_e32 vcc, s59, v17
	v_ldexp_f32 v20, v20, v21
	s_nop 0
	v_cndmask_b32_e32 v20, 0, v20, vcc
	v_cmp_nlt_f32_e32 vcc, s60, v17
	s_nop 1
	v_cndmask_b32_e32 v17, v209, v20, vcc
	v_mul_f32_e32 v20, 0x3fb8aa3b, v18
	v_fma_f32 v21, v18, s58, -v20
	v_rndne_f32_e32 v22, v20
	v_fmac_f32_e32 v21, 0x32a5705f, v18
	v_sub_f32_e32 v20, v20, v22
	v_add_f32_e32 v20, v20, v21
	v_exp_f32_e32 v20, v20
	v_cvt_i32_f32_e32 v21, v22
	v_cmp_ngt_f32_e32 vcc, s59, v18
	v_add_f32_e32 v16, v17, v16
	v_ldexp_f32 v20, v20, v21
	v_cndmask_b32_e32 v20, 0, v20, vcc
	v_cmp_nlt_f32_e32 vcc, s60, v18
	s_nop 1
	v_cndmask_b32_e32 v18, v209, v20, vcc
	v_mul_f32_e32 v20, 0x3fb8aa3b, v19
	v_fma_f32 v21, v19, s58, -v20
	v_rndne_f32_e32 v22, v20
	v_fmac_f32_e32 v21, 0x32a5705f, v19
	v_sub_f32_e32 v20, v20, v22
	v_add_f32_e32 v20, v20, v21
	v_exp_f32_e32 v20, v20
	v_cvt_i32_f32_e32 v21, v22
	v_cmp_ngt_f32_e32 vcc, s59, v19
	v_add_f32_e32 v16, v18, v16
	v_ldexp_f32 v20, v20, v21
	v_cndmask_b32_e32 v20, 0, v20, vcc
	v_cmp_nlt_f32_e32 vcc, s60, v19
	s_nop 1
	v_cndmask_b32_e32 v19, v209, v20, vcc
	v_mul_f32_e32 v20, 0x3fb8aa3b, v14
	v_fma_f32 v21, v14, s58, -v20
	v_rndne_f32_e32 v22, v20
	v_fmac_f32_e32 v21, 0x32a5705f, v14
	v_sub_f32_e32 v20, v20, v22
	v_add_f32_e32 v20, v20, v21
	v_exp_f32_e32 v20, v20
	v_cvt_i32_f32_e32 v21, v22
	v_cmp_ngt_f32_e32 vcc, s59, v14
	v_add_f32_e32 v16, v19, v16
	v_ldexp_f32 v20, v20, v21
	v_cndmask_b32_e32 v20, 0, v20, vcc
	v_cmp_nlt_f32_e32 vcc, s60, v14
	s_nop 1
	v_cndmask_b32_e32 v14, v209, v20, vcc
	v_mul_f32_e32 v20, 0x3fb8aa3b, v13
	v_fma_f32 v21, v13, s58, -v20
	v_rndne_f32_e32 v22, v20
	v_fmac_f32_e32 v21, 0x32a5705f, v13
	v_sub_f32_e32 v20, v20, v22
	v_add_f32_e32 v20, v20, v21
	v_exp_f32_e32 v20, v20
	v_cvt_i32_f32_e32 v21, v22
	v_cmp_ngt_f32_e32 vcc, s59, v13
	v_add_f32_e32 v16, v14, v16
	v_ldexp_f32 v20, v20, v21
	v_cndmask_b32_e32 v20, 0, v20, vcc
	v_cmp_nlt_f32_e32 vcc, s60, v13
	v_rndne_f32_e32 v21, v12
	s_nop 0
	v_cndmask_b32_e32 v13, v209, v20, vcc
	v_fma_f32 v20, v10, s58, -v12
	v_fmac_f32_e32 v20, 0x32a5705f, v10
	v_sub_f32_e32 v12, v12, v21
	v_add_f32_e32 v12, v12, v20
	v_exp_f32_e32 v12, v12
	v_cvt_i32_f32_e32 v20, v21
	v_cmp_ngt_f32_e32 vcc, s59, v10
	v_add_f32_e32 v16, v13, v16
	v_ldexp_f32 v12, v12, v20
	v_cndmask_b32_e32 v12, 0, v12, vcc
	v_cmp_nlt_f32_e32 vcc, s60, v10
	s_nop 1
	v_cndmask_b32_e32 v12, v209, v12, vcc
	v_add_f32_e32 v10, v12, v16
	v_add_f32_e32 v10, v9, v10
	v_div_scale_f32 v16, s[62:63], v10, v10, v9
	v_rcp_f32_e32 v20, v16
	s_nop 0
	v_fma_f32 v21, -v16, v20, 1.0
	v_fmac_f32_e32 v20, v21, v20
	v_div_scale_f32 v21, vcc, v9, v10, v9
	v_mul_f32_e32 v22, v21, v20
	v_fma_f32 v23, -v16, v22, v21
	v_fmac_f32_e32 v22, v23, v20
	v_fma_f32 v16, -v16, v22, v21
	v_div_fmas_f32 v16, v16, v20, v22
	v_div_fixup_f32 v9, v16, v10, v9
	v_div_scale_f32 v16, s[62:63], v10, v10, v12
	v_rcp_f32_e32 v20, v16
	s_nop 0
	v_fma_f32 v21, -v16, v20, 1.0
	v_fmac_f32_e32 v20, v21, v20
	v_div_scale_f32 v21, vcc, v12, v10, v12
	v_mul_f32_e32 v22, v21, v20
	v_fma_f32 v23, -v16, v22, v21
	v_fmac_f32_e32 v22, v23, v20
	v_fma_f32 v16, -v16, v22, v21
	v_div_fmas_f32 v16, v16, v20, v22
	v_div_fixup_f32 v12, v16, v10, v12
	v_div_scale_f32 v16, s[62:63], v10, v10, v13
	v_rcp_f32_e32 v20, v16
	s_nop 0
	v_fma_f32 v21, -v16, v20, 1.0
	v_fmac_f32_e32 v20, v21, v20
	v_div_scale_f32 v21, vcc, v13, v10, v13
	v_mul_f32_e32 v22, v21, v20
	v_fma_f32 v23, -v16, v22, v21
	v_fmac_f32_e32 v22, v23, v20
	v_fma_f32 v16, -v16, v22, v21
	v_div_fmas_f32 v16, v16, v20, v22
	v_div_fixup_f32 v13, v16, v10, v13
	v_div_scale_f32 v16, s[62:63], v10, v10, v14
	v_rcp_f32_e32 v20, v16
	s_nop 0
	v_fma_f32 v21, -v16, v20, 1.0
	v_fmac_f32_e32 v20, v21, v20
	v_div_scale_f32 v21, vcc, v14, v10, v14
	v_mul_f32_e32 v22, v21, v20
	v_fma_f32 v23, -v16, v22, v21
	v_fmac_f32_e32 v22, v23, v20
	v_fma_f32 v16, -v16, v22, v21
	v_div_fmas_f32 v16, v16, v20, v22
	v_div_fixup_f32 v14, v16, v10, v14
	v_div_scale_f32 v16, s[62:63], v10, v10, v19
	v_rcp_f32_e32 v20, v16
	s_nop 0
	v_fma_f32 v21, -v16, v20, 1.0
	v_fmac_f32_e32 v20, v21, v20
	v_div_scale_f32 v21, vcc, v19, v10, v19
	v_mul_f32_e32 v22, v21, v20
	v_fma_f32 v23, -v16, v22, v21
	v_fmac_f32_e32 v22, v23, v20
	v_fma_f32 v16, -v16, v22, v21
	v_div_fmas_f32 v16, v16, v20, v22
	v_div_fixup_f32 v16, v16, v10, v19
	v_div_scale_f32 v19, s[62:63], v10, v10, v18
	v_rcp_f32_e32 v20, v19
	s_nop 0
	v_fma_f32 v21, -v19, v20, 1.0
	v_fmac_f32_e32 v20, v21, v20
	v_div_scale_f32 v21, vcc, v18, v10, v18
	v_mul_f32_e32 v22, v21, v20
	v_fma_f32 v23, -v19, v22, v21
	v_fmac_f32_e32 v22, v23, v20
	v_fma_f32 v19, -v19, v22, v21
	v_div_fmas_f32 v19, v19, v20, v22
	v_div_fixup_f32 v18, v19, v10, v18
	v_div_scale_f32 v19, s[62:63], v10, v10, v17
	v_rcp_f32_e32 v20, v19
	s_nop 0
	v_fma_f32 v21, -v19, v20, 1.0
	v_fmac_f32_e32 v20, v21, v20
	v_div_scale_f32 v21, vcc, v17, v10, v17
	v_mul_f32_e32 v22, v21, v20
	v_fma_f32 v23, -v19, v22, v21
	v_fmac_f32_e32 v22, v23, v20
	v_fma_f32 v19, -v19, v22, v21
	v_div_fmas_f32 v19, v19, v20, v22
	v_div_fixup_f32 v17, v19, v10, v17
	v_div_scale_f32 v19, s[62:63], v10, v10, v15
	v_rcp_f32_e32 v20, v19
	s_nop 0
	v_fma_f32 v21, -v19, v20, 1.0
	v_fmac_f32_e32 v20, v21, v20
	v_div_scale_f32 v21, vcc, v15, v10, v15
	v_mul_f32_e32 v22, v21, v20
	v_fma_f32 v23, -v19, v22, v21
	v_fmac_f32_e32 v22, v23, v20
	v_fma_f32 v19, -v19, v22, v21
	v_div_fmas_f32 v19, v19, v20, v22
	v_div_fixup_f32 v15, v19, v10, v15
	v_div_scale_f32 v19, s[62:63], v10, v10, v11
	v_rcp_f32_e32 v20, v19
	s_nop 0
	v_fma_f32 v21, -v19, v20, 1.0
	v_fmac_f32_e32 v20, v21, v20
	v_div_scale_f32 v21, vcc, v11, v10, v11
	v_mul_f32_e32 v22, v21, v20
	v_fma_f32 v23, -v19, v22, v21
	v_fmac_f32_e32 v22, v23, v20
	v_fma_f32 v19, -v19, v22, v21
	v_div_fmas_f32 v19, v19, v20, v22
	v_div_fixup_f32 v11, v19, v10, v11
	v_div_scale_f32 v19, s[62:63], v10, v10, v8
	v_rcp_f32_e32 v20, v19
	s_nop 0
	v_fma_f32 v21, -v19, v20, 1.0
	v_fmac_f32_e32 v20, v21, v20
	v_div_scale_f32 v21, vcc, v8, v10, v8
	v_mul_f32_e32 v22, v21, v20
	v_fma_f32 v23, -v19, v22, v21
	v_fmac_f32_e32 v22, v23, v20
	v_fma_f32 v19, -v19, v22, v21
	v_div_fmas_f32 v19, v19, v20, v22
	v_div_fixup_f32 v8, v19, v10, v8
	v_div_scale_f32 v19, s[62:63], v10, v10, v7
	v_rcp_f32_e32 v20, v19
	s_nop 0
	v_fma_f32 v21, -v19, v20, 1.0
	v_fmac_f32_e32 v20, v21, v20
	v_div_scale_f32 v21, vcc, v7, v10, v7
	v_mul_f32_e32 v22, v21, v20
	v_fma_f32 v23, -v19, v22, v21
	v_fmac_f32_e32 v22, v23, v20
	v_fma_f32 v19, -v19, v22, v21
	v_div_fmas_f32 v19, v19, v20, v22
	v_div_fixup_f32 v7, v19, v10, v7
	v_div_scale_f32 v19, s[62:63], v10, v10, v6
	v_rcp_f32_e32 v20, v19
	s_nop 0
	v_fma_f32 v21, -v19, v20, 1.0
	v_fmac_f32_e32 v20, v21, v20
	v_div_scale_f32 v21, vcc, v6, v10, v6
	v_mul_f32_e32 v22, v21, v20
	v_fma_f32 v23, -v19, v22, v21
	v_fmac_f32_e32 v22, v23, v20
	v_fma_f32 v19, -v19, v22, v21
	v_div_fmas_f32 v19, v19, v20, v22
	v_div_fixup_f32 v6, v19, v10, v6
	v_div_scale_f32 v19, s[62:63], v10, v10, v5
	v_rcp_f32_e32 v20, v19
	s_nop 0
	v_fma_f32 v21, -v19, v20, 1.0
	v_fmac_f32_e32 v20, v21, v20
	v_div_scale_f32 v21, vcc, v5, v10, v5
	v_mul_f32_e32 v22, v21, v20
	v_fma_f32 v23, -v19, v22, v21
	v_fmac_f32_e32 v22, v23, v20
	v_fma_f32 v19, -v19, v22, v21
	v_div_fmas_f32 v19, v19, v20, v22
	v_div_fixup_f32 v5, v19, v10, v5
	v_div_scale_f32 v19, s[62:63], v10, v10, v4
	v_rcp_f32_e32 v20, v19
	s_nop 0
	v_fma_f32 v21, -v19, v20, 1.0
	v_fmac_f32_e32 v20, v21, v20
	v_div_scale_f32 v21, vcc, v4, v10, v4
	v_mul_f32_e32 v22, v21, v20
	v_fma_f32 v23, -v19, v22, v21
	v_fmac_f32_e32 v22, v23, v20
	v_fma_f32 v19, -v19, v22, v21
	v_div_fmas_f32 v19, v19, v20, v22
	v_div_fixup_f32 v4, v19, v10, v4
	v_div_scale_f32 v19, s[62:63], v10, v10, v3
	v_rcp_f32_e32 v20, v19
	s_nop 0
	v_fma_f32 v21, -v19, v20, 1.0
	v_fmac_f32_e32 v20, v21, v20
	v_div_scale_f32 v21, vcc, v3, v10, v3
	v_mul_f32_e32 v22, v21, v20
	v_fma_f32 v23, -v19, v22, v21
	v_fmac_f32_e32 v22, v23, v20
	v_fma_f32 v19, -v19, v22, v21
	v_div_fmas_f32 v19, v19, v20, v22
	v_div_fixup_f32 v3, v19, v10, v3
	v_div_scale_f32 v19, s[62:63], v10, v10, v2
	v_rcp_f32_e32 v20, v19
	s_nop 0
	v_fma_f32 v21, -v19, v20, 1.0
	v_fmac_f32_e32 v20, v21, v20
	v_div_scale_f32 v21, vcc, v2, v10, v2
	v_mul_f32_e32 v22, v21, v20
	v_fma_f32 v23, -v19, v22, v21
	v_fmac_f32_e32 v22, v23, v20
	v_fma_f32 v19, -v19, v22, v21
	v_div_fmas_f32 v19, v19, v20, v22
	v_div_fixup_f32 v2, v19, v10, v2
	v_cndmask_b32_e64 v2, 0, v2, s[36:37]
	v_cndmask_b32_e64 v2, v2, v3, s[34:35]
	v_cndmask_b32_e64 v2, v2, v4, s[30:31]
	v_cndmask_b32_e64 v2, v2, v5, s[28:29]
	v_cndmask_b32_e64 v2, v2, v6, s[26:27]
	v_cndmask_b32_e64 v2, v2, v7, s[24:25]
	v_cndmask_b32_e64 v2, v2, v8, s[22:23]
	v_cndmask_b32_e64 v2, v2, v11, s[20:21]
	v_cndmask_b32_e64 v2, v2, v15, s[18:19]
	v_cndmask_b32_e64 v2, v2, v17, s[16:17]
	v_cndmask_b32_e64 v2, v2, v18, s[14:15]
	v_cndmask_b32_e64 v2, v2, v16, s[12:13]
	v_cndmask_b32_e64 v2, v2, v14, s[10:11]
	v_cndmask_b32_e64 v2, v2, v13, s[8:9]
	v_cndmask_b32_e64 v2, v2, v12, s[6:7]
	v_cndmask_b32_e64 v4, v2, v9, s[4:5]
	v_lshl_add_u64 v[2:3], s[40:41], 0, v[106:107]
	global_store_dword v[2:3], v4, off
	s_branch .LBB0_1364
.Lf_lat_L0:
	s_cmp_lg_u32 s1, -1
	s_cselect_b32 s52, s1, 0
	s_cselect_b32 s53, s43, 0
	s_cmp_lg_u32 s45, -1
	s_cselect_b32 s61, s45, 0
	s_cselect_b32 s62, s43, 0
	s_cmpk_lt_i32 s0, 0x4000
	s_cselect_b32 s53, s53, s42
	s_cselect_b32 s52, s52, s33
	s_waitcnt vmcnt(7) lgkmcnt(7)
	v_lshl_add_u64 v[18:19], s[40:41], 0, v[110:111]
	v_lshl_add_u64 v[118:119], s[52:53], 0, v[112:113]
	s_mov_b32 s52, 0x1b41000
	v_add_co_u32_e32 v14, vcc, s52, v18
	ds_read_b128 v[86:89], v134
	ds_read_b128 v[82:85], v134 offset:8192
	ds_read_b128 v[78:81], v134 offset:16384
	ds_read_b128 v[74:77], v134 offset:24576
	ds_read_b128 v[70:73], v134 offset:32768
	ds_read_b128 v[66:69], v134 offset:40960
	ds_read_b128 v[62:65], v134 offset:49152
	ds_read_b128 v[58:61], v134 offset:57344
	ds_read_b128 v[54:57], v135
	ds_read_b128 v[50:53], v136
	ds_read_b128 v[46:49], v137
	ds_read_b128 v[42:45], v138
	ds_read_b128 v[38:41], v139
	ds_read_b128 v[34:37], v140
	s_waitcnt vmcnt(4) lgkmcnt(14)
	ds_read_b128 v[30:33], v141
	ds_read_b128 v[26:29], v142
	v_addc_co_u32_e32 v15, vcc, 0, v19, vcc
	global_load_dwordx4 v[2:5], v[14:15], off offset:3072
	global_load_dwordx4 v[6:9], v[14:15], off offset:2048
	s_mov_b32 s52, 0x1b40000
	v_add_co_u32_e32 v94, vcc, s52, v18
	s_cselect_b32 s63, s62, s55
	s_nop 0
	v_addc_co_u32_e32 v95, vcc, 0, v19, vcc
	global_load_dwordx4 v[10:13], v[14:15], off offset:1024
	s_nop 0
	global_load_dwordx4 v[14:17], v[14:15], off
	global_load_dwordx4 v[90:93], v[94:95], off offset:1024
	global_load_dwordx4 v[102:105], v[94:95], off
	global_load_dwordx4 v[18:21], v[94:95], off offset:3072
	global_load_dwordx4 v[22:25], v[94:95], off offset:2048
	s_cselect_b32 s62, s61, s54
	v_lshl_add_u64 v[116:117], s[62:63], 0, v[112:113]
	s_mov_b32 s52, 0x800000
	v_lshl_add_u64 v[120:121], s[40:41], 0, v[108:109]
	s_waitcnt vmcnt(7)
	v_mov_b32_e32 v221, v3
	s_waitcnt vmcnt(6)
	v_mov_b32_e32 v220, v7
	v_mov_b32_e32 v218, v6
	v_mov_b32_e32 v219, v2
	v_pk_mul_f32 v[220:221], v[220:221], v[220:221]
	s_nop 0
	v_pk_fma_f32 v[218:219], v[218:219], v[218:219], v[220:221]
	v_mov_b32_e32 v220, v8
	v_mov_b32_e32 v221, v4
	v_pk_fma_f32 v[218:219], v[220:221], v[220:221], v[218:219]
	v_mov_b32_e32 v220, v9
	v_mov_b32_e32 v221, v5
	v_pk_fma_f32 v[114:115], v[220:221], v[220:221], v[218:219]
	ds_read_b128 v[98:101], v133
	s_waitcnt vmcnt(5)
	v_mov_b32_e32 v225, v11
	s_waitcnt vmcnt(4)
	v_mov_b32_e32 v224, v15
	v_mov_b32_e32 v222, v14
	v_mov_b32_e32 v223, v10
	v_pk_mul_f32 v[224:225], v[224:225], v[224:225]
	s_waitcnt vmcnt(3)
	v_mul_f32_e32 v215, v91, v91
	v_pk_fma_f32 v[222:223], v[222:223], v[222:223], v[224:225]
	v_mov_b32_e32 v224, v16
	v_mov_b32_e32 v225, v12
	v_pk_fma_f32 v[222:223], v[224:225], v[224:225], v[222:223]
	v_mov_b32_e32 v224, v17
	v_mov_b32_e32 v225, v13
	v_pk_fma_f32 v[124:125], v[224:225], v[224:225], v[222:223]
	s_nop 0
	ds_read_b128 v[94:97], v118
	ds_read_b128 v[210:213], v116
	s_waitcnt vmcnt(0) lgkmcnt(0)
	v_mul_f32_e32 v216, v103, v103
	v_fmac_f32_e32 v215, v90, v90
	v_fmac_f32_e32 v216, v102, v102
	v_fmac_f32_e32 v215, v92, v92
	v_fmac_f32_e32 v216, v104, v104
	v_fmac_f32_e32 v215, v93, v93
	v_fmac_f32_e32 v216, v105, v105
	v_mul_f32_e32 v190, v19, v19
	v_mul_f32_e32 v214, v23, v23
	v_fmac_f32_e32 v214, v22, v22
	v_fmac_f32_e32 v190, v18, v18
	v_fmac_f32_e32 v214, v24, v24
	v_fmac_f32_e32 v190, v20, v20
	v_fmac_f32_e32 v214, v25, v25
	s_waitcnt lgkmcnt(0)
	v_mov_b32_e32 v122, v210
	v_add_f32_e32 v210, v216, v215
	v_fmac_f32_e32 v190, v21, v21
	v_add_f32_e32 v210, v210, v214
	v_add_f32_e32 v190, v210, v190
	v_add_f32_e32 v124, v190, v124
	v_add_f32_e32 v124, v124, v125
	v_add_f32_e32 v114, v124, v114
	v_add_f32_e32 v114, v114, v115
	ds_bpermute_b32 v115, v1, v114
	v_mov_b32_e32 v124, v102
	v_mov_b32_e32 v125, v104
	v_mov_b32_e32 v104, v103
	v_mov_b32_e32 v123, v212
	s_waitcnt lgkmcnt(0)
	v_add_f32_e32 v114, v114, v115
	ds_bpermute_b32 v115, v128, v114
	v_mov_b32_e32 v212, v211
	v_mov_b32_e32 v210, v98
	v_mov_b32_e32 v211, v100
	v_mov_b32_e32 v100, v99
	s_waitcnt lgkmcnt(0)
	v_add_f32_e32 v114, v114, v115
	ds_bpermute_b32 v115, v129, v114
	v_pk_add_f32 v[126:127], v[122:123], 1.0 op_sel_hi:[1,0]
	v_pk_add_f32 v[122:123], v[212:213], 1.0 op_sel_hi:[1,0]
	s_waitcnt lgkmcnt(0)
	v_add_f32_e32 v114, v114, v115
	ds_bpermute_b32 v115, v130, v114
	s_waitcnt lgkmcnt(0)
	v_add_f32_e32 v114, v114, v115
	ds_bpermute_b32 v115, v131, v114
	s_waitcnt lgkmcnt(0)
	v_add_f32_e32 v114, v114, v115
	ds_bpermute_b32 v115, v132, v114
	s_waitcnt lgkmcnt(0)
	v_add_f32_e32 v114, v114, v115
	v_fmamk_f32 v114, v114, 0x3a000000, v207
	v_cmp_gt_f32_e32 vcc, s52, v114
	v_mul_f32_e32 v115, 0x4b800000, v114
	s_mov_b32 s52, 0x2ec40000
	v_cndmask_b32_e32 v114, v114, v115, vcc
	v_rsq_f32_e32 v114, v114
	s_nop 0
	v_mul_f32_e32 v115, 0x45800000, v114
	v_cndmask_b32_e32 v114, v114, v115, vcc
	v_pk_mul_f32 v[124:125], v[124:125], v[114:115] op_sel_hi:[1,0]
	v_pk_mul_f32 v[102:103], v[104:105], v[114:115] op_sel_hi:[1,0]
	v_pk_mul_f32 v[124:125], v[210:211], v[124:125]
	v_mov_b32_e32 v211, v96
	v_pk_mul_f32 v[98:99], v[100:101], v[102:103]
	v_mov_b32_e32 v96, v95
	v_mov_b32_e32 v210, v94
	v_pk_fma_f32 v[96:97], v[122:123], v[98:99], v[96:97]
	v_pk_fma_f32 v[124:125], v[126:127], v[124:125], v[210:211]
	v_fma_f32 v33, v97, v33, 0
	v_fmac_f32_e32 v33, v125, v32
	v_and_b32_sdwa v98, v97, v208 dst_sel:DWORD dst_unused:UNUSED_PAD src0_sel:WORD_1 src1_sel:DWORD
	v_fmac_f32_e32 v33, v96, v31
	v_and_b32_sdwa v94, v125, v208 dst_sel:DWORD dst_unused:UNUSED_PAD src0_sel:WORD_1 src1_sel:DWORD
	v_and_b32_sdwa v99, v96, v208 dst_sel:DWORD dst_unused:UNUSED_PAD src0_sel:WORD_1 src1_sel:DWORD
	v_add3_u32 v98, v97, v98, s57
	v_fmac_f32_e32 v33, v124, v30
	v_fma_f32 v30, v97, v29, 0
	v_and_b32_sdwa v95, v124, v208 dst_sel:DWORD dst_unused:UNUSED_PAD src0_sel:WORD_1 src1_sel:DWORD
	v_add3_u32 v94, v125, v94, s57
	v_add3_u32 v99, v96, v99, s57
	v_and_b32_e32 v98, 0xffff0000, v98
	v_fma_f32 v89, v97, v89, 0
	v_fma_f32 v85, v97, v85, 0
	v_fma_f32 v81, v97, v81, 0
	v_fma_f32 v77, v97, v77, 0
	v_fma_f32 v73, v97, v73, 0
	v_fma_f32 v69, v97, v69, 0
	v_fma_f32 v65, v97, v65, 0
	v_fma_f32 v61, v97, v61, 0
	v_fma_f32 v57, v97, v57, 0
	v_fma_f32 v53, v97, v53, 0
	v_fma_f32 v49, v97, v49, 0
	v_fma_f32 v45, v97, v45, 0
	v_fma_f32 v41, v97, v41, 0
	v_fma_f32 v37, v97, v37, 0
	v_fmac_f32_e32 v30, v125, v28
	v_add3_u32 v95, v124, v95, s57
	v_and_b32_e32 v100, 0xffff0000, v99
	v_or_b32_sdwa v99, v98, v94 dst_sel:DWORD dst_unused:UNUSED_PAD src0_sel:DWORD src1_sel:WORD_1
	v_add_co_u32_e32 v94, vcc, s52, v120
	v_fmac_f32_e32 v89, v125, v88
	v_fmac_f32_e32 v85, v125, v84
	v_fmac_f32_e32 v81, v125, v80
	v_fmac_f32_e32 v77, v125, v76
	v_fmac_f32_e32 v73, v125, v72
	v_fmac_f32_e32 v69, v125, v68
	v_fmac_f32_e32 v65, v125, v64
	v_fmac_f32_e32 v61, v125, v60
	v_fmac_f32_e32 v57, v125, v56
	v_fmac_f32_e32 v53, v125, v52
	v_fmac_f32_e32 v49, v125, v48
	v_fmac_f32_e32 v45, v125, v44
	v_fmac_f32_e32 v41, v125, v40
	v_fmac_f32_e32 v37, v125, v36
	v_fmac_f32_e32 v30, v96, v27
	v_or_b32_sdwa v98, v100, v95 dst_sel:DWORD dst_unused:UNUSED_PAD src0_sel:DWORD src1_sel:WORD_1
	v_addc_co_u32_e32 v95, vcc, 0, v121, vcc
	v_fmac_f32_e32 v89, v96, v87
	v_fmac_f32_e32 v85, v96, v83
	v_fmac_f32_e32 v81, v96, v79
	v_fmac_f32_e32 v77, v96, v75
	v_fmac_f32_e32 v73, v96, v71
	v_fmac_f32_e32 v69, v96, v67
	v_fmac_f32_e32 v65, v96, v63
	v_fmac_f32_e32 v61, v96, v59
	v_fmac_f32_e32 v57, v96, v55
	v_fmac_f32_e32 v53, v96, v51
	v_fmac_f32_e32 v49, v96, v47
	v_fmac_f32_e32 v45, v96, v43
	v_fmac_f32_e32 v41, v96, v39
	v_fmac_f32_e32 v37, v96, v35
	v_fmac_f32_e32 v30, v124, v26
	global_store_dwordx2 v[94:95], v[98:99], off
	v_fmac_f32_e32 v89, v124, v86
	v_fmac_f32_e32 v85, v124, v82
	v_fmac_f32_e32 v81, v124, v78
	v_fmac_f32_e32 v77, v124, v74
	v_fmac_f32_e32 v73, v124, v70
	v_fmac_f32_e32 v69, v124, v66
	v_fmac_f32_e32 v65, v124, v62
	v_fmac_f32_e32 v61, v124, v58
	v_fmac_f32_e32 v57, v124, v54
	v_fmac_f32_e32 v53, v124, v50
	v_fmac_f32_e32 v49, v124, v46
	v_fmac_f32_e32 v45, v124, v42
	v_fmac_f32_e32 v41, v124, v38
	v_fmac_f32_e32 v37, v124, v34
	ds_read_b128 v[96:99], v143
	ds_read_b128 v[100:103], v118 offset:1024
	ds_read_b128 v[120:123], v116 offset:1024
	v_mov_b32_e32 v26, v90
	v_mov_b32_e32 v27, v92
	v_pk_mul_f32 v[26:27], v[26:27], v[114:115] op_sel_hi:[1,0]
	s_waitcnt lgkmcnt(0)
	v_mov_b32_e32 v28, v96
	v_mov_b32_e32 v29, v98
	v_pk_mul_f32 v[26:27], v[26:27], v[28:29]
	v_mov_b32_e32 v92, v91
	v_mov_b32_e32 v98, v97
	s_waitcnt lgkmcnt(0)
	v_mov_b32_e32 v34, v100
	v_mov_b32_e32 v28, v120
	v_mov_b32_e32 v29, v122
	v_pk_add_f32 v[28:29], v[28:29], 1.0 op_sel_hi:[1,0]
	v_mov_b32_e32 v35, v102
	v_pk_fma_f32 v[26:27], v[26:27], v[28:29], v[34:35]
	v_pk_mul_f32 v[28:29], v[92:93], v[114:115] op_sel_hi:[1,0]
	ds_read_b128 v[90:93], v134 offset:1024
	v_mov_b32_e32 v122, v121
	v_pk_mul_f32 v[28:29], v[28:29], v[98:99]
	v_pk_add_f32 v[34:35], v[122:123], 1.0 op_sel_hi:[1,0]
	v_mov_b32_e32 v102, v101
	v_pk_fma_f32 v[28:29], v[28:29], v[34:35], v[102:103]
	v_and_b32_sdwa v31, v27, v208 dst_sel:DWORD dst_unused:UNUSED_PAD src0_sel:WORD_1 src1_sel:DWORD
	s_waitcnt lgkmcnt(0)
	v_fmac_f32_e32 v89, v29, v93
	v_fmac_f32_e32 v89, v27, v92
	v_fmac_f32_e32 v89, v28, v91
	v_fmac_f32_e32 v89, v26, v90
	ds_read_b128 v[90:93], v134 offset:9216
	v_and_b32_sdwa v34, v29, v208 dst_sel:DWORD dst_unused:UNUSED_PAD src0_sel:WORD_1 src1_sel:DWORD
	v_and_b32_sdwa v35, v28, v208 dst_sel:DWORD dst_unused:UNUSED_PAD src0_sel:WORD_1 src1_sel:DWORD
	v_and_b32_sdwa v32, v26, v208 dst_sel:DWORD dst_unused:UNUSED_PAD src0_sel:WORD_1 src1_sel:DWORD
	v_add3_u32 v34, v29, v34, s57
	s_waitcnt lgkmcnt(0)
	v_fmac_f32_e32 v85, v29, v93
	v_fmac_f32_e32 v85, v27, v92
	v_fmac_f32_e32 v85, v28, v91
	v_fmac_f32_e32 v85, v26, v90
	ds_read_b128 v[90:93], v134 offset:17408
	v_add3_u32 v35, v28, v35, s57
	v_add3_u32 v32, v26, v32, s57
	v_add3_u32 v31, v27, v31, s57
	v_and_b32_e32 v34, 0xffff0000, v34
	s_waitcnt lgkmcnt(0)
	v_fmac_f32_e32 v81, v29, v93
	v_fmac_f32_e32 v81, v27, v92
	v_fmac_f32_e32 v81, v28, v91
	v_fmac_f32_e32 v81, v26, v90
	ds_read_b128 v[90:93], v134 offset:25600
	v_and_b32_e32 v36, 0xffff0000, v35
	v_or_b32_sdwa v35, v34, v31 dst_sel:DWORD dst_unused:UNUSED_PAD src0_sel:DWORD src1_sel:WORD_1
	v_or_b32_sdwa v34, v36, v32 dst_sel:DWORD dst_unused:UNUSED_PAD src0_sel:DWORD src1_sel:WORD_1
	global_store_dwordx2 v[94:95], v[34:35], off offset:512
	s_waitcnt lgkmcnt(0)
	v_fmac_f32_e32 v77, v29, v93
	v_fmac_f32_e32 v77, v27, v92
	v_fmac_f32_e32 v77, v28, v91
	v_fmac_f32_e32 v77, v26, v90
	ds_read_b128 v[90:93], v134 offset:33792
	s_waitcnt lgkmcnt(0)
	v_fmac_f32_e32 v73, v29, v93
	v_fmac_f32_e32 v73, v27, v92
	v_fmac_f32_e32 v73, v28, v91
	v_fmac_f32_e32 v73, v26, v90
	ds_read_b128 v[90:93], v134 offset:41984
	s_waitcnt lgkmcnt(0)
	v_fmac_f32_e32 v69, v29, v93
	v_fmac_f32_e32 v69, v27, v92
	v_fmac_f32_e32 v69, v28, v91
	v_fmac_f32_e32 v69, v26, v90
	ds_read_b128 v[90:93], v134 offset:50176
	s_waitcnt lgkmcnt(0)
	v_fmac_f32_e32 v65, v29, v93
	v_fmac_f32_e32 v65, v27, v92
	v_fmac_f32_e32 v65, v28, v91
	v_fmac_f32_e32 v65, v26, v90
	ds_read_b128 v[90:93], v134 offset:58368
	s_waitcnt lgkmcnt(0)
	v_fmac_f32_e32 v61, v29, v93
	v_fmac_f32_e32 v61, v27, v92
	v_fmac_f32_e32 v61, v28, v91
	v_fmac_f32_e32 v61, v26, v90
	ds_read_b128 v[90:93], v144
	s_waitcnt lgkmcnt(0)
	v_fmac_f32_e32 v57, v29, v93
	v_fmac_f32_e32 v57, v27, v92
	v_fmac_f32_e32 v57, v28, v91
	v_fmac_f32_e32 v57, v26, v90
	ds_read_b128 v[90:93], v145
	s_waitcnt lgkmcnt(0)
	v_fmac_f32_e32 v53, v29, v93
	v_fmac_f32_e32 v53, v27, v92
	v_fmac_f32_e32 v53, v28, v91
	v_fmac_f32_e32 v53, v26, v90
	ds_read_b128 v[90:93], v146
	s_waitcnt lgkmcnt(0)
	v_fmac_f32_e32 v49, v29, v93
	v_fmac_f32_e32 v49, v27, v92
	v_fmac_f32_e32 v49, v28, v91
	v_fmac_f32_e32 v49, v26, v90
	ds_read_b128 v[90:93], v147
	s_waitcnt lgkmcnt(0)
	v_fmac_f32_e32 v45, v29, v93
	v_fmac_f32_e32 v45, v27, v92
	v_fmac_f32_e32 v45, v28, v91
	v_fmac_f32_e32 v45, v26, v90
	ds_read_b128 v[90:93], v148
	s_waitcnt lgkmcnt(0)
	v_fmac_f32_e32 v41, v29, v93
	v_fmac_f32_e32 v41, v27, v92
	v_fmac_f32_e32 v41, v28, v91
	v_fmac_f32_e32 v41, v26, v90
	ds_read_b128 v[90:93], v149
	s_waitcnt lgkmcnt(0)
	v_fmac_f32_e32 v37, v29, v93
	v_fmac_f32_e32 v37, v27, v92
	v_fmac_f32_e32 v37, v28, v91
	v_fmac_f32_e32 v37, v26, v90
	ds_read_b128 v[90:93], v150
	s_waitcnt lgkmcnt(0)
	v_fmac_f32_e32 v33, v29, v93
	v_fmac_f32_e32 v33, v27, v92
	v_fmac_f32_e32 v33, v28, v91
	v_fmac_f32_e32 v33, v26, v90
	ds_read_b128 v[90:93], v151
	s_waitcnt lgkmcnt(0)
	v_fmac_f32_e32 v30, v29, v93
	v_fmac_f32_e32 v30, v27, v92
	v_fmac_f32_e32 v30, v28, v91
	v_fmac_f32_e32 v30, v26, v90
	ds_read_b128 v[90:93], v152
	ds_read_b128 v[96:99], v118 offset:2048
	ds_read_b128 v[100:103], v116 offset:2048
	v_mov_b32_e32 v27, v24
	v_mov_b32_e32 v24, v23
	v_mov_b32_e32 v26, v22
	s_waitcnt lgkmcnt(0)
	v_mov_b32_e32 v29, v92
	v_pk_mul_f32 v[22:23], v[24:25], v[114:115] op_sel_hi:[1,0]
	v_mov_b32_e32 v92, v91
	v_mov_b32_e32 v28, v90
	v_pk_mul_f32 v[22:23], v[22:23], v[92:93]
	ds_read_b128 v[90:93], v134 offset:2048
	v_pk_mul_f32 v[26:27], v[26:27], v[114:115] op_sel_hi:[1,0]
	s_waitcnt lgkmcnt(0)
	v_mov_b32_e32 v35, v98
	v_pk_mul_f32 v[26:27], v[26:27], v[28:29]
	v_mov_b32_e32 v29, v102
	v_mov_b32_e32 v102, v101
	v_mov_b32_e32 v28, v100
	v_pk_add_f32 v[24:25], v[102:103], 1.0 op_sel_hi:[1,0]
	v_mov_b32_e32 v98, v97
	v_pk_add_f32 v[28:29], v[28:29], 1.0 op_sel_hi:[1,0]
	v_mov_b32_e32 v34, v96
	v_pk_fma_f32 v[22:23], v[22:23], v[24:25], v[98:99]
	v_pk_fma_f32 v[26:27], v[26:27], v[28:29], v[34:35]
	s_waitcnt lgkmcnt(0)
	v_fmac_f32_e32 v89, v23, v93
	v_fmac_f32_e32 v89, v27, v92
	v_fmac_f32_e32 v89, v22, v91
	v_fmac_f32_e32 v89, v26, v90
	ds_read_b128 v[90:93], v134 offset:10240
	v_and_b32_sdwa v25, v26, v208 dst_sel:DWORD dst_unused:UNUSED_PAD src0_sel:WORD_1 src1_sel:DWORD
	v_add3_u32 v28, v26, v25, s57
	v_and_b32_sdwa v25, v23, v208 dst_sel:DWORD dst_unused:UNUSED_PAD src0_sel:WORD_1 src1_sel:DWORD
	v_and_b32_sdwa v29, v22, v208 dst_sel:DWORD dst_unused:UNUSED_PAD src0_sel:WORD_1 src1_sel:DWORD
	s_waitcnt lgkmcnt(0)
	v_fmac_f32_e32 v85, v23, v93
	v_fmac_f32_e32 v85, v27, v92
	v_fmac_f32_e32 v85, v22, v91
	v_fmac_f32_e32 v85, v26, v90
	ds_read_b128 v[90:93], v134 offset:18432
	v_and_b32_sdwa v24, v27, v208 dst_sel:DWORD dst_unused:UNUSED_PAD src0_sel:WORD_1 src1_sel:DWORD
	v_add3_u32 v25, v23, v25, s57
	v_add3_u32 v29, v22, v29, s57
	v_add3_u32 v24, v27, v24, s57
	s_waitcnt lgkmcnt(0)
	v_fmac_f32_e32 v81, v23, v93
	v_fmac_f32_e32 v81, v27, v92
	v_fmac_f32_e32 v81, v22, v91
	v_fmac_f32_e32 v81, v26, v90
	ds_read_b128 v[90:93], v134 offset:26624
	v_and_b32_e32 v25, 0xffff0000, v25
	v_and_b32_e32 v29, 0xffff0000, v29
	v_or_b32_sdwa v25, v25, v24 dst_sel:DWORD dst_unused:UNUSED_PAD src0_sel:DWORD src1_sel:WORD_1
	v_or_b32_sdwa v24, v29, v28 dst_sel:DWORD dst_unused:UNUSED_PAD src0_sel:DWORD src1_sel:WORD_1
	s_waitcnt lgkmcnt(0)
	v_fmac_f32_e32 v77, v23, v93
	v_fmac_f32_e32 v77, v27, v92
	v_fmac_f32_e32 v77, v22, v91
	v_fmac_f32_e32 v77, v26, v90
	ds_read_b128 v[90:93], v134 offset:34816
	global_store_dwordx2 v[94:95], v[24:25], off offset:1024
	s_waitcnt lgkmcnt(0)
	v_fmac_f32_e32 v73, v23, v93
	v_fmac_f32_e32 v73, v27, v92
	v_fmac_f32_e32 v73, v22, v91
	v_fmac_f32_e32 v73, v26, v90
	ds_read_b128 v[90:93], v134 offset:43008
	s_waitcnt lgkmcnt(0)
	v_fmac_f32_e32 v69, v23, v93
	v_fmac_f32_e32 v69, v27, v92
	v_fmac_f32_e32 v69, v22, v91
	v_fmac_f32_e32 v69, v26, v90
	ds_read_b128 v[90:93], v134 offset:51200
	s_waitcnt lgkmcnt(0)
	v_fmac_f32_e32 v65, v23, v93
	v_fmac_f32_e32 v65, v27, v92
	v_fmac_f32_e32 v65, v22, v91
	v_fmac_f32_e32 v65, v26, v90
	ds_read_b128 v[90:93], v134 offset:59392
	s_waitcnt lgkmcnt(0)
	v_fmac_f32_e32 v61, v23, v93
	v_fmac_f32_e32 v61, v27, v92
	v_fmac_f32_e32 v61, v22, v91
	v_fmac_f32_e32 v61, v26, v90
	ds_read_b128 v[90:93], v153
	s_waitcnt lgkmcnt(0)
	v_fmac_f32_e32 v57, v23, v93
	v_fmac_f32_e32 v57, v27, v92
	v_fmac_f32_e32 v57, v22, v91
	v_fmac_f32_e32 v57, v26, v90
	ds_read_b128 v[90:93], v154
	s_waitcnt lgkmcnt(0)
	v_fmac_f32_e32 v53, v23, v93
	v_fmac_f32_e32 v53, v27, v92
	v_fmac_f32_e32 v53, v22, v91
	v_fmac_f32_e32 v53, v26, v90
	ds_read_b128 v[90:93], v155
	s_waitcnt lgkmcnt(0)
	v_fmac_f32_e32 v49, v23, v93
	v_fmac_f32_e32 v49, v27, v92
	v_fmac_f32_e32 v49, v22, v91
	v_fmac_f32_e32 v49, v26, v90
	ds_read_b128 v[90:93], v156
	s_waitcnt lgkmcnt(0)
	v_fmac_f32_e32 v45, v23, v93
	v_fmac_f32_e32 v45, v27, v92
	v_fmac_f32_e32 v45, v22, v91
	v_fmac_f32_e32 v45, v26, v90
	ds_read_b128 v[90:93], v157
	s_waitcnt lgkmcnt(0)
	v_fmac_f32_e32 v41, v23, v93
	v_fmac_f32_e32 v41, v27, v92
	v_fmac_f32_e32 v41, v22, v91
	v_fmac_f32_e32 v41, v26, v90
	ds_read_b128 v[90:93], v158
	s_waitcnt lgkmcnt(0)
	v_fmac_f32_e32 v37, v23, v93
	v_fmac_f32_e32 v37, v27, v92
	v_fmac_f32_e32 v37, v22, v91
	v_fmac_f32_e32 v37, v26, v90
	ds_read_b128 v[90:93], v159
	s_waitcnt lgkmcnt(0)
	v_fmac_f32_e32 v33, v23, v93
	v_fmac_f32_e32 v33, v27, v92
	v_fmac_f32_e32 v33, v22, v91
	v_fmac_f32_e32 v33, v26, v90
	ds_read_b128 v[90:93], v160
	s_waitcnt lgkmcnt(0)
	v_fmac_f32_e32 v30, v23, v93
	v_fmac_f32_e32 v30, v27, v92
	v_fmac_f32_e32 v30, v22, v91
	v_fmac_f32_e32 v30, v26, v90
	ds_read_b128 v[24:27], v161
	ds_read_b128 v[90:93], v118 offset:3072
	ds_read_b128 v[96:99], v116 offset:3072
	v_mov_b32_e32 v22, v18
	v_mov_b32_e32 v23, v20
	v_pk_mul_f32 v[22:23], v[22:23], v[114:115] op_sel_hi:[1,0]
	s_waitcnt lgkmcnt(0)
	v_mov_b32_e32 v28, v24
	v_mov_b32_e32 v29, v26
	v_pk_mul_f32 v[22:23], v[22:23], v[28:29]
	v_mov_b32_e32 v20, v19
	v_pk_mul_f32 v[18:19], v[20:21], v[114:115] op_sel_hi:[1,0]
	v_mov_b32_e32 v26, v25
	v_pk_mul_f32 v[18:19], v[18:19], v[26:27]
	s_waitcnt lgkmcnt(0)
	v_mov_b32_e32 v34, v90
	v_mov_b32_e32 v28, v96
	v_mov_b32_e32 v29, v98
	v_pk_add_f32 v[28:29], v[28:29], 1.0 op_sel_hi:[1,0]
	v_mov_b32_e32 v35, v92
	v_mov_b32_e32 v98, v97
	v_pk_fma_f32 v[22:23], v[22:23], v[28:29], v[34:35]
	v_pk_add_f32 v[20:21], v[98:99], 1.0 op_sel_hi:[1,0]
	v_mov_b32_e32 v92, v91
	v_pk_fma_f32 v[18:19], v[18:19], v[20:21], v[92:93]
	v_and_b32_sdwa v21, v22, v208 dst_sel:DWORD dst_unused:UNUSED_PAD src0_sel:WORD_1 src1_sel:DWORD
	v_add3_u32 v24, v22, v21, s57
	v_and_b32_sdwa v21, v19, v208 dst_sel:DWORD dst_unused:UNUSED_PAD src0_sel:WORD_1 src1_sel:DWORD
	v_and_b32_sdwa v25, v18, v208 dst_sel:DWORD dst_unused:UNUSED_PAD src0_sel:WORD_1 src1_sel:DWORD
	v_and_b32_sdwa v20, v23, v208 dst_sel:DWORD dst_unused:UNUSED_PAD src0_sel:WORD_1 src1_sel:DWORD
	v_add3_u32 v21, v19, v21, s57
	v_add3_u32 v25, v18, v25, s57
	v_add3_u32 v20, v23, v20, s57
	v_and_b32_e32 v21, 0xffff0000, v21
	v_and_b32_e32 v25, 0xffff0000, v25
	v_or_b32_sdwa v21, v21, v20 dst_sel:DWORD dst_unused:UNUSED_PAD src0_sel:DWORD src1_sel:WORD_1
	v_or_b32_sdwa v20, v25, v24 dst_sel:DWORD dst_unused:UNUSED_PAD src0_sel:DWORD src1_sel:WORD_1
	ds_read_b128 v[24:27], v134 offset:3072
	global_store_dwordx2 v[94:95], v[20:21], off offset:1536
	s_waitcnt lgkmcnt(0)
	v_fmac_f32_e32 v89, v19, v27
	v_fmac_f32_e32 v89, v23, v26
	v_fmac_f32_e32 v89, v18, v25
	v_fmac_f32_e32 v89, v22, v24
	ds_read_b128 v[24:27], v134 offset:11264
	s_waitcnt lgkmcnt(0)
	v_fmac_f32_e32 v85, v19, v27
	v_fmac_f32_e32 v85, v23, v26
	v_fmac_f32_e32 v85, v18, v25
	v_fmac_f32_e32 v85, v22, v24
	ds_read_b128 v[24:27], v134 offset:19456
	s_waitcnt lgkmcnt(0)
	v_fmac_f32_e32 v81, v19, v27
	v_fmac_f32_e32 v81, v23, v26
	v_fmac_f32_e32 v81, v18, v25
	v_fmac_f32_e32 v81, v22, v24
	ds_read_b128 v[24:27], v134 offset:27648
	s_waitcnt lgkmcnt(0)
	v_fmac_f32_e32 v77, v19, v27
	v_fmac_f32_e32 v77, v23, v26
	v_fmac_f32_e32 v77, v18, v25
	v_fmac_f32_e32 v77, v22, v24
	ds_read_b128 v[24:27], v134 offset:35840
	s_waitcnt lgkmcnt(0)
	v_fmac_f32_e32 v73, v19, v27
	v_fmac_f32_e32 v73, v23, v26
	v_fmac_f32_e32 v73, v18, v25
	v_fmac_f32_e32 v73, v22, v24
	ds_read_b128 v[24:27], v134 offset:44032
	s_waitcnt lgkmcnt(0)
	v_fmac_f32_e32 v69, v19, v27
	v_fmac_f32_e32 v69, v23, v26
	v_fmac_f32_e32 v69, v18, v25
	v_fmac_f32_e32 v69, v22, v24
	ds_read_b128 v[24:27], v134 offset:52224
	s_waitcnt lgkmcnt(0)
	v_fmac_f32_e32 v65, v19, v27
	v_fmac_f32_e32 v65, v23, v26
	v_fmac_f32_e32 v65, v18, v25
	v_fmac_f32_e32 v65, v22, v24
	ds_read_b128 v[24:27], v134 offset:60416
	s_waitcnt lgkmcnt(0)
	v_fmac_f32_e32 v61, v19, v27
	v_fmac_f32_e32 v61, v23, v26
	v_fmac_f32_e32 v61, v18, v25
	v_fmac_f32_e32 v61, v22, v24
	ds_read_b128 v[24:27], v162
	s_waitcnt lgkmcnt(0)
	v_fmac_f32_e32 v57, v19, v27
	v_fmac_f32_e32 v57, v23, v26
	v_fmac_f32_e32 v57, v18, v25
	v_fmac_f32_e32 v57, v22, v24
	ds_read_b128 v[24:27], v163
	s_waitcnt lgkmcnt(0)
	v_fmac_f32_e32 v53, v19, v27
	v_fmac_f32_e32 v53, v23, v26
	v_fmac_f32_e32 v53, v18, v25
	v_fmac_f32_e32 v53, v22, v24
	ds_read_b128 v[24:27], v164
	s_waitcnt lgkmcnt(0)
	v_fmac_f32_e32 v49, v19, v27
	v_fmac_f32_e32 v49, v23, v26
	v_fmac_f32_e32 v49, v18, v25
	v_fmac_f32_e32 v49, v22, v24
	ds_read_b128 v[24:27], v165
	s_waitcnt lgkmcnt(0)
	v_fmac_f32_e32 v45, v19, v27
	v_fmac_f32_e32 v45, v23, v26
	v_fmac_f32_e32 v45, v18, v25
	v_fmac_f32_e32 v45, v22, v24
	ds_read_b128 v[24:27], v166
	s_waitcnt lgkmcnt(0)
	v_fmac_f32_e32 v41, v19, v27
	v_fmac_f32_e32 v41, v23, v26
	v_fmac_f32_e32 v41, v18, v25
	v_fmac_f32_e32 v41, v22, v24
	ds_read_b128 v[24:27], v167
	s_waitcnt lgkmcnt(0)
	v_fmac_f32_e32 v37, v19, v27
	v_fmac_f32_e32 v37, v23, v26
	v_fmac_f32_e32 v37, v18, v25
	v_fmac_f32_e32 v37, v22, v24
	ds_read_b128 v[24:27], v168
	s_waitcnt lgkmcnt(0)
	v_fmac_f32_e32 v33, v19, v27
	v_fmac_f32_e32 v33, v23, v26
	v_fmac_f32_e32 v33, v18, v25
	v_fmac_f32_e32 v33, v22, v24
	ds_read_b128 v[24:27], v169
	s_waitcnt lgkmcnt(0)
	v_fmac_f32_e32 v30, v19, v27
	v_fmac_f32_e32 v30, v23, v26
	v_fmac_f32_e32 v30, v18, v25
	v_fmac_f32_e32 v30, v22, v24
	v_add_co_u32_e32 v18, vcc, s56, v118
	ds_read_b128 v[24:27], v170
	s_nop 0
	v_addc_co_u32_e32 v19, vcc, 0, v119, vcc
	v_add_co_u32_e32 v20, vcc, s56, v116
	ds_read_b128 v[90:93], v18
	s_nop 0
	v_addc_co_u32_e32 v21, vcc, 0, v117, vcc
	ds_read_b128 v[96:99], v20
	v_mov_b32_e32 v22, v14
	v_mov_b32_e32 v23, v16
	v_pk_mul_f32 v[22:23], v[22:23], v[114:115] op_sel_hi:[1,0]
	s_waitcnt lgkmcnt(0)
	v_mov_b32_e32 v28, v24
	v_mov_b32_e32 v29, v26
	v_pk_mul_f32 v[22:23], v[22:23], v[28:29]
	v_mov_b32_e32 v16, v15
	v_pk_mul_f32 v[14:15], v[16:17], v[114:115] op_sel_hi:[1,0]
	v_mov_b32_e32 v26, v25
	v_pk_mul_f32 v[14:15], v[14:15], v[26:27]
	s_waitcnt lgkmcnt(0)
	v_mov_b32_e32 v34, v90
	v_mov_b32_e32 v35, v92
	v_mov_b32_e32 v92, v91
	v_mov_b32_e32 v28, v96
	v_mov_b32_e32 v29, v98
	v_pk_add_f32 v[28:29], v[28:29], 1.0 op_sel_hi:[1,0]
	v_mov_b32_e32 v98, v97
	v_pk_fma_f32 v[22:23], v[22:23], v[28:29], v[34:35]
	v_pk_add_f32 v[16:17], v[98:99], 1.0 op_sel_hi:[1,0]
	s_nop 0
	v_pk_fma_f32 v[14:15], v[14:15], v[16:17], v[92:93]
	v_and_b32_sdwa v17, v22, v208 dst_sel:DWORD dst_unused:UNUSED_PAD src0_sel:WORD_1 src1_sel:DWORD
	v_add3_u32 v24, v22, v17, s57
	v_and_b32_sdwa v17, v15, v208 dst_sel:DWORD dst_unused:UNUSED_PAD src0_sel:WORD_1 src1_sel:DWORD
	v_and_b32_sdwa v25, v14, v208 dst_sel:DWORD dst_unused:UNUSED_PAD src0_sel:WORD_1 src1_sel:DWORD
	v_and_b32_sdwa v16, v23, v208 dst_sel:DWORD dst_unused:UNUSED_PAD src0_sel:WORD_1 src1_sel:DWORD
	v_add3_u32 v17, v15, v17, s57
	v_add3_u32 v25, v14, v25, s57
	v_add3_u32 v16, v23, v16, s57
	v_and_b32_e32 v17, 0xffff0000, v17
	v_and_b32_e32 v25, 0xffff0000, v25
	v_or_b32_sdwa v17, v17, v16 dst_sel:DWORD dst_unused:UNUSED_PAD src0_sel:DWORD src1_sel:WORD_1
	v_or_b32_sdwa v16, v25, v24 dst_sel:DWORD dst_unused:UNUSED_PAD src0_sel:DWORD src1_sel:WORD_1
	ds_read_b128 v[24:27], v134 offset:4096
	global_store_dwordx2 v[94:95], v[16:17], off offset:2048
	s_waitcnt lgkmcnt(0)
	v_fmac_f32_e32 v89, v15, v27
	v_fmac_f32_e32 v89, v23, v26
	v_fmac_f32_e32 v89, v14, v25
	v_fmac_f32_e32 v89, v22, v24
	ds_read_b128 v[24:27], v134 offset:12288
	s_waitcnt lgkmcnt(0)
	v_fmac_f32_e32 v85, v15, v27
	v_fmac_f32_e32 v85, v23, v26
	v_fmac_f32_e32 v85, v14, v25
	v_fmac_f32_e32 v85, v22, v24
	ds_read_b128 v[24:27], v134 offset:20480
	s_waitcnt lgkmcnt(0)
	v_fmac_f32_e32 v81, v15, v27
	v_fmac_f32_e32 v81, v23, v26
	v_fmac_f32_e32 v81, v14, v25
	v_fmac_f32_e32 v81, v22, v24
	ds_read_b128 v[24:27], v134 offset:28672
	s_waitcnt lgkmcnt(0)
	v_fmac_f32_e32 v77, v15, v27
	v_fmac_f32_e32 v77, v23, v26
	v_fmac_f32_e32 v77, v14, v25
	v_fmac_f32_e32 v77, v22, v24
	ds_read_b128 v[24:27], v134 offset:36864
	s_waitcnt lgkmcnt(0)
	v_fmac_f32_e32 v73, v15, v27
	v_fmac_f32_e32 v73, v23, v26
	v_fmac_f32_e32 v73, v14, v25
	v_fmac_f32_e32 v73, v22, v24
	ds_read_b128 v[24:27], v134 offset:45056
	s_waitcnt lgkmcnt(0)
	v_fmac_f32_e32 v69, v15, v27
	v_fmac_f32_e32 v69, v23, v26
	v_fmac_f32_e32 v69, v14, v25
	v_fmac_f32_e32 v69, v22, v24
	ds_read_b128 v[24:27], v134 offset:53248
	s_waitcnt lgkmcnt(0)
	v_fmac_f32_e32 v65, v15, v27
	v_fmac_f32_e32 v65, v23, v26
	v_fmac_f32_e32 v65, v14, v25
	v_fmac_f32_e32 v65, v22, v24
	ds_read_b128 v[24:27], v134 offset:61440
	s_waitcnt lgkmcnt(0)
	v_fmac_f32_e32 v61, v15, v27
	v_fmac_f32_e32 v61, v23, v26
	v_fmac_f32_e32 v61, v14, v25
	v_fmac_f32_e32 v61, v22, v24
	ds_read_b128 v[24:27], v171
	s_waitcnt lgkmcnt(0)
	v_fmac_f32_e32 v57, v15, v27
	v_fmac_f32_e32 v57, v23, v26
	v_fmac_f32_e32 v57, v14, v25
	v_fmac_f32_e32 v57, v22, v24
	ds_read_b128 v[24:27], v172
	s_waitcnt lgkmcnt(0)
	v_fmac_f32_e32 v53, v15, v27
	v_fmac_f32_e32 v53, v23, v26
	v_fmac_f32_e32 v53, v14, v25
	v_fmac_f32_e32 v53, v22, v24
	ds_read_b128 v[24:27], v173
	s_waitcnt lgkmcnt(0)
	v_fmac_f32_e32 v49, v15, v27
	v_fmac_f32_e32 v49, v23, v26
	v_fmac_f32_e32 v49, v14, v25
	v_fmac_f32_e32 v49, v22, v24
	ds_read_b128 v[24:27], v174
	s_waitcnt lgkmcnt(0)
	v_fmac_f32_e32 v45, v15, v27
	v_fmac_f32_e32 v45, v23, v26
	v_fmac_f32_e32 v45, v14, v25
	v_fmac_f32_e32 v45, v22, v24
	ds_read_b128 v[24:27], v175
	s_waitcnt lgkmcnt(0)
	v_fmac_f32_e32 v41, v15, v27
	v_fmac_f32_e32 v41, v23, v26
	v_fmac_f32_e32 v41, v14, v25
	v_fmac_f32_e32 v41, v22, v24
	ds_read_b128 v[24:27], v176
	s_waitcnt lgkmcnt(0)
	v_fmac_f32_e32 v37, v15, v27
	v_fmac_f32_e32 v37, v23, v26
	v_fmac_f32_e32 v37, v14, v25
	v_fmac_f32_e32 v37, v22, v24
	ds_read_b128 v[24:27], v177
	s_waitcnt lgkmcnt(0)
	v_fmac_f32_e32 v33, v15, v27
	v_fmac_f32_e32 v33, v23, v26
	v_fmac_f32_e32 v33, v14, v25
	v_fmac_f32_e32 v33, v22, v24
	ds_read_b128 v[24:27], v178
	s_waitcnt lgkmcnt(0)
	v_fmac_f32_e32 v30, v15, v27
	v_fmac_f32_e32 v30, v23, v26
	v_fmac_f32_e32 v30, v14, v25
	v_fmac_f32_e32 v30, v22, v24
	ds_read_b128 v[22:25], v179
	ds_read_b128 v[26:29], v18 offset:1024
	ds_read_b128 v[90:93], v20 offset:1024
	v_mov_b32_e32 v15, v12
	v_mov_b32_e32 v12, v11
	v_mov_b32_e32 v14, v10
	s_waitcnt lgkmcnt(0)
	v_mov_b32_e32 v17, v24
	v_pk_mul_f32 v[10:11], v[12:13], v[114:115] op_sel_hi:[1,0]
	v_mov_b32_e32 v24, v23
	v_mov_b32_e32 v16, v22
	v_pk_mul_f32 v[10:11], v[10:11], v[24:25]
	ds_read_b128 v[22:25], v134 offset:5120
	v_pk_mul_f32 v[14:15], v[14:15], v[114:115] op_sel_hi:[1,0]
	s_waitcnt lgkmcnt(0)
	v_mov_b32_e32 v35, v28
	v_pk_mul_f32 v[14:15], v[14:15], v[16:17]
	v_mov_b32_e32 v17, v92
	v_mov_b32_e32 v92, v91
	v_mov_b32_e32 v16, v90
	v_pk_add_f32 v[12:13], v[92:93], 1.0 op_sel_hi:[1,0]
	v_mov_b32_e32 v28, v27
	v_pk_add_f32 v[16:17], v[16:17], 1.0 op_sel_hi:[1,0]
	v_mov_b32_e32 v34, v26
	v_pk_fma_f32 v[10:11], v[10:11], v[12:13], v[28:29]
	v_pk_fma_f32 v[14:15], v[14:15], v[16:17], v[34:35]
	s_waitcnt lgkmcnt(0)
	v_fmac_f32_e32 v89, v11, v25
	v_fmac_f32_e32 v89, v15, v24
	v_fmac_f32_e32 v89, v10, v23
	v_fmac_f32_e32 v89, v14, v22
	ds_read_b128 v[22:25], v134 offset:13312
	v_and_b32_sdwa v13, v14, v208 dst_sel:DWORD dst_unused:UNUSED_PAD src0_sel:WORD_1 src1_sel:DWORD
	v_add3_u32 v16, v14, v13, s57
	v_and_b32_sdwa v13, v11, v208 dst_sel:DWORD dst_unused:UNUSED_PAD src0_sel:WORD_1 src1_sel:DWORD
	v_and_b32_sdwa v17, v10, v208 dst_sel:DWORD dst_unused:UNUSED_PAD src0_sel:WORD_1 src1_sel:DWORD
	s_waitcnt lgkmcnt(0)
	v_fmac_f32_e32 v85, v11, v25
	v_fmac_f32_e32 v85, v15, v24
	v_fmac_f32_e32 v85, v10, v23
	v_fmac_f32_e32 v85, v14, v22
	ds_read_b128 v[22:25], v134 offset:21504
	v_and_b32_sdwa v12, v15, v208 dst_sel:DWORD dst_unused:UNUSED_PAD src0_sel:WORD_1 src1_sel:DWORD
	v_add3_u32 v13, v11, v13, s57
	v_add3_u32 v17, v10, v17, s57
	v_add3_u32 v12, v15, v12, s57
	s_waitcnt lgkmcnt(0)
	v_fmac_f32_e32 v81, v11, v25
	v_fmac_f32_e32 v81, v15, v24
	v_fmac_f32_e32 v81, v10, v23
	v_fmac_f32_e32 v81, v14, v22
	ds_read_b128 v[22:25], v134 offset:29696
	v_and_b32_e32 v13, 0xffff0000, v13
	v_and_b32_e32 v17, 0xffff0000, v17
	v_or_b32_sdwa v13, v13, v12 dst_sel:DWORD dst_unused:UNUSED_PAD src0_sel:DWORD src1_sel:WORD_1
	v_or_b32_sdwa v12, v17, v16 dst_sel:DWORD dst_unused:UNUSED_PAD src0_sel:DWORD src1_sel:WORD_1
	s_waitcnt lgkmcnt(0)
	v_fmac_f32_e32 v77, v11, v25
	v_fmac_f32_e32 v77, v15, v24
	v_fmac_f32_e32 v77, v10, v23
	v_fmac_f32_e32 v77, v14, v22
	ds_read_b128 v[22:25], v134 offset:37888
	global_store_dwordx2 v[94:95], v[12:13], off offset:2560
	s_waitcnt lgkmcnt(0)
	v_fmac_f32_e32 v73, v11, v25
	v_fmac_f32_e32 v73, v15, v24
	v_fmac_f32_e32 v73, v10, v23
	v_fmac_f32_e32 v73, v14, v22
	ds_read_b128 v[22:25], v134 offset:46080
	s_waitcnt lgkmcnt(0)
	v_fmac_f32_e32 v69, v11, v25
	v_fmac_f32_e32 v69, v15, v24
	v_fmac_f32_e32 v69, v10, v23
	v_fmac_f32_e32 v69, v14, v22
	ds_read_b128 v[22:25], v134 offset:54272
	s_waitcnt lgkmcnt(0)
	v_fmac_f32_e32 v65, v11, v25
	v_fmac_f32_e32 v65, v15, v24
	v_fmac_f32_e32 v65, v10, v23
	v_fmac_f32_e32 v65, v14, v22
	ds_read_b128 v[22:25], v134 offset:62464
	s_waitcnt lgkmcnt(0)
	v_fmac_f32_e32 v61, v11, v25
	v_fmac_f32_e32 v61, v15, v24
	v_fmac_f32_e32 v61, v10, v23
	v_fmac_f32_e32 v61, v14, v22
	ds_read_b128 v[22:25], v180
	s_waitcnt lgkmcnt(0)
	v_fmac_f32_e32 v57, v11, v25
	v_fmac_f32_e32 v57, v15, v24
	v_fmac_f32_e32 v57, v10, v23
	v_fmac_f32_e32 v57, v14, v22
	ds_read_b128 v[22:25], v181
	s_waitcnt lgkmcnt(0)
	v_fmac_f32_e32 v53, v11, v25
	v_fmac_f32_e32 v53, v15, v24
	v_fmac_f32_e32 v53, v10, v23
	v_fmac_f32_e32 v53, v14, v22
	ds_read_b128 v[22:25], v182
	s_waitcnt lgkmcnt(0)
	v_fmac_f32_e32 v49, v11, v25
	v_fmac_f32_e32 v49, v15, v24
	v_fmac_f32_e32 v49, v10, v23
	v_fmac_f32_e32 v49, v14, v22
	ds_read_b128 v[22:25], v183
	s_waitcnt lgkmcnt(0)
	v_fmac_f32_e32 v45, v11, v25
	v_fmac_f32_e32 v45, v15, v24
	v_fmac_f32_e32 v45, v10, v23
	v_fmac_f32_e32 v45, v14, v22
	ds_read_b128 v[22:25], v184
	s_waitcnt lgkmcnt(0)
	v_fmac_f32_e32 v41, v11, v25
	v_fmac_f32_e32 v41, v15, v24
	v_fmac_f32_e32 v41, v10, v23
	v_fmac_f32_e32 v41, v14, v22
	ds_read_b128 v[22:25], v185
	s_waitcnt lgkmcnt(0)
	v_fmac_f32_e32 v37, v11, v25
	v_fmac_f32_e32 v37, v15, v24
	v_fmac_f32_e32 v37, v10, v23
	v_fmac_f32_e32 v37, v14, v22
	ds_read_b128 v[22:25], v186
	s_waitcnt lgkmcnt(0)
	v_fmac_f32_e32 v33, v11, v25
	v_fmac_f32_e32 v33, v15, v24
	v_fmac_f32_e32 v33, v10, v23
	v_fmac_f32_e32 v33, v14, v22
	ds_read_b128 v[22:25], v187
	s_waitcnt lgkmcnt(0)
	v_fmac_f32_e32 v30, v11, v25
	v_fmac_f32_e32 v30, v15, v24
	v_fmac_f32_e32 v30, v10, v23
	v_fmac_f32_e32 v30, v14, v22
	ds_read_b128 v[12:15], v188
	ds_read_b128 v[22:25], v18 offset:2048
	ds_read_b128 v[26:29], v20 offset:2048
	v_mov_b32_e32 v10, v6
	v_mov_b32_e32 v11, v8
	v_pk_mul_f32 v[10:11], v[10:11], v[114:115] op_sel_hi:[1,0]
	s_waitcnt lgkmcnt(0)
	v_mov_b32_e32 v16, v12
	v_mov_b32_e32 v17, v14
	v_pk_mul_f32 v[10:11], v[10:11], v[16:17]
	v_mov_b32_e32 v8, v7
	v_pk_mul_f32 v[6:7], v[8:9], v[114:115] op_sel_hi:[1,0]
	v_mov_b32_e32 v14, v13
	v_pk_mul_f32 v[6:7], v[6:7], v[14:15]
	s_waitcnt lgkmcnt(0)
	v_mov_b32_e32 v34, v22
	v_mov_b32_e32 v16, v26
	v_mov_b32_e32 v17, v28
	v_pk_add_f32 v[16:17], v[16:17], 1.0 op_sel_hi:[1,0]
	v_mov_b32_e32 v35, v24
	v_mov_b32_e32 v28, v27
	v_pk_fma_f32 v[10:11], v[10:11], v[16:17], v[34:35]
	v_pk_add_f32 v[8:9], v[28:29], 1.0 op_sel_hi:[1,0]
	v_mov_b32_e32 v24, v23
	v_pk_fma_f32 v[6:7], v[6:7], v[8:9], v[24:25]
	v_and_b32_sdwa v9, v10, v208 dst_sel:DWORD dst_unused:UNUSED_PAD src0_sel:WORD_1 src1_sel:DWORD
	v_add3_u32 v12, v10, v9, s57
	v_and_b32_sdwa v9, v7, v208 dst_sel:DWORD dst_unused:UNUSED_PAD src0_sel:WORD_1 src1_sel:DWORD
	v_and_b32_sdwa v13, v6, v208 dst_sel:DWORD dst_unused:UNUSED_PAD src0_sel:WORD_1 src1_sel:DWORD
	v_and_b32_sdwa v8, v11, v208 dst_sel:DWORD dst_unused:UNUSED_PAD src0_sel:WORD_1 src1_sel:DWORD
	v_add3_u32 v9, v7, v9, s57
	v_add3_u32 v13, v6, v13, s57
	v_add3_u32 v8, v11, v8, s57
	v_and_b32_e32 v9, 0xffff0000, v9
	v_and_b32_e32 v13, 0xffff0000, v13
	v_or_b32_sdwa v9, v9, v8 dst_sel:DWORD dst_unused:UNUSED_PAD src0_sel:DWORD src1_sel:WORD_1
	v_or_b32_sdwa v8, v13, v12 dst_sel:DWORD dst_unused:UNUSED_PAD src0_sel:DWORD src1_sel:WORD_1
	ds_read_b128 v[12:15], v134 offset:6144
	global_store_dwordx2 v[94:95], v[8:9], off offset:3072
	s_waitcnt lgkmcnt(0)
	v_fmac_f32_e32 v89, v7, v15
	v_fmac_f32_e32 v89, v11, v14
	v_fmac_f32_e32 v89, v6, v13
	v_fmac_f32_e32 v89, v10, v12
	ds_read_b128 v[12:15], v134 offset:14336
	s_waitcnt lgkmcnt(0)
	v_fmac_f32_e32 v85, v7, v15
	v_fmac_f32_e32 v85, v11, v14
	v_fmac_f32_e32 v85, v6, v13
	v_fmac_f32_e32 v85, v10, v12
	ds_read_b128 v[12:15], v134 offset:22528
	s_waitcnt lgkmcnt(0)
	v_fmac_f32_e32 v81, v7, v15
	v_fmac_f32_e32 v81, v11, v14
	v_fmac_f32_e32 v81, v6, v13
	v_fmac_f32_e32 v81, v10, v12
	ds_read_b128 v[12:15], v134 offset:30720
	s_waitcnt lgkmcnt(0)
	v_fmac_f32_e32 v77, v7, v15
	v_fmac_f32_e32 v77, v11, v14
	v_fmac_f32_e32 v77, v6, v13
	v_fmac_f32_e32 v77, v10, v12
	ds_read_b128 v[12:15], v134 offset:38912
	s_waitcnt lgkmcnt(0)
	v_fmac_f32_e32 v73, v7, v15
	v_fmac_f32_e32 v73, v11, v14
	v_fmac_f32_e32 v73, v6, v13
	v_fmac_f32_e32 v73, v10, v12
	ds_read_b128 v[12:15], v134 offset:47104
	s_waitcnt lgkmcnt(0)
	v_fmac_f32_e32 v69, v7, v15
	v_fmac_f32_e32 v69, v11, v14
	v_fmac_f32_e32 v69, v6, v13
	v_fmac_f32_e32 v69, v10, v12
	ds_read_b128 v[12:15], v134 offset:55296
	s_waitcnt lgkmcnt(0)
	v_fmac_f32_e32 v65, v7, v15
	v_fmac_f32_e32 v65, v11, v14
	v_fmac_f32_e32 v65, v6, v13
	v_fmac_f32_e32 v65, v10, v12
	ds_read_b128 v[12:15], v134 offset:63488
	s_waitcnt lgkmcnt(0)
	v_fmac_f32_e32 v61, v7, v15
	v_fmac_f32_e32 v61, v11, v14
	v_fmac_f32_e32 v61, v6, v13
	v_fmac_f32_e32 v61, v10, v12
	ds_read_b128 v[12:15], v189
	s_waitcnt lgkmcnt(0)
	v_fmac_f32_e32 v57, v7, v15
	v_fmac_f32_e32 v57, v11, v14
	v_fmac_f32_e32 v57, v6, v13
	v_fmac_f32_e32 v57, v10, v12
	ds_read_b128 v[12:15], v191
	s_waitcnt lgkmcnt(0)
	v_fmac_f32_e32 v53, v7, v15
	v_fmac_f32_e32 v53, v11, v14
	v_fmac_f32_e32 v53, v6, v13
	v_fmac_f32_e32 v53, v10, v12
	ds_read_b128 v[12:15], v192
	s_waitcnt lgkmcnt(0)
	v_fmac_f32_e32 v49, v7, v15
	v_fmac_f32_e32 v49, v11, v14
	v_fmac_f32_e32 v49, v6, v13
	v_fmac_f32_e32 v49, v10, v12
	ds_read_b128 v[12:15], v193
	s_waitcnt lgkmcnt(0)
	v_fmac_f32_e32 v45, v7, v15
	v_fmac_f32_e32 v45, v11, v14
	v_fmac_f32_e32 v45, v6, v13
	v_fmac_f32_e32 v45, v10, v12
	ds_read_b128 v[12:15], v194
	s_waitcnt lgkmcnt(0)
	v_fmac_f32_e32 v41, v7, v15
	v_fmac_f32_e32 v41, v11, v14
	v_fmac_f32_e32 v41, v6, v13
	v_fmac_f32_e32 v41, v10, v12
	ds_read_b128 v[12:15], v195
	s_waitcnt lgkmcnt(0)
	v_fmac_f32_e32 v37, v7, v15
	v_fmac_f32_e32 v37, v11, v14
	v_fmac_f32_e32 v37, v6, v13
	v_fmac_f32_e32 v37, v10, v12
	ds_read_b128 v[12:15], v196
	s_waitcnt lgkmcnt(0)
	v_fmac_f32_e32 v33, v7, v15
	v_fmac_f32_e32 v33, v11, v14
	v_fmac_f32_e32 v33, v6, v13
	v_fmac_f32_e32 v33, v10, v12
	ds_read_b128 v[12:15], v197
	s_waitcnt lgkmcnt(0)
	v_fmac_f32_e32 v30, v7, v15
	v_fmac_f32_e32 v30, v11, v14
	v_fmac_f32_e32 v30, v6, v13
	v_fmac_f32_e32 v30, v10, v12
	ds_read_b128 v[8:11], v198
	ds_read_b128 v[12:15], v18 offset:3072
	s_nop 0
	ds_read_b128 v[16:19], v20 offset:3072
	v_mov_b32_e32 v6, v2
	v_mov_b32_e32 v7, v4
	v_pk_mul_f32 v[6:7], v[6:7], v[114:115] op_sel_hi:[1,0]
	s_waitcnt lgkmcnt(0)
	v_mov_b32_e32 v20, v8
	v_mov_b32_e32 v21, v10
	v_pk_mul_f32 v[6:7], v[6:7], v[20:21]
	v_mov_b32_e32 v4, v3
	v_pk_mul_f32 v[2:3], v[4:5], v[114:115] op_sel_hi:[1,0]
	v_mov_b32_e32 v10, v9
	v_pk_mul_f32 v[2:3], v[2:3], v[10:11]
	s_waitcnt lgkmcnt(0)
	v_mov_b32_e32 v22, v12
	v_mov_b32_e32 v20, v16
	v_mov_b32_e32 v21, v18
	v_pk_add_f32 v[20:21], v[20:21], 1.0 op_sel_hi:[1,0]
	v_mov_b32_e32 v23, v14
	v_mov_b32_e32 v18, v17
	v_pk_fma_f32 v[6:7], v[6:7], v[20:21], v[22:23]
	v_pk_add_f32 v[4:5], v[18:19], 1.0 op_sel_hi:[1,0]
	v_mov_b32_e32 v14, v13
	v_pk_fma_f32 v[2:3], v[2:3], v[4:5], v[14:15]
	v_and_b32_sdwa v5, v6, v208 dst_sel:DWORD dst_unused:UNUSED_PAD src0_sel:WORD_1 src1_sel:DWORD
	v_add3_u32 v8, v6, v5, s57
	v_and_b32_sdwa v5, v3, v208 dst_sel:DWORD dst_unused:UNUSED_PAD src0_sel:WORD_1 src1_sel:DWORD
	v_and_b32_sdwa v9, v2, v208 dst_sel:DWORD dst_unused:UNUSED_PAD src0_sel:WORD_1 src1_sel:DWORD
	v_and_b32_sdwa v4, v7, v208 dst_sel:DWORD dst_unused:UNUSED_PAD src0_sel:WORD_1 src1_sel:DWORD
	v_add3_u32 v5, v3, v5, s57
	v_add3_u32 v9, v2, v9, s57
	v_add3_u32 v4, v7, v4, s57
	v_and_b32_e32 v5, 0xffff0000, v5
	v_and_b32_e32 v9, 0xffff0000, v9
	v_or_b32_sdwa v5, v5, v4 dst_sel:DWORD dst_unused:UNUSED_PAD src0_sel:DWORD src1_sel:WORD_1
	v_or_b32_sdwa v4, v9, v8 dst_sel:DWORD dst_unused:UNUSED_PAD src0_sel:DWORD src1_sel:WORD_1
	ds_read_b128 v[8:11], v134 offset:7168
	global_store_dwordx2 v[94:95], v[4:5], off offset:3584
	s_waitcnt lgkmcnt(0)
	v_fmac_f32_e32 v89, v3, v11
	v_fmac_f32_e32 v89, v7, v10
	v_fmac_f32_e32 v89, v2, v9
	v_fmac_f32_e32 v89, v6, v8
	ds_read_b128 v[8:11], v134 offset:15360
	s_waitcnt lgkmcnt(0)
	v_fmac_f32_e32 v85, v3, v11
	v_fmac_f32_e32 v85, v7, v10
	v_fmac_f32_e32 v85, v2, v9
	v_fmac_f32_e32 v85, v6, v8
	ds_read_b128 v[8:11], v134 offset:23552
	s_waitcnt lgkmcnt(0)
	v_fmac_f32_e32 v81, v3, v11
	v_fmac_f32_e32 v81, v7, v10
	v_fmac_f32_e32 v81, v2, v9
	v_fmac_f32_e32 v81, v6, v8
	ds_read_b128 v[8:11], v134 offset:31744
	s_waitcnt lgkmcnt(0)
	v_fmac_f32_e32 v77, v3, v11
	v_fmac_f32_e32 v77, v7, v10
	v_fmac_f32_e32 v77, v2, v9
	v_fmac_f32_e32 v77, v6, v8
	ds_read_b128 v[8:11], v134 offset:39936
	s_waitcnt lgkmcnt(0)
	v_fmac_f32_e32 v73, v3, v11
	v_fmac_f32_e32 v73, v7, v10
	v_fmac_f32_e32 v73, v2, v9
	v_fmac_f32_e32 v73, v6, v8
	ds_read_b128 v[8:11], v134 offset:48128
	s_waitcnt lgkmcnt(0)
	v_fmac_f32_e32 v69, v3, v11
	v_fmac_f32_e32 v69, v7, v10
	v_fmac_f32_e32 v69, v2, v9
	v_fmac_f32_e32 v69, v6, v8
	ds_read_b128 v[8:11], v134 offset:56320
	s_waitcnt lgkmcnt(0)
	v_fmac_f32_e32 v65, v3, v11
	v_fmac_f32_e32 v65, v7, v10
	v_fmac_f32_e32 v65, v2, v9
	v_fmac_f32_e32 v65, v6, v8
	ds_read_b128 v[8:11], v134 offset:64512
	s_waitcnt lgkmcnt(0)
	v_fmac_f32_e32 v61, v3, v11
	v_fmac_f32_e32 v61, v7, v10
	v_fmac_f32_e32 v61, v2, v9
	v_fmac_f32_e32 v61, v6, v8
	ds_read_b128 v[8:11], v199
	s_waitcnt lgkmcnt(0)
	v_fmac_f32_e32 v57, v3, v11
	v_fmac_f32_e32 v57, v7, v10
	v_fmac_f32_e32 v57, v2, v9
	v_fmac_f32_e32 v57, v6, v8
	ds_read_b128 v[8:11], v200
	s_waitcnt lgkmcnt(0)
	v_fmac_f32_e32 v53, v3, v11
	v_fmac_f32_e32 v53, v7, v10
	v_fmac_f32_e32 v53, v2, v9
	v_fmac_f32_e32 v53, v6, v8
	ds_read_b128 v[8:11], v201
	s_waitcnt lgkmcnt(0)
	v_fmac_f32_e32 v49, v3, v11
	v_fmac_f32_e32 v49, v7, v10
	v_fmac_f32_e32 v49, v2, v9
	v_fmac_f32_e32 v49, v6, v8
	ds_read_b128 v[8:11], v202
	s_waitcnt lgkmcnt(0)
	v_fmac_f32_e32 v45, v3, v11
	v_fmac_f32_e32 v45, v7, v10
	v_fmac_f32_e32 v45, v2, v9
	v_fmac_f32_e32 v45, v6, v8
	ds_read_b128 v[8:11], v203
	s_waitcnt lgkmcnt(0)
	v_fmac_f32_e32 v41, v3, v11
	v_fmac_f32_e32 v41, v7, v10
	v_fmac_f32_e32 v41, v2, v9
	v_fmac_f32_e32 v41, v6, v8
	ds_read_b128 v[8:11], v204
	s_waitcnt lgkmcnt(0)
	v_fmac_f32_e32 v37, v3, v11
	v_fmac_f32_e32 v37, v7, v10
	v_fmac_f32_e32 v37, v2, v9
	v_fmac_f32_e32 v37, v6, v8
	ds_read_b128 v[8:11], v205
	s_waitcnt lgkmcnt(0)
	v_fmac_f32_e32 v33, v3, v11
	v_fmac_f32_e32 v33, v7, v10
	v_fmac_f32_e32 v33, v2, v9
	v_fmac_f32_e32 v33, v6, v8
	ds_read_b128 v[8:11], v206
	s_waitcnt lgkmcnt(0)
	v_fmac_f32_e32 v30, v3, v11
	v_fmac_f32_e32 v30, v7, v10
	v_fmac_f32_e32 v30, v2, v9
	v_fmac_f32_e32 v30, v6, v8
	ds_bpermute_b32 v6, v1, v81
	ds_bpermute_b32 v7, v1, v77
	ds_bpermute_b32 v22, v1, v49
	ds_bpermute_b32 v10, v1, v73
	ds_bpermute_b32 v24, v1, v41
	s_waitcnt lgkmcnt(4)
	v_add_f32_e32 v6, v81, v6
	ds_bpermute_b32 v8, v128, v6
	s_waitcnt lgkmcnt(4)
	v_add_f32_e32 v7, v77, v7
	ds_bpermute_b32 v9, v128, v7
	s_waitcnt lgkmcnt(4)
	v_add_f32_e32 v22, v49, v22
	ds_bpermute_b32 v23, v128, v22
	s_waitcnt lgkmcnt(2)
	v_add_f32_e32 v6, v6, v8
	ds_bpermute_b32 v8, v129, v6
	s_waitcnt lgkmcnt(2)
	v_add_f32_e32 v7, v7, v9
	ds_bpermute_b32 v9, v129, v7
	s_waitcnt lgkmcnt(2)
	v_add_f32_e32 v22, v22, v23
	ds_bpermute_b32 v23, v129, v22
	s_waitcnt lgkmcnt(2)
	v_add_f32_e32 v6, v6, v8
	ds_bpermute_b32 v8, v130, v6
	s_waitcnt lgkmcnt(2)
	v_add_f32_e32 v7, v7, v9
	ds_bpermute_b32 v9, v130, v7
	v_add_f32_e32 v10, v73, v10
	s_waitcnt lgkmcnt(2)
	v_add_f32_e32 v22, v22, v23
	s_waitcnt lgkmcnt(1)
	v_add_f32_e32 v6, v6, v8
	ds_bpermute_b32 v8, v131, v6
	s_waitcnt lgkmcnt(1)
	v_add_f32_e32 v9, v7, v9
	ds_bpermute_b32 v12, v131, v9
	v_add_f32_e32 v23, v41, v24
	ds_bpermute_b32 v11, v128, v10
	s_waitcnt lgkmcnt(2)
	v_add_f32_e32 v6, v6, v8
	ds_bpermute_b32 v8, v1, v69
	ds_bpermute_b32 v24, v128, v23
	ds_bpermute_b32 v27, v130, v22
	s_waitcnt lgkmcnt(3)
	v_add_f32_e32 v10, v10, v11
	ds_bpermute_b32 v11, v129, v10
	s_waitcnt lgkmcnt(3)
	v_add_f32_e32 v13, v69, v8
	ds_bpermute_b32 v14, v128, v13
	v_add_f32_e32 v8, v9, v12
	s_waitcnt lgkmcnt(3)
	v_add_f32_e32 v23, v23, v24
	ds_bpermute_b32 v24, v129, v23
	s_waitcnt lgkmcnt(2)
	v_add_f32_e32 v10, v10, v11
	s_waitcnt lgkmcnt(1)
	v_add_f32_e32 v12, v13, v14
	ds_bpermute_b32 v14, v1, v65
	v_add_f32_e32 v22, v22, v27
	s_waitcnt lgkmcnt(1)
	v_add_f32_e32 v23, v23, v24
	ds_bpermute_b32 v11, v130, v10
	ds_bpermute_b32 v27, v131, v22
	s_waitcnt lgkmcnt(2)
	v_add_f32_e32 v14, v65, v14
	ds_bpermute_b32 v15, v128, v14
	ds_bpermute_b32 v24, v130, v23
	s_waitcnt lgkmcnt(3)
	v_add_f32_e32 v10, v10, v11
	s_waitcnt lgkmcnt(2)
	v_add_f32_e32 v22, v22, v27
	ds_bpermute_b32 v11, v131, v10
	s_waitcnt lgkmcnt(2)
	v_add_f32_e32 v14, v14, v15
	ds_bpermute_b32 v15, v129, v14
	s_waitcnt lgkmcnt(2)
	v_add_f32_e32 v27, v23, v24
	ds_bpermute_b32 v28, v131, v27
	ds_bpermute_b32 v2, v1, v89
	ds_bpermute_b32 v3, v1, v85
	s_waitcnt lgkmcnt(3)
	v_add_f32_e32 v14, v14, v15
	ds_bpermute_b32 v15, v130, v14
	v_add_f32_e32 v10, v10, v11
	ds_bpermute_b32 v11, v1, v61
	ds_bpermute_b32 v18, v1, v57
	ds_bpermute_b32 v29, v1, v37
	s_waitcnt lgkmcnt(3)
	v_add_f32_e32 v14, v14, v15
	ds_bpermute_b32 v15, v131, v14
	ds_bpermute_b32 v31, v1, v30
	v_add_f32_e32 v2, v89, v2
	v_add_f32_e32 v3, v85, v3
	s_waitcnt lgkmcnt(4)
	v_add_f32_e32 v16, v61, v11
	s_waitcnt lgkmcnt(1)
	v_add_f32_e32 v14, v14, v15
	ds_bpermute_b32 v15, v1, v53
	v_add_f32_e32 v18, v57, v18
	v_add_f32_e32 v29, v37, v29
	s_waitcnt lgkmcnt(1)
	v_add_f32_e32 v30, v30, v31
	ds_bpermute_b32 v4, v128, v2
	s_waitcnt lgkmcnt(1)
	v_add_f32_e32 v20, v53, v15
	ds_bpermute_b32 v21, v128, v20
	ds_bpermute_b32 v5, v128, v3
	ds_bpermute_b32 v17, v128, v16
	ds_bpermute_b32 v19, v128, v18
	ds_bpermute_b32 v32, v128, v29
	s_waitcnt lgkmcnt(4)
	v_add_f32_e32 v20, v20, v21
	ds_bpermute_b32 v21, v129, v20
	ds_bpermute_b32 v31, v128, v30
	v_add_f32_e32 v2, v2, v4
	s_waitcnt lgkmcnt(5)
	v_add_f32_e32 v3, v3, v5
	s_waitcnt lgkmcnt(4)
	v_add_f32_e32 v16, v16, v17
	s_waitcnt lgkmcnt(1)
	v_add_f32_e32 v20, v20, v21
	ds_bpermute_b32 v21, v130, v20
	v_add_f32_e32 v18, v18, v19
	v_add_f32_e32 v29, v29, v32
	s_waitcnt lgkmcnt(1)
	v_add_f32_e32 v30, v30, v31
	ds_bpermute_b32 v4, v129, v2
	s_waitcnt lgkmcnt(1)
	v_add_f32_e32 v20, v20, v21
	ds_bpermute_b32 v21, v1, v45
	ds_bpermute_b32 v25, v131, v20
	ds_bpermute_b32 v5, v129, v3
	ds_bpermute_b32 v13, v129, v12
	ds_bpermute_b32 v17, v129, v16
	s_waitcnt lgkmcnt(4)
	v_add_f32_e32 v21, v45, v21
	ds_bpermute_b32 v26, v128, v21
	s_waitcnt lgkmcnt(4)
	v_add_f32_e32 v20, v20, v25
	ds_bpermute_b32 v19, v129, v18
	ds_bpermute_b32 v32, v129, v29
	ds_bpermute_b32 v31, v129, v30
	s_waitcnt lgkmcnt(3)
	v_add_f32_e32 v21, v21, v26
	ds_bpermute_b32 v26, v129, v21
	v_add_f32_e32 v2, v2, v4
	v_add_f32_e32 v3, v3, v5
	v_add_f32_e32 v12, v12, v13
	v_add_f32_e32 v16, v16, v17
	s_waitcnt lgkmcnt(0)
	v_add_f32_e32 v25, v21, v26
	ds_bpermute_b32 v26, v130, v25
	v_add_f32_e32 v18, v18, v19
	v_add_f32_e32 v29, v29, v32
	v_add_f32_e32 v30, v30, v31
	ds_bpermute_b32 v4, v130, v2
	s_waitcnt lgkmcnt(1)
	v_add_f32_e32 v25, v25, v26
	ds_bpermute_b32 v26, v131, v25
	ds_bpermute_b32 v5, v130, v3
	ds_bpermute_b32 v13, v130, v12
	ds_bpermute_b32 v17, v130, v16
	ds_bpermute_b32 v19, v130, v18
	s_waitcnt lgkmcnt(4)
	v_add_f32_e32 v24, v25, v26
	v_add_f32_e32 v26, v27, v28
	ds_bpermute_b32 v28, v1, v33
	ds_bpermute_b32 v32, v130, v29
	ds_bpermute_b32 v31, v130, v30
	v_add_f32_e32 v2, v2, v4
	s_waitcnt lgkmcnt(6)
	v_add_f32_e32 v3, v3, v5
	s_waitcnt lgkmcnt(2)
	v_add_f32_e32 v28, v33, v28
	ds_bpermute_b32 v33, v128, v28
	v_add_f32_e32 v12, v12, v13
	v_add_f32_e32 v16, v16, v17
	v_add_f32_e32 v18, v18, v19
	s_waitcnt lgkmcnt(2)
	v_add_f32_e32 v29, v29, v32
	s_waitcnt lgkmcnt(0)
	v_add_f32_e32 v28, v28, v33
	ds_bpermute_b32 v33, v129, v28
	v_add_f32_e32 v35, v30, v31
	ds_bpermute_b32 v4, v131, v2
	ds_bpermute_b32 v5, v131, v3
	ds_bpermute_b32 v13, v131, v12
	s_waitcnt lgkmcnt(3)
	v_add_f32_e32 v28, v28, v33
	ds_bpermute_b32 v33, v130, v28
	ds_bpermute_b32 v17, v131, v16
	ds_bpermute_b32 v19, v131, v18
	ds_bpermute_b32 v32, v131, v29
	ds_bpermute_b32 v36, v131, v35
	s_waitcnt lgkmcnt(4)
	v_add_f32_e32 v33, v28, v33
	ds_bpermute_b32 v34, v131, v33
	v_add_f32_e32 v2, v2, v4
	v_add_f32_e32 v3, v3, v5
	v_add_f32_e32 v12, v12, v13
	s_waitcnt lgkmcnt(4)
	v_add_f32_e32 v16, v16, v17
	s_waitcnt lgkmcnt(3)
	v_add_f32_e32 v18, v18, v19
	s_waitcnt lgkmcnt(2)
	v_add_f32_e32 v28, v29, v32
	s_waitcnt lgkmcnt(0)
	v_add_f32_e32 v29, v33, v34
	v_add_f32_e32 v32, v35, v36
	ds_bpermute_b32 v4, v132, v2
	ds_bpermute_b32 v5, v132, v3
	ds_bpermute_b32 v7, v132, v6
	ds_bpermute_b32 v9, v132, v8
	ds_bpermute_b32 v11, v132, v10
	ds_bpermute_b32 v13, v132, v12
	ds_bpermute_b32 v15, v132, v14
	ds_bpermute_b32 v17, v132, v16
	ds_bpermute_b32 v19, v132, v18
	ds_bpermute_b32 v21, v132, v20
	ds_bpermute_b32 v23, v132, v22
	ds_bpermute_b32 v25, v132, v24
	ds_bpermute_b32 v27, v132, v26
	ds_bpermute_b32 v30, v132, v28
	ds_bpermute_b32 v31, v132, v29
	ds_bpermute_b32 v33, v132, v32
	s_and_saveexec_b64 s[52:53], s[2:3]
	s_cbranch_execz .LBB0_1364
	s_waitcnt lgkmcnt(14)
	v_add_f32_e32 v2, v2, v4
	v_add_f32_e32 v3, v3, v5
	s_mov_b32 s61, 0xff61b1e6
	v_max3_f32 v4, v2, s61, v3
	s_waitcnt lgkmcnt(13)
	v_add_f32_e32 v5, v6, v7
	s_waitcnt lgkmcnt(12)
	v_add_f32_e32 v6, v8, v9
	v_max3_f32 v4, v4, v5, v6
	s_waitcnt lgkmcnt(11)
	v_add_f32_e32 v7, v10, v11
	s_waitcnt lgkmcnt(10)
	v_add_f32_e32 v8, v12, v13
	v_max3_f32 v4, v4, v7, v8
	s_waitcnt lgkmcnt(9)
	v_add_f32_e32 v11, v14, v15
	s_waitcnt lgkmcnt(8)
	v_add_f32_e32 v15, v16, v17
	v_max3_f32 v4, v4, v11, v15
	s_waitcnt lgkmcnt(7)
	v_add_f32_e32 v16, v18, v19
	s_waitcnt lgkmcnt(6)
	v_add_f32_e32 v17, v20, v21
	v_max3_f32 v4, v4, v16, v17
	s_waitcnt lgkmcnt(5)
	v_add_f32_e32 v18, v22, v23
	s_waitcnt lgkmcnt(4)
	v_add_f32_e32 v19, v24, v25
	v_max3_f32 v4, v4, v18, v19
	s_waitcnt lgkmcnt(3)
	v_add_f32_e32 v14, v26, v27
	s_waitcnt lgkmcnt(2)
	v_add_f32_e32 v13, v28, v30
	s_waitcnt lgkmcnt(0)
	v_add_f32_e32 v32, v32, v33
	v_max3_f32 v4, v4, v14, v13
	v_add_f32_e32 v10, v29, v31
	v_max3_f32 v12, v4, v10, v32
	v_sub_f32_e32 v4, v32, v12
	v_mul_f32_e32 v9, 0x3fb8aa3b, v4
	v_fma_f32 v20, v4, s58, -v9
	v_rndne_f32_e32 v21, v9
	v_fmac_f32_e32 v20, 0x32a5705f, v4
	v_sub_f32_e32 v9, v9, v21
	v_add_f32_e32 v9, v9, v20
	v_exp_f32_e32 v9, v9
	v_cvt_i32_f32_e32 v20, v21
	v_cmp_ngt_f32_e32 vcc, s59, v4
	v_sub_f32_e32 v2, v2, v12
	v_sub_f32_e32 v3, v3, v12
	v_ldexp_f32 v9, v9, v20
	v_cndmask_b32_e32 v9, 0, v9, vcc
	v_cmp_nlt_f32_e32 vcc, s60, v4
	v_mul_f32_e32 v4, 0x3fb8aa3b, v2
	v_fma_f32 v20, v2, s58, -v4
	v_rndne_f32_e32 v21, v4
	v_fmac_f32_e32 v20, 0x32a5705f, v2
	v_sub_f32_e32 v4, v4, v21
	v_add_f32_e32 v4, v4, v20
	v_exp_f32_e32 v4, v4
	v_cvt_i32_f32_e32 v20, v21
	v_cndmask_b32_e32 v9, v209, v9, vcc
	v_cmp_ngt_f32_e32 vcc, s59, v2
	v_sub_f32_e32 v17, v17, v12
	v_ldexp_f32 v4, v4, v20
	v_cndmask_b32_e32 v4, 0, v4, vcc
	v_cmp_nlt_f32_e32 vcc, s60, v2
	v_sub_f32_e32 v18, v18, v12
	v_sub_f32_e32 v19, v19, v12
	v_cndmask_b32_e32 v2, v209, v4, vcc
	v_mul_f32_e32 v4, 0x3fb8aa3b, v3
	v_fma_f32 v20, v3, s58, -v4
	v_rndne_f32_e32 v21, v4
	v_fmac_f32_e32 v20, 0x32a5705f, v3
	v_sub_f32_e32 v4, v4, v21
	v_add_f32_e32 v4, v4, v20
	v_exp_f32_e32 v4, v4
	v_cvt_i32_f32_e32 v20, v21
	v_cmp_ngt_f32_e32 vcc, s59, v3
	v_sub_f32_e32 v14, v14, v12
	v_sub_f32_e32 v13, v13, v12
	v_ldexp_f32 v4, v4, v20
	v_cndmask_b32_e32 v4, 0, v4, vcc
	v_cmp_nlt_f32_e32 vcc, s60, v3
	v_sub_f32_e32 v10, v10, v12
	s_nop 0
	v_cndmask_b32_e32 v3, v209, v4, vcc
	v_sub_f32_e32 v4, v5, v12
	v_mul_f32_e32 v5, 0x3fb8aa3b, v4
	v_fma_f32 v21, v4, s58, -v5
	v_rndne_f32_e32 v22, v5
	v_fmac_f32_e32 v21, 0x32a5705f, v4
	v_sub_f32_e32 v5, v5, v22
	v_add_f32_e32 v5, v5, v21
	v_exp_f32_e32 v5, v5
	v_cvt_i32_f32_e32 v21, v22
	v_cmp_ngt_f32_e32 vcc, s59, v4
	v_add_f32_e32 v20, v2, v3
	v_ldexp_f32 v5, v5, v21
	v_cndmask_b32_e32 v5, 0, v5, vcc
	v_cmp_nlt_f32_e32 vcc, s60, v4
	s_nop 1
	v_cndmask_b32_e32 v4, v209, v5, vcc
	v_sub_f32_e32 v5, v6, v12
	v_mul_f32_e32 v6, 0x3fb8aa3b, v5
	v_fma_f32 v21, v5, s58, -v6
	v_rndne_f32_e32 v22, v6
	v_fmac_f32_e32 v21, 0x32a5705f, v5
	v_sub_f32_e32 v6, v6, v22
	v_add_f32_e32 v6, v6, v21
	v_exp_f32_e32 v6, v6
	v_cvt_i32_f32_e32 v21, v22
	v_cmp_ngt_f32_e32 vcc, s59, v5
	v_add_f32_e32 v20, v4, v20
	v_ldexp_f32 v6, v6, v21
	v_cndmask_b32_e32 v6, 0, v6, vcc
	v_cmp_nlt_f32_e32 vcc, s60, v5
	s_nop 1
	v_cndmask_b32_e32 v5, v209, v6, vcc
	v_sub_f32_e32 v6, v7, v12
	v_mul_f32_e32 v7, 0x3fb8aa3b, v6
	v_fma_f32 v21, v6, s58, -v7
	v_rndne_f32_e32 v22, v7
	v_fmac_f32_e32 v21, 0x32a5705f, v6
	v_sub_f32_e32 v7, v7, v22
	v_add_f32_e32 v7, v7, v21
	v_exp_f32_e32 v7, v7
	v_cvt_i32_f32_e32 v21, v22
	v_cmp_ngt_f32_e32 vcc, s59, v6
	v_add_f32_e32 v20, v5, v20
	v_ldexp_f32 v7, v7, v21
	v_cndmask_b32_e32 v7, 0, v7, vcc
	v_cmp_nlt_f32_e32 vcc, s60, v6
	s_nop 1
	v_cndmask_b32_e32 v6, v209, v7, vcc
	v_sub_f32_e32 v7, v8, v12
	v_mul_f32_e32 v8, 0x3fb8aa3b, v7
	v_fma_f32 v21, v7, s58, -v8
	v_rndne_f32_e32 v22, v8
	v_fmac_f32_e32 v21, 0x32a5705f, v7
	v_sub_f32_e32 v8, v8, v22
	v_add_f32_e32 v8, v8, v21
	v_exp_f32_e32 v8, v8
	v_cvt_i32_f32_e32 v21, v22
	v_cmp_ngt_f32_e32 vcc, s59, v7
	v_add_f32_e32 v20, v6, v20
	v_ldexp_f32 v8, v8, v21
	v_cndmask_b32_e32 v8, 0, v8, vcc
	v_cmp_nlt_f32_e32 vcc, s60, v7
	s_nop 1
	v_cndmask_b32_e32 v7, v209, v8, vcc
	v_sub_f32_e32 v8, v11, v12
	v_mul_f32_e32 v11, 0x3fb8aa3b, v8
	v_fma_f32 v21, v8, s58, -v11
	v_rndne_f32_e32 v22, v11
	v_fmac_f32_e32 v21, 0x32a5705f, v8
	v_sub_f32_e32 v11, v11, v22
	v_add_f32_e32 v11, v11, v21
	v_exp_f32_e32 v11, v11
	v_cvt_i32_f32_e32 v21, v22
	v_cmp_ngt_f32_e32 vcc, s59, v8
	v_add_f32_e32 v20, v7, v20
	v_ldexp_f32 v11, v11, v21
	v_cndmask_b32_e32 v11, 0, v11, vcc
	v_cmp_nlt_f32_e32 vcc, s60, v8
	s_nop 1
	v_cndmask_b32_e32 v8, v209, v11, vcc
	v_sub_f32_e32 v11, v15, v12
	v_mul_f32_e32 v15, 0x3fb8aa3b, v11
	v_fma_f32 v21, v11, s58, -v15
	v_rndne_f32_e32 v22, v15
	v_fmac_f32_e32 v21, 0x32a5705f, v11
	v_sub_f32_e32 v15, v15, v22
	v_add_f32_e32 v15, v15, v21
	v_exp_f32_e32 v15, v15
	v_cvt_i32_f32_e32 v21, v22
	v_cmp_ngt_f32_e32 vcc, s59, v11
	v_add_f32_e32 v20, v8, v20
	v_ldexp_f32 v15, v15, v21
	v_cndmask_b32_e32 v15, 0, v15, vcc
	v_cmp_nlt_f32_e32 vcc, s60, v11
	s_nop 1
	v_cndmask_b32_e32 v11, v209, v15, vcc
	v_sub_f32_e32 v15, v16, v12
	v_mul_f32_e32 v16, 0x3fb8aa3b, v15
	v_fma_f32 v21, v15, s58, -v16
	v_rndne_f32_e32 v22, v16
	v_fmac_f32_e32 v21, 0x32a5705f, v15
	v_sub_f32_e32 v16, v16, v22
	v_add_f32_e32 v16, v16, v21
	v_exp_f32_e32 v16, v16
	v_cvt_i32_f32_e32 v21, v22
	v_cmp_ngt_f32_e32 vcc, s59, v15
	v_add_f32_e32 v20, v11, v20
	v_mul_f32_e32 v12, 0x3fb8aa3b, v10
	v_ldexp_f32 v16, v16, v21
	v_cndmask_b32_e32 v16, 0, v16, vcc
	v_cmp_nlt_f32_e32 vcc, s60, v15
	s_nop 1
	v_cndmask_b32_e32 v15, v209, v16, vcc
	v_add_f32_e32 v16, v15, v20
	v_mul_f32_e32 v20, 0x3fb8aa3b, v17
	v_fma_f32 v21, v17, s58, -v20
	v_rndne_f32_e32 v22, v20
	v_fmac_f32_e32 v21, 0x32a5705f, v17
	v_sub_f32_e32 v20, v20, v22
	v_add_f32_e32 v20, v20, v21
	v_exp_f32_e32 v20, v20
	v_cvt_i32_f32_e32 v21, v22
	v_cmp_ngt_f32_e32 vcc, s59, v17
	v_ldexp_f32 v20, v20, v21
	s_nop 0
	v_cndmask_b32_e32 v20, 0, v20, vcc
	v_cmp_nlt_f32_e32 vcc, s60, v17
	s_nop 1
	v_cndmask_b32_e32 v17, v209, v20, vcc
	v_mul_f32_e32 v20, 0x3fb8aa3b, v18
	v_fma_f32 v21, v18, s58, -v20
	v_rndne_f32_e32 v22, v20
	v_fmac_f32_e32 v21, 0x32a5705f, v18
	v_sub_f32_e32 v20, v20, v22
	v_add_f32_e32 v20, v20, v21
	v_exp_f32_e32 v20, v20
	v_cvt_i32_f32_e32 v21, v22
	v_cmp_ngt_f32_e32 vcc, s59, v18
	v_add_f32_e32 v16, v17, v16
	v_ldexp_f32 v20, v20, v21
	v_cndmask_b32_e32 v20, 0, v20, vcc
	v_cmp_nlt_f32_e32 vcc, s60, v18
	s_nop 1
	v_cndmask_b32_e32 v18, v209, v20, vcc
	v_mul_f32_e32 v20, 0x3fb8aa3b, v19
	v_fma_f32 v21, v19, s58, -v20
	v_rndne_f32_e32 v22, v20
	v_fmac_f32_e32 v21, 0x32a5705f, v19
	v_sub_f32_e32 v20, v20, v22
	v_add_f32_e32 v20, v20, v21
	v_exp_f32_e32 v20, v20
	v_cvt_i32_f32_e32 v21, v22
	v_cmp_ngt_f32_e32 vcc, s59, v19
	v_add_f32_e32 v16, v18, v16
	v_ldexp_f32 v20, v20, v21
	v_cndmask_b32_e32 v20, 0, v20, vcc
	v_cmp_nlt_f32_e32 vcc, s60, v19
	s_nop 1
	v_cndmask_b32_e32 v19, v209, v20, vcc
	v_mul_f32_e32 v20, 0x3fb8aa3b, v14
	v_fma_f32 v21, v14, s58, -v20
	v_rndne_f32_e32 v22, v20
	v_fmac_f32_e32 v21, 0x32a5705f, v14
	v_sub_f32_e32 v20, v20, v22
	v_add_f32_e32 v20, v20, v21
	v_exp_f32_e32 v20, v20
	v_cvt_i32_f32_e32 v21, v22
	v_cmp_ngt_f32_e32 vcc, s59, v14
	v_add_f32_e32 v16, v19, v16
	v_ldexp_f32 v20, v20, v21
	v_cndmask_b32_e32 v20, 0, v20, vcc
	v_cmp_nlt_f32_e32 vcc, s60, v14
	s_nop 1
	v_cndmask_b32_e32 v14, v209, v20, vcc
	v_mul_f32_e32 v20, 0x3fb8aa3b, v13
	v_fma_f32 v21, v13, s58, -v20
	v_rndne_f32_e32 v22, v20
	v_fmac_f32_e32 v21, 0x32a5705f, v13
	v_sub_f32_e32 v20, v20, v22
	v_add_f32_e32 v20, v20, v21
	v_exp_f32_e32 v20, v20
	v_cvt_i32_f32_e32 v21, v22
	v_cmp_ngt_f32_e32 vcc, s59, v13
	v_add_f32_e32 v16, v14, v16
	v_ldexp_f32 v20, v20, v21
	v_cndmask_b32_e32 v20, 0, v20, vcc
	v_cmp_nlt_f32_e32 vcc, s60, v13
	v_rndne_f32_e32 v21, v12
	s_nop 0
	v_cndmask_b32_e32 v13, v209, v20, vcc
	v_fma_f32 v20, v10, s58, -v12
	v_fmac_f32_e32 v20, 0x32a5705f, v10
	v_sub_f32_e32 v12, v12, v21
	v_add_f32_e32 v12, v12, v20
	v_exp_f32_e32 v12, v12
	v_cvt_i32_f32_e32 v20, v21
	v_cmp_ngt_f32_e32 vcc, s59, v10
	v_add_f32_e32 v16, v13, v16
	v_ldexp_f32 v12, v12, v20
	v_cndmask_b32_e32 v12, 0, v12, vcc
	v_cmp_nlt_f32_e32 vcc, s60, v10
	s_nop 1
	v_cndmask_b32_e32 v12, v209, v12, vcc
	v_add_f32_e32 v10, v12, v16
	v_add_f32_e32 v10, v9, v10
	v_div_scale_f32 v16, s[62:63], v10, v10, v9
	v_rcp_f32_e32 v20, v16
	s_nop 0
	v_fma_f32 v21, -v16, v20, 1.0
	v_fmac_f32_e32 v20, v21, v20
	v_div_scale_f32 v21, vcc, v9, v10, v9
	v_mul_f32_e32 v22, v21, v20
	v_fma_f32 v23, -v16, v22, v21
	v_fmac_f32_e32 v22, v23, v20
	v_fma_f32 v16, -v16, v22, v21
	v_div_fmas_f32 v16, v16, v20, v22
	v_div_fixup_f32 v9, v16, v10, v9
	v_div_scale_f32 v16, s[62:63], v10, v10, v12
	v_rcp_f32_e32 v20, v16
	s_nop 0
	v_fma_f32 v21, -v16, v20, 1.0
	v_fmac_f32_e32 v20, v21, v20
	v_div_scale_f32 v21, vcc, v12, v10, v12
	v_mul_f32_e32 v22, v21, v20
	v_fma_f32 v23, -v16, v22, v21
	v_fmac_f32_e32 v22, v23, v20
	v_fma_f32 v16, -v16, v22, v21
	v_div_fmas_f32 v16, v16, v20, v22
	v_div_fixup_f32 v12, v16, v10, v12
	v_div_scale_f32 v16, s[62:63], v10, v10, v13
	v_rcp_f32_e32 v20, v16
	s_nop 0
	v_fma_f32 v21, -v16, v20, 1.0
	v_fmac_f32_e32 v20, v21, v20
	v_div_scale_f32 v21, vcc, v13, v10, v13
	v_mul_f32_e32 v22, v21, v20
	v_fma_f32 v23, -v16, v22, v21
	v_fmac_f32_e32 v22, v23, v20
	v_fma_f32 v16, -v16, v22, v21
	v_div_fmas_f32 v16, v16, v20, v22
	v_div_fixup_f32 v13, v16, v10, v13
	v_div_scale_f32 v16, s[62:63], v10, v10, v14
	v_rcp_f32_e32 v20, v16
	s_nop 0
	v_fma_f32 v21, -v16, v20, 1.0
	v_fmac_f32_e32 v20, v21, v20
	v_div_scale_f32 v21, vcc, v14, v10, v14
	v_mul_f32_e32 v22, v21, v20
	v_fma_f32 v23, -v16, v22, v21
	v_fmac_f32_e32 v22, v23, v20
	v_fma_f32 v16, -v16, v22, v21
	v_div_fmas_f32 v16, v16, v20, v22
	v_div_fixup_f32 v14, v16, v10, v14
	v_div_scale_f32 v16, s[62:63], v10, v10, v19
	v_rcp_f32_e32 v20, v16
	s_nop 0
	v_fma_f32 v21, -v16, v20, 1.0
	v_fmac_f32_e32 v20, v21, v20
	v_div_scale_f32 v21, vcc, v19, v10, v19
	v_mul_f32_e32 v22, v21, v20
	v_fma_f32 v23, -v16, v22, v21
	v_fmac_f32_e32 v22, v23, v20
	v_fma_f32 v16, -v16, v22, v21
	v_div_fmas_f32 v16, v16, v20, v22
	v_div_fixup_f32 v16, v16, v10, v19
	v_div_scale_f32 v19, s[62:63], v10, v10, v18
	v_rcp_f32_e32 v20, v19
	s_nop 0
	v_fma_f32 v21, -v19, v20, 1.0
	v_fmac_f32_e32 v20, v21, v20
	v_div_scale_f32 v21, vcc, v18, v10, v18
	v_mul_f32_e32 v22, v21, v20
	v_fma_f32 v23, -v19, v22, v21
	v_fmac_f32_e32 v22, v23, v20
	v_fma_f32 v19, -v19, v22, v21
	v_div_fmas_f32 v19, v19, v20, v22
	v_div_fixup_f32 v18, v19, v10, v18
	v_div_scale_f32 v19, s[62:63], v10, v10, v17
	v_rcp_f32_e32 v20, v19
	s_nop 0
	v_fma_f32 v21, -v19, v20, 1.0
	v_fmac_f32_e32 v20, v21, v20
	v_div_scale_f32 v21, vcc, v17, v10, v17
	v_mul_f32_e32 v22, v21, v20
	v_fma_f32 v23, -v19, v22, v21
	v_fmac_f32_e32 v22, v23, v20
	v_fma_f32 v19, -v19, v22, v21
	v_div_fmas_f32 v19, v19, v20, v22
	v_div_fixup_f32 v17, v19, v10, v17
	v_div_scale_f32 v19, s[62:63], v10, v10, v15
	v_rcp_f32_e32 v20, v19
	s_nop 0
	v_fma_f32 v21, -v19, v20, 1.0
	v_fmac_f32_e32 v20, v21, v20
	v_div_scale_f32 v21, vcc, v15, v10, v15
	v_mul_f32_e32 v22, v21, v20
	v_fma_f32 v23, -v19, v22, v21
	v_fmac_f32_e32 v22, v23, v20
	v_fma_f32 v19, -v19, v22, v21
	v_div_fmas_f32 v19, v19, v20, v22
	v_div_fixup_f32 v15, v19, v10, v15
	v_div_scale_f32 v19, s[62:63], v10, v10, v11
	v_rcp_f32_e32 v20, v19
	s_nop 0
	v_fma_f32 v21, -v19, v20, 1.0
	v_fmac_f32_e32 v20, v21, v20
	v_div_scale_f32 v21, vcc, v11, v10, v11
	v_mul_f32_e32 v22, v21, v20
	v_fma_f32 v23, -v19, v22, v21
	v_fmac_f32_e32 v22, v23, v20
	v_fma_f32 v19, -v19, v22, v21
	v_div_fmas_f32 v19, v19, v20, v22
	v_div_fixup_f32 v11, v19, v10, v11
	v_div_scale_f32 v19, s[62:63], v10, v10, v8
	v_rcp_f32_e32 v20, v19
	s_nop 0
	v_fma_f32 v21, -v19, v20, 1.0
	v_fmac_f32_e32 v20, v21, v20
	v_div_scale_f32 v21, vcc, v8, v10, v8
	v_mul_f32_e32 v22, v21, v20
	v_fma_f32 v23, -v19, v22, v21
	v_fmac_f32_e32 v22, v23, v20
	v_fma_f32 v19, -v19, v22, v21
	v_div_fmas_f32 v19, v19, v20, v22
	v_div_fixup_f32 v8, v19, v10, v8
	v_div_scale_f32 v19, s[62:63], v10, v10, v7
	v_rcp_f32_e32 v20, v19
	s_nop 0
	v_fma_f32 v21, -v19, v20, 1.0
	v_fmac_f32_e32 v20, v21, v20
	v_div_scale_f32 v21, vcc, v7, v10, v7
	v_mul_f32_e32 v22, v21, v20
	v_fma_f32 v23, -v19, v22, v21
	v_fmac_f32_e32 v22, v23, v20
	v_fma_f32 v19, -v19, v22, v21
	v_div_fmas_f32 v19, v19, v20, v22
	v_div_fixup_f32 v7, v19, v10, v7
	v_div_scale_f32 v19, s[62:63], v10, v10, v6
	v_rcp_f32_e32 v20, v19
	s_nop 0
	v_fma_f32 v21, -v19, v20, 1.0
	v_fmac_f32_e32 v20, v21, v20
	v_div_scale_f32 v21, vcc, v6, v10, v6
	v_mul_f32_e32 v22, v21, v20
	v_fma_f32 v23, -v19, v22, v21
	v_fmac_f32_e32 v22, v23, v20
	v_fma_f32 v19, -v19, v22, v21
	v_div_fmas_f32 v19, v19, v20, v22
	v_div_fixup_f32 v6, v19, v10, v6
	v_div_scale_f32 v19, s[62:63], v10, v10, v5
	v_rcp_f32_e32 v20, v19
	s_nop 0
	v_fma_f32 v21, -v19, v20, 1.0
	v_fmac_f32_e32 v20, v21, v20
	v_div_scale_f32 v21, vcc, v5, v10, v5
	v_mul_f32_e32 v22, v21, v20
	v_fma_f32 v23, -v19, v22, v21
	v_fmac_f32_e32 v22, v23, v20
	v_fma_f32 v19, -v19, v22, v21
	v_div_fmas_f32 v19, v19, v20, v22
	v_div_fixup_f32 v5, v19, v10, v5
	v_div_scale_f32 v19, s[62:63], v10, v10, v4
	v_rcp_f32_e32 v20, v19
	s_nop 0
	v_fma_f32 v21, -v19, v20, 1.0
	v_fmac_f32_e32 v20, v21, v20
	v_div_scale_f32 v21, vcc, v4, v10, v4
	v_mul_f32_e32 v22, v21, v20
	v_fma_f32 v23, -v19, v22, v21
	v_fmac_f32_e32 v22, v23, v20
	v_fma_f32 v19, -v19, v22, v21
	v_div_fmas_f32 v19, v19, v20, v22
	v_div_fixup_f32 v4, v19, v10, v4
	v_div_scale_f32 v19, s[62:63], v10, v10, v3
	v_rcp_f32_e32 v20, v19
	s_nop 0
	v_fma_f32 v21, -v19, v20, 1.0
	v_fmac_f32_e32 v20, v21, v20
	v_div_scale_f32 v21, vcc, v3, v10, v3
	v_mul_f32_e32 v22, v21, v20
	v_fma_f32 v23, -v19, v22, v21
	v_fmac_f32_e32 v22, v23, v20
	v_fma_f32 v19, -v19, v22, v21
	v_div_fmas_f32 v19, v19, v20, v22
	v_div_fixup_f32 v3, v19, v10, v3
	v_div_scale_f32 v19, s[62:63], v10, v10, v2
	v_rcp_f32_e32 v20, v19
	s_nop 0
	v_fma_f32 v21, -v19, v20, 1.0
	v_fmac_f32_e32 v20, v21, v20
	v_div_scale_f32 v21, vcc, v2, v10, v2
	v_mul_f32_e32 v22, v21, v20
	v_fma_f32 v23, -v19, v22, v21
	v_fmac_f32_e32 v22, v23, v20
	v_fma_f32 v19, -v19, v22, v21
	v_div_fmas_f32 v19, v19, v20, v22
	v_div_fixup_f32 v2, v19, v10, v2
	v_cndmask_b32_e64 v2, 0, v2, s[36:37]
	v_cndmask_b32_e64 v2, v2, v3, s[34:35]
	v_cndmask_b32_e64 v2, v2, v4, s[30:31]
	v_cndmask_b32_e64 v2, v2, v5, s[28:29]
	v_cndmask_b32_e64 v2, v2, v6, s[26:27]
	v_cndmask_b32_e64 v2, v2, v7, s[24:25]
	v_cndmask_b32_e64 v2, v2, v8, s[22:23]
	v_cndmask_b32_e64 v2, v2, v11, s[20:21]
	v_cndmask_b32_e64 v2, v2, v15, s[18:19]
	v_cndmask_b32_e64 v2, v2, v17, s[16:17]
	v_cndmask_b32_e64 v2, v2, v18, s[14:15]
	v_cndmask_b32_e64 v2, v2, v16, s[12:13]
	v_cndmask_b32_e64 v2, v2, v14, s[10:11]
	v_cndmask_b32_e64 v2, v2, v13, s[8:9]
	v_cndmask_b32_e64 v2, v2, v12, s[6:7]
	v_cndmask_b32_e64 v4, v2, v9, s[4:5]
	v_lshl_add_u64 v[2:3], s[40:41], 0, v[106:107]
	global_store_dword v[2:3], v4, off
	s_branch .LBB0_1364
